# router phase: top-2 pick fused for both rows of a pass (half-wave per row), plus LDS weight prefetch in router loop
# speedup vs baseline: 1.0096x; 1.0010x over previous
; __global__ void __launch_bounds__(NTHREADS, 2) hybrid_fwd(Args a) {
;     ...
;             for (int v = bid; v < 256; v += G) {
;                 u32x2 raw[2][8];
; #pragma unroll
;                 for (int q = 0; q < 2; ++q)
; #pragma unroll
;                     for (int j = 0; j < 8; ++j) raw[q][j] = __builtin_nontemporal_load((const u32x2*)(YB + (size_t)(v * 32 + wave + 8 * q) * DM + j * 256 + lane * 4));
;                 __syncthreads();
;                 if (tid < 16) hist[tid] = 0;
;                 __syncthreads();
;                 asm volatile("s_waitcnt vmcnt(0)" ::: "memory"); __syncthreads();
.LBB0_887:
	s_add_i32 s6, s22, s51
	s_ashr_i32 s7, s6, 31
	s_add_i32 s8, s6, 8
	s_lshl_b64 s[12:13], s[6:7], 12
	s_ashr_i32 s9, s8, 31
	v_lshl_add_u64 v[16:17], v[26:27], 0, s[12:13]
	s_lshl_b64 s[10:11], s[8:9], 12
	flat_load_dwordx2 v[58:59], v[16:17] nt
	flat_load_dwordx2 v[56:57], v[16:17] offset:512 nt
	flat_load_dwordx2 v[54:55], v[16:17] offset:1024 nt
	flat_load_dwordx2 v[52:53], v[16:17] offset:1536 nt
	flat_load_dwordx2 v[50:51], v[16:17] offset:2048 nt
	flat_load_dwordx2 v[48:49], v[16:17] offset:2560 nt
	flat_load_dwordx2 v[46:47], v[16:17] offset:3072 nt
	flat_load_dwordx2 v[44:45], v[16:17] offset:3584 nt
	v_lshl_add_u64 v[16:17], v[26:27], 0, s[10:11]
	flat_load_dwordx2 v[42:43], v[16:17] nt
	flat_load_dwordx2 v[40:41], v[16:17] offset:512 nt
	flat_load_dwordx2 v[38:39], v[16:17] offset:1024 nt
	flat_load_dwordx2 v[36:37], v[16:17] offset:1536 nt
	flat_load_dwordx2 v[22:23], v[16:17] offset:2048 nt
	flat_load_dwordx2 v[20:21], v[16:17] offset:2560 nt
	flat_load_dwordx2 v[18:19], v[16:17] offset:3072 nt
	s_nop 0
	flat_load_dwordx2 v[16:17], v[16:17] offset:3584 nt
	s_waitcnt vmcnt(0) lgkmcnt(0)
	s_barrier
	s_and_saveexec_b64 s[14:15], s[0:1]
	ds_write_b32 v156, v193
	s_or_b64 exec, exec, s[14:15]
	s_waitcnt lgkmcnt(0)
	s_barrier
	s_waitcnt vmcnt(0)
	s_add_i32 s38, s6, 16
	s_barrier
	s_mov_b64 s[14:15], s[34:35]
	v_lshlrev_b32_e32 v192, 2, v24
	s_mov_b64 s[16:17], s[36:37]
	v_lshl_add_u64 v[94:95], s[14:15], 0, v[192:193]
	v_lshlrev_b32_e32 v66, 16, v58
	v_lshl_add_u64 v[96:97], s[16:17], 0, v[192:193]
	flat_load_dwordx4 v[80:83], v[94:95]
	flat_load_dwordx4 v[86:89], v[96:97]
	v_and_b32_e32 v67, 0xffff0000, v58
	v_lshlrev_b32_e32 v64, 16, v59
	v_and_b32_e32 v65, 0xffff0000, v59
	v_add_f32_e32 v35, v66, v67
	v_add_f32_e32 v58, v64, v65
	v_lshlrev_b32_e32 v74, 16, v56
	v_and_b32_e32 v75, 0xffff0000, v56
	v_lshlrev_b32_e32 v72, 16, v57
	v_and_b32_e32 v73, 0xffff0000, v57
	v_add_f32_e32 v35, v35, v58
	v_add_f32_e32 v56, v74, v75
	v_add_f32_e32 v57, v72, v73
	v_lshlrev_b32_e32 v68, 16, v54
	v_and_b32_e32 v69, 0xffff0000, v54
	v_lshlrev_b32_e32 v70, 16, v55
	v_and_b32_e32 v71, 0xffff0000, v55
	v_add_f32_e32 v35, 0, v35
	v_add_f32_e32 v56, v56, v57
	v_add_f32_e32 v54, v68, v69
	v_add_f32_e32 v55, v70, v71
	v_lshlrev_b32_e32 v60, 16, v52
	v_and_b32_e32 v61, 0xffff0000, v52
	v_lshlrev_b32_e32 v62, 16, v53
	v_and_b32_e32 v63, 0xffff0000, v53
	v_add_f32_e32 v35, v35, v56
	v_add_f32_e32 v54, v54, v55
	v_add_f32_e32 v52, v60, v61
	v_add_f32_e32 v53, v62, v63
	v_add_f32_e32 v35, v35, v54
	v_add_f32_e32 v52, v52, v53
	v_lshlrev_b32_e32 v56, 16, v50
	v_and_b32_e32 v57, 0xffff0000, v50
	v_lshlrev_b32_e32 v58, 16, v51
	v_and_b32_e32 v59, 0xffff0000, v51
	v_add_f32_e32 v35, v35, v52
	v_add_f32_e32 v50, v56, v57
	v_add_f32_e32 v51, v58, v59
	v_lshlrev_b32_e32 v52, 16, v48
	v_and_b32_e32 v53, 0xffff0000, v48
	v_lshlrev_b32_e32 v54, 16, v49
	v_and_b32_e32 v55, 0xffff0000, v49
	v_add_f32_e32 v50, v50, v51
	v_add_f32_e32 v48, v52, v53
	v_add_f32_e32 v49, v54, v55
	v_add_f32_e32 v35, v35, v50
	v_add_f32_e32 v48, v48, v49
	v_add_f32_e32 v35, v35, v48
	v_lshlrev_b32_e32 v48, 16, v46
	v_and_b32_e32 v49, 0xffff0000, v46
	v_lshlrev_b32_e32 v50, 16, v47
	v_and_b32_e32 v51, 0xffff0000, v47
	v_add_f32_e32 v46, v48, v49
	v_add_f32_e32 v47, v50, v51
	v_add_f32_e32 v46, v46, v47
	v_add_f32_e32 v35, v35, v46
	v_lshlrev_b32_e32 v46, 16, v44
	v_and_b32_e32 v47, 0xffff0000, v44
	v_lshlrev_b32_e32 v44, 16, v45
	v_and_b32_e32 v45, 0xffff0000, v45
	v_add_f32_e32 v76, v46, v47
	v_add_f32_e32 v77, v44, v45
	v_add_f32_e32 v76, v76, v77
	v_add_f32_e32 v35, v35, v76
	s_lshl_b64 s[14:15], s[6:7], 11
	s_nop 0
	v_add_f32_dpp v35, v35, v35 quad_perm:[1,0,3,2] row_mask:0xf bank_mask:0xf bound_ctrl:1
	s_nop 1
	v_add_f32_dpp v35, v35, v35 quad_perm:[2,3,0,1] row_mask:0xf bank_mask:0xf bound_ctrl:1
	s_nop 1
	v_add_f32_dpp v35, v35, v35 row_ror:4 row_mask:0xf bank_mask:0xf bound_ctrl:1
	s_nop 1
	v_add_f32_dpp v35, v35, v35 row_ror:8 row_mask:0xf bank_mask:0xf bound_ctrl:1
	v_mov_b32_e32 v76, v35
	s_nop 1
	v_permlane16_swap_b32_e32 v35, v76
	v_add_f32_e32 v35, v35, v76
	v_mov_b32_e32 v76, v35
	s_nop 1
	v_permlane32_swap_b32_e32 v35, v76
	v_add_f32_e32 v35, v35, v76
	v_fmac_f32_e32 v65, 0xba000000, v35
	v_fmac_f32_e32 v67, 0xba000000, v35
	v_fmac_f32_e32 v64, 0xba000000, v35
	v_fmac_f32_e32 v66, 0xba000000, v35
	v_mul_f32_e32 v76, v67, v67
	v_mul_f32_e32 v77, v65, v65
	v_fmac_f32_e32 v76, v66, v66
	v_fmac_f32_e32 v77, v64, v64
	v_fmac_f32_e32 v73, 0xba000000, v35
	v_fmac_f32_e32 v75, 0xba000000, v35
	v_add_f32_e32 v76, v76, v77
	v_fmac_f32_e32 v72, 0xba000000, v35
	v_fmac_f32_e32 v74, 0xba000000, v35
	v_mul_f32_e32 v77, v75, v75
	v_mul_f32_e32 v78, v73, v73
	v_fmac_f32_e32 v77, v74, v74
	v_fmac_f32_e32 v78, v72, v72
	v_add_f32_e32 v77, v77, v78
	v_fmac_f32_e32 v71, 0xba000000, v35
	v_fmac_f32_e32 v69, 0xba000000, v35
	v_add_f32_e32 v76, v76, v77
	v_fmac_f32_e32 v70, 0xba000000, v35
	v_fmac_f32_e32 v68, 0xba000000, v35
	v_mul_f32_e32 v77, v69, v69
	v_mul_f32_e32 v78, v71, v71
	v_fmac_f32_e32 v77, v68, v68
	v_fmac_f32_e32 v78, v70, v70
	v_add_f32_e32 v77, v77, v78
	v_fmac_f32_e32 v63, 0xba000000, v35
	v_fmac_f32_e32 v61, 0xba000000, v35
	v_add_f32_e32 v76, v76, v77
	v_fmac_f32_e32 v62, 0xba000000, v35
	v_fmac_f32_e32 v60, 0xba000000, v35
	v_mul_f32_e32 v77, v61, v61
	v_mul_f32_e32 v78, v63, v63
	v_fmac_f32_e32 v77, v60, v60
	v_fmac_f32_e32 v78, v62, v62
	v_add_f32_e32 v77, v77, v78
	v_fmac_f32_e32 v59, 0xba000000, v35
	v_fmac_f32_e32 v57, 0xba000000, v35
	v_add_f32_e32 v76, v76, v77
	v_fmac_f32_e32 v58, 0xba000000, v35
	v_fmac_f32_e32 v56, 0xba000000, v35
	v_mul_f32_e32 v77, v57, v57
	v_mul_f32_e32 v78, v59, v59
	v_fmac_f32_e32 v77, v56, v56
	v_fmac_f32_e32 v78, v58, v58
	v_add_f32_e32 v77, v77, v78
	v_fmac_f32_e32 v55, 0xba000000, v35
	v_fmac_f32_e32 v53, 0xba000000, v35
	v_add_f32_e32 v76, v76, v77
	v_fmac_f32_e32 v54, 0xba000000, v35
	v_fmac_f32_e32 v52, 0xba000000, v35
	v_mul_f32_e32 v77, v53, v53
	v_mul_f32_e32 v78, v55, v55
	v_fmac_f32_e32 v77, v52, v52
	v_fmac_f32_e32 v78, v54, v54
	v_add_f32_e32 v77, v77, v78
	v_fmac_f32_e32 v51, 0xba000000, v35
	v_fmac_f32_e32 v49, 0xba000000, v35
	v_add_f32_e32 v76, v76, v77
	v_fmac_f32_e32 v50, 0xba000000, v35
	v_fmac_f32_e32 v48, 0xba000000, v35
	v_mul_f32_e32 v77, v49, v49
	v_mul_f32_e32 v78, v51, v51
	v_fmac_f32_e32 v77, v48, v48
	v_fmac_f32_e32 v78, v50, v50
	v_add_f32_e32 v77, v77, v78
	v_fmac_f32_e32 v45, 0xba000000, v35
	v_fmac_f32_e32 v47, 0xba000000, v35
	v_add_f32_e32 v76, v76, v77
	v_fmac_f32_e32 v44, 0xba000000, v35
	v_fmac_f32_e32 v46, 0xba000000, v35
	v_mul_f32_e32 v35, v47, v47
	v_mul_f32_e32 v77, v45, v45
	v_fmac_f32_e32 v35, v46, v46
	v_fmac_f32_e32 v77, v44, v44
	v_add_f32_e32 v35, v35, v77
	v_add_f32_e32 v35, v76, v35
	v_lshl_add_u64 v[78:79], v[30:31], 0, s[14:15]
	s_nop 0
	v_add_f32_dpp v35, v35, v35 quad_perm:[1,0,3,2] row_mask:0xf bank_mask:0xf bound_ctrl:1
	s_nop 1
	v_add_f32_dpp v35, v35, v35 quad_perm:[2,3,0,1] row_mask:0xf bank_mask:0xf bound_ctrl:1
	s_nop 1
	v_add_f32_dpp v35, v35, v35 row_ror:4 row_mask:0xf bank_mask:0xf bound_ctrl:1
	s_nop 1
	v_add_f32_dpp v35, v35, v35 row_ror:8 row_mask:0xf bank_mask:0xf bound_ctrl:1
	v_mov_b32_e32 v76, v35
	s_nop 1
	v_permlane16_swap_b32_e32 v35, v76
	v_add_f32_e32 v35, v35, v76
	v_mov_b32_e32 v76, v35
	s_nop 1
	v_permlane32_swap_b32_e32 v35, v76
	v_add_f32_e32 v35, v35, v76
	v_fmamk_f32 v35, v35, 0x3a000000, v207
	v_rsq_f32_e32 v84, v35
	v_lshl_add_u64 v[76:77], v[28:29], 0, s[12:13]
	v_pk_mul_f32 v[66:67], v[84:85], v[66:67] op_sel_hi:[0,1]
	v_pk_mul_f32 v[90:91], v[84:85], v[64:65] op_sel_hi:[0,1]
	s_waitcnt vmcnt(0) lgkmcnt(0)
	v_pk_fma_f32 v[64:65], v[80:81], v[66:67], v[86:87]
	v_mov_b32_e32 v85, 0
	v_med3_f32 v35, v64, s69, v208
	v_med3_f32 v66, v65, s69, v208
	v_cvt_pk_fp8_f32 v85, v35, v66
	v_pk_fma_f32 v[66:67], v[82:83], v[90:91], v[88:89]
	s_nop 0
	v_med3_f32 v35, v66, s69, v208
	v_med3_f32 v80, v67, s69, v208
	v_cvt_pk_fp8_f32 v85, v35, v80 op_sel:[0,0,1]
	v_cvt_pk_bf16_f32 v80, v64, v65
	v_cvt_pk_bf16_f32 v81, v66, v67
	flat_store_dwordx2 v[76:77], v[80:81] nt
	flat_store_dword v[78:79], v85 nt
	flat_load_dwordx4 v[80:83], v[94:95] offset:1024
	s_nop 0
	flat_load_dwordx4 v[86:89], v[96:97] offset:1024
	v_pk_mul_f32 v[74:75], v[84:85], v[74:75] op_sel_hi:[0,1]
	v_pk_mul_f32 v[90:91], v[84:85], v[72:73] op_sel_hi:[0,1]
	v_mov_b32_e32 v85, 0
	s_waitcnt vmcnt(0) lgkmcnt(0)
	v_pk_fma_f32 v[72:73], v[80:81], v[74:75], v[86:87]
	s_nop 0
	v_med3_f32 v35, v72, s69, v208
	v_med3_f32 v74, v73, s69, v208
	v_cvt_pk_fp8_f32 v85, v35, v74
	v_pk_fma_f32 v[74:75], v[82:83], v[90:91], v[88:89]
	s_nop 0
	v_med3_f32 v35, v74, s69, v208
	v_med3_f32 v80, v75, s69, v208
	v_cvt_pk_fp8_f32 v85, v35, v80 op_sel:[0,0,1]
	v_cvt_pk_bf16_f32 v80, v72, v73
	v_cvt_pk_bf16_f32 v81, v74, v75
	flat_store_dwordx2 v[76:77], v[80:81] offset:512 nt
	flat_store_dword v[78:79], v85 offset:256 nt
	flat_load_dwordx4 v[86:89], v[94:95] offset:2048
	flat_load_dwordx4 v[90:93], v[96:97] offset:2048
	v_pk_mul_f32 v[68:69], v[84:85], v[68:69] op_sel_hi:[0,1]
	v_mov_b32_e32 v35, 0
	v_pk_mul_f32 v[70:71], v[84:85], v[70:71] op_sel_hi:[0,1]
	v_pk_mul_f32 v[60:61], v[84:85], v[60:61] op_sel_hi:[0,1]
	v_pk_mul_f32 v[62:63], v[84:85], v[62:63] op_sel_hi:[0,1]
	v_pk_mul_f32 v[56:57], v[84:85], v[56:57] op_sel_hi:[0,1]
	v_pk_mul_f32 v[58:59], v[84:85], v[58:59] op_sel_hi:[0,1]
	v_pk_mul_f32 v[52:53], v[84:85], v[52:53] op_sel_hi:[0,1]
	v_pk_mul_f32 v[54:55], v[84:85], v[54:55] op_sel_hi:[0,1]
	v_pk_mul_f32 v[48:49], v[84:85], v[48:49] op_sel_hi:[0,1]
	v_pk_mul_f32 v[50:51], v[84:85], v[50:51] op_sel_hi:[0,1]
	v_pk_mul_f32 v[46:47], v[84:85], v[46:47] op_sel_hi:[0,1]
	v_pk_mul_f32 v[44:45], v[84:85], v[44:45] op_sel_hi:[0,1]
	s_waitcnt vmcnt(0) lgkmcnt(0)
	v_pk_fma_f32 v[82:83], v[86:87], v[68:69], v[90:91]
	s_nop 0
	v_med3_f32 v68, v82, s69, v208
	v_med3_f32 v69, v83, s69, v208
	v_cvt_pk_fp8_f32 v35, v68, v69
	v_pk_fma_f32 v[80:81], v[88:89], v[70:71], v[92:93]
	v_add_co_u32_e32 v90, vcc, s33, v94
	v_med3_f32 v68, v80, s69, v208
	v_med3_f32 v69, v81, s69, v208
	v_cvt_pk_fp8_f32 v35, v68, v69 op_sel:[0,0,1]
	v_cvt_pk_bf16_f32 v68, v82, v83
	v_cvt_pk_bf16_f32 v69, v80, v81
	flat_store_dwordx2 v[76:77], v[68:69] offset:1024 nt
	flat_store_dword v[78:79], v35 offset:512 nt
	flat_load_dwordx4 v[68:71], v[94:95] offset:3072
	s_nop 0
	flat_load_dwordx4 v[86:89], v[96:97] offset:3072
	v_addc_co_u32_e32 v91, vcc, 0, v95, vcc
	v_mov_b32_e32 v35, 0
	v_add_co_u32_e32 v96, vcc, s33, v96
	s_waitcnt vmcnt(0) lgkmcnt(0)
	v_pk_fma_f32 v[94:95], v[68:69], v[60:61], v[86:87]
	s_nop 0
	v_med3_f32 v60, v94, s69, v208
	v_med3_f32 v61, v95, s69, v208
	v_cvt_pk_fp8_f32 v35, v60, v61
	v_pk_fma_f32 v[92:93], v[70:71], v[62:63], v[88:89]
	v_addc_co_u32_e32 v97, vcc, 0, v97, vcc
	v_med3_f32 v60, v92, s69, v208
	v_med3_f32 v61, v93, s69, v208
	v_cvt_pk_fp8_f32 v35, v60, v61 op_sel:[0,0,1]
	v_cvt_pk_bf16_f32 v60, v94, v95
	v_cvt_pk_bf16_f32 v61, v92, v93
	flat_store_dwordx2 v[76:77], v[60:61] offset:1536 nt
	flat_store_dword v[78:79], v35 offset:768 nt
	flat_load_dwordx4 v[60:63], v[90:91]
	s_nop 0
	flat_load_dwordx4 v[68:71], v[96:97]
	v_mov_b32_e32 v35, 0
	s_waitcnt vmcnt(0) lgkmcnt(0)
	v_pk_fma_f32 v[114:115], v[60:61], v[56:57], v[68:69]
	s_nop 0
	v_med3_f32 v56, v114, s69, v208
	v_med3_f32 v57, v115, s69, v208
	v_cvt_pk_fp8_f32 v35, v56, v57
	v_pk_fma_f32 v[112:113], v[62:63], v[58:59], v[70:71]
	s_nop 0
	v_med3_f32 v56, v112, s69, v208
	v_med3_f32 v57, v113, s69, v208
	v_cvt_pk_fp8_f32 v35, v56, v57 op_sel:[0,0,1]
	v_cvt_pk_bf16_f32 v56, v114, v115
	v_cvt_pk_bf16_f32 v57, v112, v113
	flat_store_dwordx2 v[76:77], v[56:57] offset:2048 nt
	flat_store_dword v[78:79], v35 offset:1024 nt
	flat_load_dwordx4 v[56:59], v[90:91] offset:1024
	s_nop 0
	flat_load_dwordx4 v[60:63], v[96:97] offset:1024
	v_mov_b32_e32 v35, 0
	s_waitcnt vmcnt(0) lgkmcnt(0)
	v_pk_fma_f32 v[118:119], v[56:57], v[52:53], v[60:61]
	s_nop 0
	v_med3_f32 v52, v118, s69, v208
	v_med3_f32 v53, v119, s69, v208
	v_cvt_pk_fp8_f32 v35, v52, v53
	v_pk_fma_f32 v[116:117], v[58:59], v[54:55], v[62:63]
	s_nop 0
	v_med3_f32 v52, v116, s69, v208
	v_med3_f32 v53, v117, s69, v208
	v_cvt_pk_fp8_f32 v35, v52, v53 op_sel:[0,0,1]
	v_cvt_pk_bf16_f32 v52, v118, v119
	v_cvt_pk_bf16_f32 v53, v116, v117
	flat_store_dwordx2 v[76:77], v[52:53] offset:2560 nt
	flat_store_dword v[78:79], v35 offset:1280 nt
	flat_load_dwordx4 v[52:55], v[90:91] offset:2048
	s_nop 0
	flat_load_dwordx4 v[56:59], v[96:97] offset:2048
	v_mov_b32_e32 v35, 0
	s_waitcnt vmcnt(0) lgkmcnt(0)
	v_pk_fma_f32 v[122:123], v[52:53], v[48:49], v[56:57]
	s_nop 0
	v_med3_f32 v48, v122, s69, v208
	v_med3_f32 v49, v123, s69, v208
	v_cvt_pk_fp8_f32 v35, v48, v49
	v_pk_fma_f32 v[120:121], v[54:55], v[50:51], v[58:59]
	s_nop 0
	v_med3_f32 v48, v120, s69, v208
	v_med3_f32 v49, v121, s69, v208
	v_cvt_pk_fp8_f32 v35, v48, v49 op_sel:[0,0,1]
	v_cvt_pk_bf16_f32 v48, v122, v123
	v_cvt_pk_bf16_f32 v49, v120, v121
	flat_store_dwordx2 v[76:77], v[48:49] offset:3072 nt
	flat_store_dword v[78:79], v35 offset:1536 nt
	flat_load_dwordx4 v[48:51], v[90:91] offset:3072
	s_nop 0
	flat_load_dwordx4 v[52:55], v[96:97] offset:3072
	v_mov_b32_e32 v35, 0
	s_waitcnt vmcnt(0) lgkmcnt(0)
	v_pk_fma_f32 v[124:125], v[48:49], v[46:47], v[52:53]
	s_nop 0
	v_med3_f32 v46, v124, s69, v208
	v_med3_f32 v47, v125, s69, v208
	v_mov_b32_e32 v48, 0
	v_cvt_pk_fp8_f32 v48, v46, v47
	v_pk_fma_f32 v[126:127], v[50:51], v[44:45], v[54:55]
	s_nop 0
	v_med3_f32 v44, v126, s69, v208
	v_med3_f32 v45, v127, s69, v208
	v_cvt_pk_fp8_f32 v48, v44, v45 op_sel:[0,0,1]
	v_cvt_pk_bf16_f32 v44, v124, v125
	v_cvt_pk_bf16_f32 v45, v126, v127
	flat_store_dwordx2 v[76:77], v[44:45] offset:3584 nt
	flat_store_dword v[78:79], v48 offset:1792 nt
	v_lshlrev_b32_e32 v84, 16, v42
	v_and_b32_e32 v85, 0xffff0000, v42
	v_lshlrev_b32_e32 v78, 16, v43
	v_and_b32_e32 v79, 0xffff0000, v43
	v_add_f32_e32 v42, v84, v85
	v_add_f32_e32 v43, v78, v79
	v_lshlrev_b32_e32 v76, 16, v40
	v_and_b32_e32 v77, 0xffff0000, v40
	v_lshlrev_b32_e32 v70, 16, v41
	v_and_b32_e32 v71, 0xffff0000, v41
	v_add_f32_e32 v42, v42, v43
	v_add_f32_e32 v40, v76, v77
	v_add_f32_e32 v41, v70, v71
	v_lshlrev_b32_e32 v62, 16, v38
	v_and_b32_e32 v63, 0xffff0000, v38
	v_lshlrev_b32_e32 v68, 16, v39
	v_and_b32_e32 v69, 0xffff0000, v39
	v_add_f32_e32 v42, 0, v42
	v_add_f32_e32 v40, v40, v41
	v_add_f32_e32 v38, v62, v63
	v_add_f32_e32 v39, v68, v69
	v_lshlrev_b32_e32 v58, 16, v36
	v_and_b32_e32 v59, 0xffff0000, v36
	v_lshlrev_b32_e32 v60, 16, v37
	v_and_b32_e32 v61, 0xffff0000, v37
	v_add_f32_e32 v40, v42, v40
	v_add_f32_e32 v38, v38, v39
	v_add_f32_e32 v36, v58, v59
	v_add_f32_e32 v37, v60, v61
	v_lshlrev_b32_e32 v50, 16, v22
	v_and_b32_e32 v51, 0xffff0000, v22
	v_lshlrev_b32_e32 v52, 16, v23
	v_and_b32_e32 v53, 0xffff0000, v23
	v_add_f32_e32 v38, v40, v38
	v_add_f32_e32 v36, v36, v37
	v_add_f32_e32 v22, v50, v51
	v_add_f32_e32 v23, v52, v53
	v_lshlrev_b32_e32 v46, 16, v20
	v_and_b32_e32 v47, 0xffff0000, v20
	v_lshlrev_b32_e32 v48, 16, v21
	v_and_b32_e32 v49, 0xffff0000, v21
	v_add_f32_e32 v36, v38, v36
	v_add_f32_e32 v22, v22, v23
	v_add_f32_e32 v20, v46, v47
	v_add_f32_e32 v21, v48, v49
	v_lshlrev_b32_e32 v40, 16, v18
	v_and_b32_e32 v41, 0xffff0000, v18
	v_lshlrev_b32_e32 v42, 16, v19
	v_and_b32_e32 v43, 0xffff0000, v19
	v_add_f32_e32 v22, v36, v22
	v_add_f32_e32 v20, v20, v21
	v_add_f32_e32 v18, v40, v41
	v_add_f32_e32 v19, v42, v43
	v_lshlrev_b32_e32 v38, 16, v16
	v_and_b32_e32 v39, 0xffff0000, v16
	v_lshlrev_b32_e32 v36, 16, v17
	v_and_b32_e32 v37, 0xffff0000, v17
	v_add_f32_e32 v20, v22, v20
	v_add_f32_e32 v18, v18, v19
	v_add_f32_e32 v16, v38, v39
	v_add_f32_e32 v17, v36, v37
	v_add_f32_e32 v18, v20, v18
	v_add_f32_e32 v16, v16, v17
	v_add_f32_e32 v16, v18, v16
	s_mov_b64 s[12:13], s[34:35]
	s_mov_b64 s[14:15], s[36:37]
	v_add_f32_dpp v16, v16, v16 quad_perm:[1,0,3,2] row_mask:0xf bank_mask:0xf bound_ctrl:1
	v_lshl_add_u64 v[100:101], s[12:13], 0, v[192:193]
	v_lshl_add_u64 v[56:57], v[28:29], 0, s[10:11]
	v_add_f32_dpp v16, v16, v16 quad_perm:[2,3,0,1] row_mask:0xf bank_mask:0xf bound_ctrl:1
	v_lshl_add_u64 v[86:87], s[14:15], 0, v[192:193]
	s_lshl_b64 s[8:9], s[8:9], 11
	v_add_f32_dpp v16, v16, v16 row_ror:4 row_mask:0xf bank_mask:0xf bound_ctrl:1
	v_lshl_add_u64 v[54:55], v[30:31], 0, s[8:9]
	s_nop 0
	v_add_f32_dpp v16, v16, v16 row_ror:8 row_mask:0xf bank_mask:0xf bound_ctrl:1
	v_mov_b32_e32 v17, v16
	s_nop 1
	v_permlane16_swap_b32_e32 v16, v17
	v_add_f32_e32 v16, v16, v17
	v_mov_b32_e32 v17, v16
	s_nop 1
	v_permlane32_swap_b32_e32 v16, v17
	v_add_f32_e32 v16, v16, v17
	v_fmac_f32_e32 v79, 0xba000000, v16
	v_fmac_f32_e32 v85, 0xba000000, v16
	v_fmac_f32_e32 v78, 0xba000000, v16
	v_fmac_f32_e32 v84, 0xba000000, v16
	v_mul_f32_e32 v17, v85, v85
	v_mul_f32_e32 v18, v79, v79
	v_fmac_f32_e32 v17, v84, v84
	v_fmac_f32_e32 v18, v78, v78
	v_fmac_f32_e32 v71, 0xba000000, v16
	v_fmac_f32_e32 v77, 0xba000000, v16
	v_add_f32_e32 v17, v17, v18
	v_fmac_f32_e32 v70, 0xba000000, v16
	v_fmac_f32_e32 v76, 0xba000000, v16
	v_mul_f32_e32 v18, v77, v77
	v_mul_f32_e32 v19, v71, v71
	v_fmac_f32_e32 v18, v76, v76
	v_fmac_f32_e32 v19, v70, v70
	v_add_f32_e32 v18, v18, v19
	v_fmac_f32_e32 v69, 0xba000000, v16
	v_fmac_f32_e32 v63, 0xba000000, v16
	v_add_f32_e32 v17, v17, v18
	v_fmac_f32_e32 v68, 0xba000000, v16
	v_fmac_f32_e32 v62, 0xba000000, v16
	v_mul_f32_e32 v18, v63, v63
	v_mul_f32_e32 v19, v69, v69
	v_fmac_f32_e32 v18, v62, v62
	v_fmac_f32_e32 v19, v68, v68
	v_add_f32_e32 v18, v18, v19
	v_fmac_f32_e32 v61, 0xba000000, v16
	v_fmac_f32_e32 v59, 0xba000000, v16
	v_add_f32_e32 v17, v17, v18
	v_fmac_f32_e32 v60, 0xba000000, v16
	v_fmac_f32_e32 v58, 0xba000000, v16
	v_mul_f32_e32 v18, v59, v59
	v_mul_f32_e32 v19, v61, v61
	v_fmac_f32_e32 v18, v58, v58
	v_fmac_f32_e32 v19, v60, v60
	v_add_f32_e32 v18, v18, v19
	v_fmac_f32_e32 v53, 0xba000000, v16
	v_fmac_f32_e32 v51, 0xba000000, v16
	v_add_f32_e32 v17, v17, v18
	v_fmac_f32_e32 v52, 0xba000000, v16
	v_fmac_f32_e32 v50, 0xba000000, v16
	v_mul_f32_e32 v18, v51, v51
	v_mul_f32_e32 v19, v53, v53
	v_fmac_f32_e32 v18, v50, v50
	v_fmac_f32_e32 v19, v52, v52
	v_add_f32_e32 v18, v18, v19
	v_fmac_f32_e32 v49, 0xba000000, v16
	v_fmac_f32_e32 v47, 0xba000000, v16
	v_add_f32_e32 v17, v17, v18
	v_fmac_f32_e32 v48, 0xba000000, v16
	v_fmac_f32_e32 v46, 0xba000000, v16
	v_mul_f32_e32 v18, v47, v47
	v_mul_f32_e32 v19, v49, v49
	v_fmac_f32_e32 v18, v46, v46
	v_fmac_f32_e32 v19, v48, v48
	v_add_f32_e32 v18, v18, v19
	v_fmac_f32_e32 v43, 0xba000000, v16
	v_fmac_f32_e32 v41, 0xba000000, v16
	v_add_f32_e32 v17, v17, v18
	v_fmac_f32_e32 v42, 0xba000000, v16
	v_fmac_f32_e32 v40, 0xba000000, v16
	v_mul_f32_e32 v18, v41, v41
	v_mul_f32_e32 v19, v43, v43
	v_fmac_f32_e32 v18, v40, v40
	v_fmac_f32_e32 v19, v42, v42
	v_add_f32_e32 v18, v18, v19
	v_fmac_f32_e32 v37, 0xba000000, v16
	v_fmac_f32_e32 v39, 0xba000000, v16
	v_add_f32_e32 v17, v17, v18
	v_fmac_f32_e32 v36, 0xba000000, v16
	v_fmac_f32_e32 v38, 0xba000000, v16
	v_mul_f32_e32 v16, v39, v39
	v_mul_f32_e32 v18, v37, v37
	v_fmac_f32_e32 v16, v38, v38
	v_fmac_f32_e32 v18, v36, v36
	v_add_f32_e32 v16, v16, v18
	v_add_f32_e32 v16, v17, v16
	s_nop 1
	v_add_f32_dpp v16, v16, v16 quad_perm:[1,0,3,2] row_mask:0xf bank_mask:0xf bound_ctrl:1
	s_nop 1
	v_add_f32_dpp v16, v16, v16 quad_perm:[2,3,0,1] row_mask:0xf bank_mask:0xf bound_ctrl:1
	s_nop 1
	v_add_f32_dpp v16, v16, v16 row_ror:4 row_mask:0xf bank_mask:0xf bound_ctrl:1
	s_nop 1
	v_add_f32_dpp v16, v16, v16 row_ror:8 row_mask:0xf bank_mask:0xf bound_ctrl:1
	v_mov_b32_e32 v17, v16
	s_nop 1
	v_permlane16_swap_b32_e32 v16, v17
	v_add_f32_e32 v16, v16, v17
	v_mov_b32_e32 v17, v16
	s_nop 1
	v_permlane32_swap_b32_e32 v16, v17
	v_add_f32_e32 v16, v16, v17
	v_fmamk_f32 v16, v16, 0x3a000000, v207
	v_rsq_f32_e32 v44, v16
	flat_load_dwordx4 v[16:19], v[100:101]
	flat_load_dwordx4 v[20:23], v[86:87]
	v_pk_mul_f32 v[84:85], v[44:45], v[84:85] op_sel_hi:[0,1]
	v_pk_mul_f32 v[78:79], v[44:45], v[78:79] op_sel_hi:[0,1]
	v_pk_mul_f32 v[76:77], v[44:45], v[76:77] op_sel_hi:[0,1]
	v_pk_mul_f32 v[70:71], v[44:45], v[70:71] op_sel_hi:[0,1]
	v_pk_mul_f32 v[62:63], v[44:45], v[62:63] op_sel_hi:[0,1]
	v_pk_mul_f32 v[68:69], v[44:45], v[68:69] op_sel_hi:[0,1]
	v_pk_mul_f32 v[58:59], v[44:45], v[58:59] op_sel_hi:[0,1]
	v_pk_mul_f32 v[60:61], v[44:45], v[60:61] op_sel_hi:[0,1]
	v_pk_mul_f32 v[50:51], v[44:45], v[50:51] op_sel_hi:[0,1]
	v_pk_mul_f32 v[52:53], v[44:45], v[52:53] op_sel_hi:[0,1]
	v_mov_b32_e32 v45, 0
	s_waitcnt vmcnt(0) lgkmcnt(0)
	v_pk_fma_f32 v[128:129], v[18:19], v[78:79], v[22:23]
	v_pk_fma_f32 v[130:131], v[16:17], v[84:85], v[20:21]
	v_mov_b32_e32 v20, 0
	v_cvt_pk_bf16_f32 v16, v130, v131
	v_cvt_pk_bf16_f32 v17, v128, v129
	flat_store_dwordx2 v[56:57], v[16:17] nt
	v_med3_f32 v16, v130, s69, v208
	v_med3_f32 v17, v131, s69, v208
	v_cvt_pk_fp8_f32 v20, v16, v17
	v_med3_f32 v18, v128, s69, v208
	v_med3_f32 v19, v129, s69, v208
	v_cvt_pk_fp8_f32 v20, v18, v19 op_sel:[0,0,1]
	flat_store_dword v[54:55], v20 nt
	flat_load_dwordx4 v[16:19], v[100:101] offset:1024
	s_nop 0
	flat_load_dwordx4 v[20:23], v[86:87] offset:1024
	s_waitcnt vmcnt(0) lgkmcnt(0)
	v_pk_fma_f32 v[104:105], v[18:19], v[70:71], v[22:23]
	v_pk_fma_f32 v[106:107], v[16:17], v[76:77], v[20:21]
	v_mov_b32_e32 v20, 0
	v_cvt_pk_bf16_f32 v16, v106, v107
	v_cvt_pk_bf16_f32 v17, v104, v105
	flat_store_dwordx2 v[56:57], v[16:17] offset:512 nt
	v_med3_f32 v16, v106, s69, v208
	v_med3_f32 v17, v107, s69, v208
	v_cvt_pk_fp8_f32 v20, v16, v17
	v_med3_f32 v18, v104, s69, v208
	v_med3_f32 v19, v105, s69, v208
	v_cvt_pk_fp8_f32 v20, v18, v19 op_sel:[0,0,1]
	flat_store_dword v[54:55], v20 offset:256 nt
	flat_load_dwordx4 v[16:19], v[100:101] offset:2048
	s_nop 0
	flat_load_dwordx4 v[20:23], v[86:87] offset:2048
	s_waitcnt vmcnt(0) lgkmcnt(0)
	v_pk_fma_f32 v[96:97], v[18:19], v[68:69], v[22:23]
	v_pk_fma_f32 v[98:99], v[16:17], v[62:63], v[20:21]
	v_mov_b32_e32 v20, 0
	v_cvt_pk_bf16_f32 v16, v98, v99
	v_cvt_pk_bf16_f32 v17, v96, v97
	flat_store_dwordx2 v[56:57], v[16:17] offset:1024 nt
	v_med3_f32 v16, v98, s69, v208
	v_med3_f32 v17, v99, s69, v208
	v_cvt_pk_fp8_f32 v20, v16, v17
	v_med3_f32 v18, v96, s69, v208
	v_med3_f32 v19, v97, s69, v208
	v_cvt_pk_fp8_f32 v20, v18, v19 op_sel:[0,0,1]
	flat_store_dword v[54:55], v20 offset:512 nt
	flat_load_dwordx4 v[16:19], v[100:101] offset:3072
	s_nop 0
	flat_load_dwordx4 v[20:23], v[86:87] offset:3072
	s_waitcnt vmcnt(0) lgkmcnt(0)
; #define LAS __attribute__((address_space(3)))
; __global__ void __launch_bounds__(NTHREADS, 2) hybrid_fwd(Args a) {
;     ...
;                     if (qp == 0) {
; #pragma unroll
;                         for (int q = 0; q < 2; ++q)
; #pragma unroll
;                             for (int j = 0; j < 8; ++j) raw[q][j] = __builtin_nontemporal_load((const u32x2*)(YB + (size_t)(v * 32 + wave + 8 * (2 + q)) * DM + j * 256 + lane * 4));
;                         __builtin_amdgcn_sched_barrier(0);
;                     }
;                     f32x2 y2[8][4];
; #pragma unroll
;                     for (int j = 0; j < 8; ++j)
; #pragma unroll
;                         for (int c = 0; c < 4; ++c) y2[j][c] = (f32x2){ya[j][c], yb[j][c]};
;                     f32x2 acc2[16];
; #pragma unroll
;                     for (int e = 0; e < 16; ++e) acc2[e] = (f32x2){0.f, 0.f};
; #pragma unroll
;                     for (int j = 0; j < 8; ++j) {
; #pragma unroll
;                         for (int e = 0; e < 16; ++e) { const f32x4 w = *(const LAS f32x4*)(rwT + e * 2052 + j * 256 + lane * 4);
;                             acc2[e] += y2[j][0] * (f32x2){w[0], w[0]}; acc2[e] += y2[j][1] * (f32x2){w[1], w[1]};
;                             acc2[e] += y2[j][2] * (f32x2){w[2], w[2]}; acc2[e] += y2[j][3] * (f32x2){w[3], w[3]}; }
	v_pk_fma_f32 v[88:89], v[18:19], v[60:61], v[22:23]
	v_pk_fma_f32 v[90:91], v[16:17], v[58:59], v[20:21]
	v_mov_b32_e32 v20, 0
	v_cvt_pk_bf16_f32 v16, v90, v91
	v_cvt_pk_bf16_f32 v17, v88, v89
	flat_store_dwordx2 v[56:57], v[16:17] offset:1536 nt
	v_med3_f32 v16, v90, s69, v208
	v_med3_f32 v17, v91, s69, v208
	v_cvt_pk_fp8_f32 v20, v16, v17
	v_med3_f32 v18, v88, s69, v208
	v_med3_f32 v19, v89, s69, v208
	v_add_co_u32_e32 v16, vcc, s33, v100
	v_cvt_pk_fp8_f32 v20, v18, v19 op_sel:[0,0,1]
	s_nop 0
	v_addc_co_u32_e32 v17, vcc, 0, v101, vcc
	v_add_co_u32_e32 v18, vcc, s33, v86
	flat_store_dword v[54:55], v20 offset:768 nt
	s_nop 0
	v_addc_co_u32_e32 v19, vcc, 0, v87, vcc
	flat_load_dwordx4 v[20:23], v[16:17]
	flat_load_dwordx4 v[58:61], v[18:19]
	s_waitcnt vmcnt(0) lgkmcnt(0)
	v_pk_fma_f32 v[84:85], v[22:23], v[52:53], v[60:61]
	v_pk_fma_f32 v[86:87], v[20:21], v[50:51], v[58:59]
	v_med3_f32 v22, v84, s69, v208
	v_cvt_pk_bf16_f32 v20, v86, v87
	v_cvt_pk_bf16_f32 v21, v84, v85
	flat_store_dwordx2 v[56:57], v[20:21] offset:2048 nt
	v_med3_f32 v20, v86, s69, v208
	v_med3_f32 v21, v87, s69, v208
	v_cvt_pk_fp8_f32 v45, v20, v21
	v_med3_f32 v23, v85, s69, v208
	v_cvt_pk_fp8_f32 v45, v22, v23 op_sel:[0,0,1]
	flat_store_dword v[54:55], v45 offset:1024 nt
	flat_load_dwordx4 v[20:23], v[16:17] offset:1024
	flat_load_dwordx4 v[50:53], v[18:19] offset:1024
	v_pk_mul_f32 v[46:47], v[44:45], v[46:47] op_sel_hi:[0,1]
	v_pk_mul_f32 v[48:49], v[44:45], v[48:49] op_sel_hi:[0,1]
	v_mov_b32_e32 v45, 0
	s_waitcnt vmcnt(0) lgkmcnt(0)
	v_pk_fma_f32 v[76:77], v[22:23], v[48:49], v[52:53]
	v_pk_fma_f32 v[78:79], v[20:21], v[46:47], v[50:51]
	v_med3_f32 v22, v76, s69, v208
	v_cvt_pk_bf16_f32 v20, v78, v79
	v_cvt_pk_bf16_f32 v21, v76, v77
	flat_store_dwordx2 v[56:57], v[20:21] offset:2560 nt
	v_med3_f32 v20, v78, s69, v208
	v_med3_f32 v21, v79, s69, v208
	v_cvt_pk_fp8_f32 v45, v20, v21
	v_med3_f32 v23, v77, s69, v208
	v_cvt_pk_fp8_f32 v45, v22, v23 op_sel:[0,0,1]
	flat_store_dword v[54:55], v45 offset:1280 nt
	flat_load_dwordx4 v[20:23], v[16:17] offset:2048
	flat_load_dwordx4 v[46:49], v[18:19] offset:2048
	v_pk_mul_f32 v[40:41], v[44:45], v[40:41] op_sel_hi:[0,1]
	v_pk_mul_f32 v[42:43], v[44:45], v[42:43] op_sel_hi:[0,1]
	v_pk_mul_f32 v[38:39], v[44:45], v[38:39] op_sel_hi:[0,1]
	v_pk_mul_f32 v[36:37], v[44:45], v[36:37] op_sel_hi:[0,1]
	s_waitcnt vmcnt(0) lgkmcnt(0)
	v_pk_fma_f32 v[68:69], v[22:23], v[42:43], v[48:49]
	v_pk_fma_f32 v[70:71], v[20:21], v[40:41], v[46:47]
	v_mov_b32_e32 v40, 0
	v_cvt_pk_bf16_f32 v20, v70, v71
	v_cvt_pk_bf16_f32 v21, v68, v69
	flat_store_dwordx2 v[56:57], v[20:21] offset:3072 nt
	v_med3_f32 v20, v70, s69, v208
	v_med3_f32 v21, v71, s69, v208
	v_cvt_pk_fp8_f32 v40, v20, v21
	v_med3_f32 v22, v68, s69, v208
	v_med3_f32 v23, v69, s69, v208
	v_cvt_pk_fp8_f32 v40, v22, v23 op_sel:[0,0,1]
	flat_store_dword v[54:55], v40 offset:1536 nt
	flat_load_dwordx4 v[20:23], v[16:17] offset:3072
	s_nop 0
	flat_load_dwordx4 v[16:19], v[18:19] offset:3072
	s_waitcnt vmcnt(0) lgkmcnt(0)
	v_pk_fma_f32 v[60:61], v[22:23], v[36:37], v[18:19]
	v_pk_fma_f32 v[62:63], v[20:21], v[38:39], v[16:17]
	v_mov_b32_e32 v20, 0
	v_cvt_pk_bf16_f32 v16, v62, v63
	v_cvt_pk_bf16_f32 v17, v60, v61
	flat_store_dwordx2 v[56:57], v[16:17] offset:3584 nt
	v_med3_f32 v16, v62, s69, v208
	v_med3_f32 v17, v63, s69, v208
	v_cvt_pk_fp8_f32 v20, v16, v17
	v_med3_f32 v18, v60, s69, v208
	v_med3_f32 v19, v61, s69, v208
	v_cvt_pk_fp8_f32 v20, v18, v19 op_sel:[0,0,1]
	flat_store_dword v[54:55], v20 offset:1792 nt
	s_ashr_i32 s39, s38, 31
	s_add_i32 s40, s6, 24
	s_lshl_b64 s[44:45], s[38:39], 12
	s_ashr_i32 s41, s40, 31
	v_lshl_add_u64 v[16:17], v[26:27], 0, s[44:45]
	s_lshl_b64 s[42:43], s[40:41], 12
	flat_load_dwordx2 v[58:59], v[16:17] nt
	flat_load_dwordx2 v[56:57], v[16:17] offset:512 nt
	flat_load_dwordx2 v[54:55], v[16:17] offset:1024 nt
	flat_load_dwordx2 v[52:53], v[16:17] offset:1536 nt
	flat_load_dwordx2 v[50:51], v[16:17] offset:2048 nt
	flat_load_dwordx2 v[48:49], v[16:17] offset:2560 nt
	flat_load_dwordx2 v[46:47], v[16:17] offset:3072 nt
	flat_load_dwordx2 v[44:45], v[16:17] offset:3584 nt
	v_lshl_add_u64 v[16:17], v[26:27], 0, s[42:43]
	flat_load_dwordx2 v[42:43], v[16:17] nt
	flat_load_dwordx2 v[40:41], v[16:17] offset:512 nt
	flat_load_dwordx2 v[38:39], v[16:17] offset:1024 nt
	flat_load_dwordx2 v[36:37], v[16:17] offset:1536 nt
	flat_load_dwordx2 v[22:23], v[16:17] offset:2048 nt
	flat_load_dwordx2 v[20:21], v[16:17] offset:2560 nt
	flat_load_dwordx2 v[18:19], v[16:17] offset:3072 nt
	s_nop 0
	flat_load_dwordx2 v[16:17], v[16:17] offset:3584 nt
	v_add_u32_e32 v238, 0x10000, v25
	ds_read_b128 v[158:161], v25 offset:0
	ds_read_b128 v[162:165], v25 offset:8208
	ds_read_b128 v[166:169], v25 offset:16416
	ds_read_b128 v[170:173], v25 offset:24624
	ds_read_b128 v[174:177], v25 offset:32832
	ds_read_b128 v[178:181], v25 offset:41040
	ds_read_b128 v[182:185], v25 offset:49248
	ds_read_b128 v[186:189], v25 offset:57456
	v_mov_b32_e32 v100, v94
	v_mov_b32_e32 v101, v90
	v_mov_b32_e32 v90, v95
	v_mov_b32_e32 v102, v92
	v_mov_b32_e32 v103, v88
	v_mov_b32_e32 v88, v93
	v_mov_b32_e32 v92, v114
	v_mov_b32_e32 v93, v86
	v_mov_b32_e32 v86, v115
	v_mov_b32_e32 v94, v112
	v_mov_b32_e32 v95, v84
	v_mov_b32_e32 v84, v113
	ds_read_b128 v[198:201], v238 offset:128
	v_mov_b32_e32 v136, v64
	v_mov_b32_e32 v137, v130
	v_mov_b32_e32 v130, v65
	v_mov_b32_e32 v108, v82
	v_mov_b32_e32 v109, v98
	v_mov_b32_e32 v98, v83
	v_mov_b32_e32 v82, v116
	v_mov_b32_e32 v83, v76
	v_mov_b32_e32 v76, v117
	s_waitcnt lgkmcnt(8)
; #define LAS __attribute__((address_space(3)))
; __global__ void __launch_bounds__(NTHREADS, 2) hybrid_fwd(Args a) {
;     ...
;                     for (int j = 0; j < 8; ++j) {
; #pragma unroll
;                         for (int e = 0; e < 16; ++e) { const f32x4 w = *(const LAS f32x4*)(rwT + e * 2052 + j * 256 + lane * 4);
;                             acc2[e] += y2[j][0] * (f32x2){w[0], w[0]}; acc2[e] += y2[j][1] * (f32x2){w[1], w[1]};
;                             acc2[e] += y2[j][2] * (f32x2){w[2], w[2]}; acc2[e] += y2[j][3] * (f32x2){w[3], w[3]}; }
;                         __builtin_amdgcn_sched_barrier(0);
	v_pk_fma_f32 v[116:117], v[136:137], v[158:159], 0 op_sel_hi:[1,0,0]
	v_mov_b32_e32 v138, v66
	v_mov_b32_e32 v139, v128
	v_pk_fma_f32 v[112:113], v[158:159], v[130:131], v[116:117] op_sel:[1,0,0]
	v_mov_b32_e32 v128, v67
	v_pk_fma_f32 v[112:113], v[160:161], v[138:139], v[112:113] op_sel_hi:[0,1,1]
	v_mov_b32_e32 v114, v161
	v_pk_fma_f32 v[112:113], v[114:115], v[128:129], v[112:113] op_sel_hi:[0,1,1]
	ds_read_b128 v[202:205], v238 offset:8336
	v_mov_b32_e32 v110, v80
	v_mov_b32_e32 v111, v96
	v_mov_b32_e32 v96, v81
	v_mov_b32_e32 v80, v118
	v_mov_b32_e32 v81, v78
	v_mov_b32_e32 v78, v119
	s_waitcnt lgkmcnt(8)
	v_pk_fma_f32 v[118:119], v[136:137], v[162:163], 0 op_sel_hi:[1,0,0]
	v_mov_b32_e32 v134, v74
	v_pk_fma_f32 v[114:115], v[162:163], v[130:131], v[118:119] op_sel:[1,0,0]
	v_mov_b32_e32 v135, v104
	v_pk_fma_f32 v[114:115], v[164:165], v[138:139], v[114:115] op_sel_hi:[0,1,1]
	v_mov_b32_e32 v116, v165
	v_pk_fma_f32 v[152:153], v[116:117], v[128:129], v[114:115] op_sel_hi:[0,1,1]
	ds_read_b128 v[216:219], v238 offset:16544
	v_mov_b32_e32 v104, v75
	v_mov_b32_e32 v74, v120
	v_mov_b32_e32 v75, v68
	v_mov_b32_e32 v68, v121
	s_waitcnt lgkmcnt(8)
	v_pk_fma_f32 v[118:119], v[136:137], v[166:167], 0 op_sel_hi:[1,0,0]
	v_mov_b32_e32 v132, v72
	v_pk_fma_f32 v[114:115], v[166:167], v[130:131], v[118:119] op_sel:[1,0,0]
	v_mov_b32_e32 v133, v106
	v_pk_fma_f32 v[114:115], v[168:169], v[138:139], v[114:115] op_sel_hi:[0,1,1]
	v_mov_b32_e32 v116, v169
	v_pk_fma_f32 v[154:155], v[116:117], v[128:129], v[114:115] op_sel_hi:[0,1,1]
	ds_read_b128 v[220:223], v238 offset:24752
	v_mov_b32_e32 v106, v73
	v_mov_b32_e32 v72, v122
	v_mov_b32_e32 v73, v70
	v_mov_b32_e32 v70, v123
	s_waitcnt lgkmcnt(8)
	v_pk_fma_f32 v[118:119], v[136:137], v[170:171], 0 op_sel_hi:[1,0,0]
	v_mov_b32_e32 v66, v124
	v_pk_fma_f32 v[114:115], v[170:171], v[130:131], v[118:119] op_sel:[1,0,0]
	v_mov_b32_e32 v67, v62
	v_pk_fma_f32 v[114:115], v[172:173], v[138:139], v[114:115] op_sel_hi:[0,1,1]
	v_mov_b32_e32 v116, v173
	v_pk_fma_f32 v[114:115], v[116:117], v[128:129], v[114:115] op_sel_hi:[0,1,1]
	ds_read_b128 v[224:227], v238 offset:32960
	v_mov_b32_e32 v62, v125
	v_mov_b32_e32 v64, v126
	v_mov_b32_e32 v65, v60
	v_mov_b32_e32 v60, v127
	s_waitcnt lgkmcnt(8)
	v_pk_fma_f32 v[120:121], v[136:137], v[174:175], 0 op_sel_hi:[1,0,0]
	s_nop 0
	v_pk_fma_f32 v[116:117], v[174:175], v[130:131], v[120:121] op_sel:[1,0,0]
	s_nop 0
	v_pk_fma_f32 v[116:117], v[176:177], v[138:139], v[116:117] op_sel_hi:[0,1,1]
	v_mov_b32_e32 v118, v177
	v_pk_fma_f32 v[116:117], v[118:119], v[128:129], v[116:117] op_sel_hi:[0,1,1]
	ds_read_b128 v[228:231], v238 offset:41168
	s_waitcnt lgkmcnt(8)
	v_pk_fma_f32 v[122:123], v[136:137], v[178:179], 0 op_sel_hi:[1,0,0]
	s_nop 0
	v_pk_fma_f32 v[118:119], v[178:179], v[130:131], v[122:123] op_sel:[1,0,0]
	s_nop 0
	v_pk_fma_f32 v[118:119], v[180:181], v[138:139], v[118:119] op_sel_hi:[0,1,1]
	v_mov_b32_e32 v120, v181
	v_pk_fma_f32 v[118:119], v[120:121], v[128:129], v[118:119] op_sel_hi:[0,1,1]
	ds_read_b128 v[232:235], v238 offset:49376
	s_waitcnt lgkmcnt(8)
	v_pk_fma_f32 v[124:125], v[136:137], v[182:183], 0 op_sel_hi:[1,0,0]
	s_nop 0
	v_pk_fma_f32 v[120:121], v[182:183], v[130:131], v[124:125] op_sel:[1,0,0]
	s_nop 0
	v_pk_fma_f32 v[120:121], v[184:185], v[138:139], v[120:121] op_sel_hi:[0,1,1]
	v_mov_b32_e32 v122, v185
	v_pk_fma_f32 v[120:121], v[122:123], v[128:129], v[120:121] op_sel_hi:[0,1,1]
	ds_read_b128 v[242:245], v238 offset:57584
	s_waitcnt lgkmcnt(8)
	v_pk_fma_f32 v[126:127], v[136:137], v[186:187], 0 op_sel_hi:[1,0,0]
	s_nop 0
	v_pk_fma_f32 v[122:123], v[186:187], v[130:131], v[126:127] op_sel:[1,0,0]
	s_nop 0
	v_pk_fma_f32 v[122:123], v[188:189], v[138:139], v[122:123] op_sel_hi:[0,1,1]
	v_mov_b32_e32 v124, v189
	v_pk_fma_f32 v[122:123], v[124:125], v[128:129], v[122:123] op_sel_hi:[0,1,1]
	ds_read_b128 v[246:249], v25 offset:1024
	s_waitcnt lgkmcnt(8)
	v_pk_fma_f32 v[140:141], v[136:137], v[198:199], 0 op_sel_hi:[1,0,0]
	s_nop 0
	v_pk_fma_f32 v[124:125], v[198:199], v[130:131], v[140:141] op_sel:[1,0,0]
	ds_read_b128 v[250:253], v25 offset:9232
	v_pk_fma_f32 v[124:125], v[200:201], v[138:139], v[124:125] op_sel_hi:[0,1,1]
	v_mov_b32_e32 v126, v201
	v_pk_fma_f32 v[124:125], v[126:127], v[128:129], v[124:125] op_sel_hi:[0,1,1]
	s_waitcnt lgkmcnt(8)
	v_pk_fma_f32 v[126:127], v[136:137], v[202:203], 0 op_sel_hi:[1,0,0]
	s_nop 0
	v_pk_fma_f32 v[126:127], v[202:203], v[130:131], v[126:127] op_sel:[1,0,0]
	v_mov_b32_e32 v140, v205
	v_pk_fma_f32 v[126:127], v[204:205], v[138:139], v[126:127] op_sel_hi:[0,1,1]
	v_pk_fma_f32 v[126:127], v[140:141], v[128:129], v[126:127] op_sel_hi:[0,1,1]
	ds_read_b128 v[158:161], v25 offset:17440
	s_waitcnt lgkmcnt(8)
	v_pk_fma_f32 v[144:145], v[136:137], v[216:217], 0 op_sel_hi:[1,0,0]
	s_nop 0
	v_pk_fma_f32 v[140:141], v[216:217], v[130:131], v[144:145] op_sel:[1,0,0]
	s_nop 0
	v_pk_fma_f32 v[140:141], v[218:219], v[138:139], v[140:141] op_sel_hi:[0,1,1]
	v_mov_b32_e32 v142, v219
	v_pk_fma_f32 v[140:141], v[142:143], v[128:129], v[140:141] op_sel_hi:[0,1,1]
	ds_read_b128 v[162:165], v25 offset:25648
	s_waitcnt lgkmcnt(8)
	v_pk_fma_f32 v[146:147], v[136:137], v[220:221], 0 op_sel_hi:[1,0,0]
	s_nop 0
	v_pk_fma_f32 v[142:143], v[220:221], v[130:131], v[146:147] op_sel:[1,0,0]
	s_nop 0
	v_pk_fma_f32 v[142:143], v[222:223], v[138:139], v[142:143] op_sel_hi:[0,1,1]
	v_mov_b32_e32 v144, v223
	v_pk_fma_f32 v[142:143], v[144:145], v[128:129], v[142:143] op_sel_hi:[0,1,1]
	ds_read_b128 v[166:169], v25 offset:33856
	s_waitcnt lgkmcnt(8)
; #define LAS __attribute__((address_space(3)))
; __global__ void __launch_bounds__(NTHREADS, 2) hybrid_fwd(Args a) {
;     ...
;                     for (int j = 0; j < 8; ++j) {
; #pragma unroll
;                         for (int e = 0; e < 16; ++e) { const f32x4 w = *(const LAS f32x4*)(rwT + e * 2052 + j * 256 + lane * 4);
;                             acc2[e] += y2[j][0] * (f32x2){w[0], w[0]}; acc2[e] += y2[j][1] * (f32x2){w[1], w[1]};
;                             acc2[e] += y2[j][2] * (f32x2){w[2], w[2]}; acc2[e] += y2[j][3] * (f32x2){w[3], w[3]}; }
;                         __builtin_amdgcn_sched_barrier(0);
	v_pk_fma_f32 v[148:149], v[136:137], v[224:225], 0 op_sel_hi:[1,0,0]
	s_nop 0
	v_pk_fma_f32 v[144:145], v[224:225], v[130:131], v[148:149] op_sel:[1,0,0]
	s_nop 0
	v_pk_fma_f32 v[144:145], v[226:227], v[138:139], v[144:145] op_sel_hi:[0,1,1]
	v_mov_b32_e32 v146, v227
	v_pk_fma_f32 v[144:145], v[146:147], v[128:129], v[144:145] op_sel_hi:[0,1,1]
	ds_read_b128 v[170:173], v25 offset:42064
	s_waitcnt lgkmcnt(8)
	v_pk_fma_f32 v[150:151], v[136:137], v[228:229], 0 op_sel_hi:[1,0,0]
	s_nop 0
	v_pk_fma_f32 v[146:147], v[228:229], v[130:131], v[150:151] op_sel:[1,0,0]
	s_nop 0
	v_pk_fma_f32 v[146:147], v[230:231], v[138:139], v[146:147] op_sel_hi:[0,1,1]
	v_mov_b32_e32 v148, v231
	v_pk_fma_f32 v[146:147], v[148:149], v[128:129], v[146:147] op_sel_hi:[0,1,1]
	ds_read_b128 v[174:177], v25 offset:50272
	s_waitcnt lgkmcnt(8)
	v_pk_fma_f32 v[194:195], v[136:137], v[232:233], 0 op_sel_hi:[1,0,0]
	s_nop 0
	v_pk_fma_f32 v[148:149], v[232:233], v[130:131], v[194:195] op_sel:[1,0,0]
	ds_read_b128 v[178:181], v25 offset:58480
	v_pk_fma_f32 v[148:149], v[234:235], v[138:139], v[148:149] op_sel_hi:[0,1,1]
	v_mov_b32_e32 v150, v235
	v_pk_fma_f32 v[148:149], v[150:151], v[128:129], v[148:149] op_sel_hi:[0,1,1]
	s_waitcnt lgkmcnt(8)
	v_pk_fma_f32 v[136:137], v[136:137], v[242:243], 0 op_sel_hi:[1,0,0]
	s_nop 0
	v_pk_fma_f32 v[130:131], v[242:243], v[130:131], v[136:137] op_sel:[1,0,0]
	v_mov_b32_e32 v136, v245
	v_pk_fma_f32 v[130:131], v[244:245], v[138:139], v[130:131] op_sel_hi:[0,1,1]
	v_pk_fma_f32 v[150:151], v[136:137], v[128:129], v[130:131] op_sel_hi:[0,1,1]
	ds_read_b128 v[182:185], v238 offset:1152
	s_waitcnt lgkmcnt(8)
	v_pk_fma_f32 v[112:113], v[132:133], v[246:247], v[112:113] op_sel_hi:[1,0,1]
	s_nop 0
	v_pk_fma_f32 v[112:113], v[246:247], v[106:107], v[112:113] op_sel:[1,0,0]
	v_mov_b32_e32 v128, v249
	v_pk_fma_f32 v[112:113], v[248:249], v[134:135], v[112:113] op_sel_hi:[0,1,1]
	v_pk_fma_f32 v[112:113], v[128:129], v[104:105], v[112:113] op_sel_hi:[0,1,1]
	ds_read_b128 v[186:189], v238 offset:9360
	s_waitcnt lgkmcnt(8)
	v_pk_fma_f32 v[136:137], v[132:133], v[250:251], v[152:153] op_sel_hi:[1,0,1]
	s_nop 0
	v_pk_fma_f32 v[128:129], v[250:251], v[106:107], v[136:137] op_sel:[1,0,0]
	s_nop 0
	v_pk_fma_f32 v[128:129], v[252:253], v[134:135], v[128:129] op_sel_hi:[0,1,1]
	v_mov_b32_e32 v130, v253
	v_pk_fma_f32 v[152:153], v[130:131], v[104:105], v[128:129] op_sel_hi:[0,1,1]
	ds_read_b128 v[198:201], v238 offset:17568
	s_waitcnt lgkmcnt(8)
	v_pk_fma_f32 v[136:137], v[132:133], v[158:159], v[154:155] op_sel_hi:[1,0,1]
	s_nop 0
	v_pk_fma_f32 v[128:129], v[158:159], v[106:107], v[136:137] op_sel:[1,0,0]
	ds_read_b128 v[202:205], v238 offset:25776
	v_pk_fma_f32 v[128:129], v[160:161], v[134:135], v[128:129] op_sel_hi:[0,1,1]
	v_mov_b32_e32 v130, v161
	v_pk_fma_f32 v[128:129], v[130:131], v[104:105], v[128:129] op_sel_hi:[0,1,1]
	s_waitcnt lgkmcnt(8)
	v_pk_fma_f32 v[114:115], v[132:133], v[162:163], v[114:115] op_sel_hi:[1,0,1]
	s_nop 0
	v_pk_fma_f32 v[114:115], v[162:163], v[106:107], v[114:115] op_sel:[1,0,0]
	v_mov_b32_e32 v130, v165
	v_pk_fma_f32 v[114:115], v[164:165], v[134:135], v[114:115] op_sel_hi:[0,1,1]
	ds_read_b128 v[216:219], v238 offset:33984
	v_pk_fma_f32 v[114:115], v[130:131], v[104:105], v[114:115] op_sel_hi:[0,1,1]
	s_waitcnt lgkmcnt(8)
	v_pk_fma_f32 v[116:117], v[132:133], v[166:167], v[116:117] op_sel_hi:[1,0,1]
	s_nop 0
	v_pk_fma_f32 v[116:117], v[166:167], v[106:107], v[116:117] op_sel:[1,0,0]
	v_mov_b32_e32 v130, v169
	v_pk_fma_f32 v[116:117], v[168:169], v[134:135], v[116:117] op_sel_hi:[0,1,1]
	ds_read_b128 v[220:223], v238 offset:42192
	v_pk_fma_f32 v[116:117], v[130:131], v[104:105], v[116:117] op_sel_hi:[0,1,1]
	s_waitcnt lgkmcnt(8)
	v_pk_fma_f32 v[118:119], v[132:133], v[170:171], v[118:119] op_sel_hi:[1,0,1]
	s_nop 0
	v_pk_fma_f32 v[118:119], v[170:171], v[106:107], v[118:119] op_sel:[1,0,0]
	v_mov_b32_e32 v130, v173
	v_pk_fma_f32 v[118:119], v[172:173], v[134:135], v[118:119] op_sel_hi:[0,1,1]
	ds_read_b128 v[224:227], v238 offset:50400
	v_pk_fma_f32 v[118:119], v[130:131], v[104:105], v[118:119] op_sel_hi:[0,1,1]
	s_waitcnt lgkmcnt(8)
	v_pk_fma_f32 v[120:121], v[132:133], v[174:175], v[120:121] op_sel_hi:[1,0,1]
	s_nop 0
	v_pk_fma_f32 v[120:121], v[174:175], v[106:107], v[120:121] op_sel:[1,0,0]
	v_mov_b32_e32 v130, v177
	v_pk_fma_f32 v[120:121], v[176:177], v[134:135], v[120:121] op_sel_hi:[0,1,1]
	ds_read_b128 v[228:231], v238 offset:58608
	v_pk_fma_f32 v[120:121], v[130:131], v[104:105], v[120:121] op_sel_hi:[0,1,1]
	s_waitcnt lgkmcnt(8)
	v_pk_fma_f32 v[122:123], v[132:133], v[178:179], v[122:123] op_sel_hi:[1,0,1]
	s_nop 0
	v_pk_fma_f32 v[122:123], v[178:179], v[106:107], v[122:123] op_sel:[1,0,0]
	v_mov_b32_e32 v130, v181
	v_pk_fma_f32 v[122:123], v[180:181], v[134:135], v[122:123] op_sel_hi:[0,1,1]
	ds_read_b128 v[232:235], v25 offset:2048
	v_pk_fma_f32 v[122:123], v[130:131], v[104:105], v[122:123] op_sel_hi:[0,1,1]
	s_waitcnt lgkmcnt(8)
	v_pk_fma_f32 v[124:125], v[132:133], v[182:183], v[124:125] op_sel_hi:[1,0,1]
	s_nop 0
	v_pk_fma_f32 v[124:125], v[182:183], v[106:107], v[124:125] op_sel:[1,0,0]
	v_mov_b32_e32 v130, v185
	v_pk_fma_f32 v[124:125], v[184:185], v[134:135], v[124:125] op_sel_hi:[0,1,1]
	ds_read_b128 v[242:245], v25 offset:10256
	v_pk_fma_f32 v[124:125], v[130:131], v[104:105], v[124:125] op_sel_hi:[0,1,1]
	s_waitcnt lgkmcnt(8)
	v_pk_fma_f32 v[126:127], v[132:133], v[186:187], v[126:127] op_sel_hi:[1,0,1]
	s_nop 0
	v_pk_fma_f32 v[126:127], v[186:187], v[106:107], v[126:127] op_sel:[1,0,0]
	v_mov_b32_e32 v130, v189
	v_pk_fma_f32 v[126:127], v[188:189], v[134:135], v[126:127] op_sel_hi:[0,1,1]
	ds_read_b128 v[246:249], v25 offset:18464
	v_pk_fma_f32 v[126:127], v[130:131], v[104:105], v[126:127] op_sel_hi:[0,1,1]
	s_waitcnt lgkmcnt(8)
; #define LAS __attribute__((address_space(3)))
; __global__ void __launch_bounds__(NTHREADS, 2) hybrid_fwd(Args a) {
;     ...
;                     for (int j = 0; j < 8; ++j) {
; #pragma unroll
;                         for (int e = 0; e < 16; ++e) { const f32x4 w = *(const LAS f32x4*)(rwT + e * 2052 + j * 256 + lane * 4);
;                             acc2[e] += y2[j][0] * (f32x2){w[0], w[0]}; acc2[e] += y2[j][1] * (f32x2){w[1], w[1]};
;                             acc2[e] += y2[j][2] * (f32x2){w[2], w[2]}; acc2[e] += y2[j][3] * (f32x2){w[3], w[3]}; }
;                         __builtin_amdgcn_sched_barrier(0);
	v_pk_fma_f32 v[130:131], v[132:133], v[198:199], v[140:141] op_sel_hi:[1,0,1]
	s_nop 0
	v_pk_fma_f32 v[130:131], v[198:199], v[106:107], v[130:131] op_sel:[1,0,0]
	v_mov_b32_e32 v136, v201
	v_pk_fma_f32 v[130:131], v[200:201], v[134:135], v[130:131] op_sel_hi:[0,1,1]
	v_pk_fma_f32 v[130:131], v[136:137], v[104:105], v[130:131] op_sel_hi:[0,1,1]
	ds_read_b128 v[250:253], v25 offset:26672
	s_waitcnt lgkmcnt(8)
	v_pk_fma_f32 v[140:141], v[132:133], v[202:203], v[142:143] op_sel_hi:[1,0,1]
	s_nop 0
	v_pk_fma_f32 v[136:137], v[202:203], v[106:107], v[140:141] op_sel:[1,0,0]
	s_nop 0
	v_pk_fma_f32 v[136:137], v[204:205], v[134:135], v[136:137] op_sel_hi:[0,1,1]
	v_mov_b32_e32 v138, v205
	v_pk_fma_f32 v[136:137], v[138:139], v[104:105], v[136:137] op_sel_hi:[0,1,1]
	ds_read_b128 v[162:165], v25 offset:34880
	s_waitcnt lgkmcnt(8)
	v_pk_fma_f32 v[142:143], v[132:133], v[216:217], v[144:145] op_sel_hi:[1,0,1]
	s_nop 0
	v_pk_fma_f32 v[138:139], v[216:217], v[106:107], v[142:143] op_sel:[1,0,0]
	s_nop 0
	v_pk_fma_f32 v[138:139], v[218:219], v[134:135], v[138:139] op_sel_hi:[0,1,1]
	v_mov_b32_e32 v140, v219
	v_pk_fma_f32 v[138:139], v[140:141], v[104:105], v[138:139] op_sel_hi:[0,1,1]
	ds_read_b128 v[166:169], v25 offset:43088
	s_waitcnt lgkmcnt(8)
	v_pk_fma_f32 v[144:145], v[132:133], v[220:221], v[146:147] op_sel_hi:[1,0,1]
	s_nop 0
	v_pk_fma_f32 v[140:141], v[220:221], v[106:107], v[144:145] op_sel:[1,0,0]
	s_nop 0
	v_pk_fma_f32 v[140:141], v[222:223], v[134:135], v[140:141] op_sel_hi:[0,1,1]
	v_mov_b32_e32 v142, v223
	v_pk_fma_f32 v[140:141], v[142:143], v[104:105], v[140:141] op_sel_hi:[0,1,1]
	ds_read_b128 v[170:173], v25 offset:51296
	s_waitcnt lgkmcnt(8)
	v_pk_fma_f32 v[146:147], v[132:133], v[224:225], v[148:149] op_sel_hi:[1,0,1]
	s_nop 0
	v_pk_fma_f32 v[142:143], v[224:225], v[106:107], v[146:147] op_sel:[1,0,0]
	s_nop 0
	v_pk_fma_f32 v[142:143], v[226:227], v[134:135], v[142:143] op_sel_hi:[0,1,1]
	v_mov_b32_e32 v144, v227
	v_pk_fma_f32 v[142:143], v[144:145], v[104:105], v[142:143] op_sel_hi:[0,1,1]
	ds_read_b128 v[174:177], v25 offset:59504
	s_waitcnt lgkmcnt(8)
	v_pk_fma_f32 v[132:133], v[132:133], v[228:229], v[150:151] op_sel_hi:[1,0,1]
	s_nop 0
	v_pk_fma_f32 v[106:107], v[228:229], v[106:107], v[132:133] op_sel:[1,0,0]
	v_mov_b32_e32 v132, v231
	v_pk_fma_f32 v[106:107], v[230:231], v[134:135], v[106:107] op_sel_hi:[0,1,1]
	v_pk_fma_f32 v[144:145], v[132:133], v[104:105], v[106:107] op_sel_hi:[0,1,1]
	ds_read_b128 v[178:181], v238 offset:2176
	ds_read_b128 v[182:185], v238 offset:10384
	s_waitcnt lgkmcnt(8)
	v_pk_fma_f32 v[112:113], v[108:109], v[232:233], v[112:113] op_sel_hi:[1,0,1]
	s_nop 0
	v_pk_fma_f32 v[104:105], v[232:233], v[98:99], v[112:113] op_sel:[1,0,0]
	v_mov_b32_e32 v112, v245
	v_pk_fma_f32 v[104:105], v[234:235], v[110:111], v[104:105] op_sel_hi:[0,1,1]
	v_mov_b32_e32 v106, v235
	v_pk_fma_f32 v[104:105], v[106:107], v[96:97], v[104:105] op_sel_hi:[0,1,1]
	v_pk_fma_f32 v[106:107], v[108:109], v[242:243], v[152:153] op_sel_hi:[1,0,1]
	s_nop 0
	v_pk_fma_f32 v[106:107], v[242:243], v[98:99], v[106:107] op_sel:[1,0,0]
	s_nop 0
	v_pk_fma_f32 v[106:107], v[244:245], v[110:111], v[106:107] op_sel_hi:[0,1,1]
	ds_read_b128 v[186:189], v238 offset:18592
	v_pk_fma_f32 v[146:147], v[112:113], v[96:97], v[106:107] op_sel_hi:[0,1,1]
	s_waitcnt lgkmcnt(8)
	v_pk_fma_f32 v[106:107], v[108:109], v[246:247], v[128:129] op_sel_hi:[1,0,1]
	s_nop 0
	v_pk_fma_f32 v[106:107], v[246:247], v[98:99], v[106:107] op_sel:[1,0,0]
	v_mov_b32_e32 v112, v249
	v_pk_fma_f32 v[106:107], v[248:249], v[110:111], v[106:107] op_sel_hi:[0,1,1]
	ds_read_b128 v[158:161], v238 offset:26800
	v_pk_fma_f32 v[106:107], v[112:113], v[96:97], v[106:107] op_sel_hi:[0,1,1]
	s_waitcnt lgkmcnt(8)
	v_pk_fma_f32 v[112:113], v[108:109], v[250:251], v[114:115] op_sel_hi:[1,0,1]
	s_nop 0
	v_pk_fma_f32 v[112:113], v[250:251], v[98:99], v[112:113] op_sel:[1,0,0]
	v_mov_b32_e32 v114, v253
	v_pk_fma_f32 v[112:113], v[252:253], v[110:111], v[112:113] op_sel_hi:[0,1,1]
	ds_read_b128 v[198:201], v238 offset:35008
	v_pk_fma_f32 v[112:113], v[114:115], v[96:97], v[112:113] op_sel_hi:[0,1,1]
	s_waitcnt lgkmcnt(8)
	v_pk_fma_f32 v[114:115], v[108:109], v[162:163], v[116:117] op_sel_hi:[1,0,1]
	s_nop 0
	v_pk_fma_f32 v[114:115], v[162:163], v[98:99], v[114:115] op_sel:[1,0,0]
	v_mov_b32_e32 v116, v165
	v_pk_fma_f32 v[114:115], v[164:165], v[110:111], v[114:115] op_sel_hi:[0,1,1]
	ds_read_b128 v[202:205], v238 offset:43216
	v_pk_fma_f32 v[114:115], v[116:117], v[96:97], v[114:115] op_sel_hi:[0,1,1]
	s_waitcnt lgkmcnt(8)
	v_pk_fma_f32 v[116:117], v[108:109], v[166:167], v[118:119] op_sel_hi:[1,0,1]
	s_nop 0
	v_pk_fma_f32 v[116:117], v[166:167], v[98:99], v[116:117] op_sel:[1,0,0]
	v_mov_b32_e32 v118, v169
	v_pk_fma_f32 v[116:117], v[168:169], v[110:111], v[116:117] op_sel_hi:[0,1,1]
	ds_read_b128 v[216:219], v238 offset:51424
	v_pk_fma_f32 v[116:117], v[118:119], v[96:97], v[116:117] op_sel_hi:[0,1,1]
	s_waitcnt lgkmcnt(8)
	v_pk_fma_f32 v[118:119], v[108:109], v[170:171], v[120:121] op_sel_hi:[1,0,1]
	s_nop 0
	v_pk_fma_f32 v[118:119], v[170:171], v[98:99], v[118:119] op_sel:[1,0,0]
	v_mov_b32_e32 v120, v173
	v_pk_fma_f32 v[118:119], v[172:173], v[110:111], v[118:119] op_sel_hi:[0,1,1]
	ds_read_b128 v[220:223], v238 offset:59632
	v_pk_fma_f32 v[118:119], v[120:121], v[96:97], v[118:119] op_sel_hi:[0,1,1]
	s_waitcnt lgkmcnt(8)
	v_pk_fma_f32 v[120:121], v[108:109], v[174:175], v[122:123] op_sel_hi:[1,0,1]
	s_nop 0
	v_pk_fma_f32 v[120:121], v[174:175], v[98:99], v[120:121] op_sel:[1,0,0]
	v_mov_b32_e32 v122, v177
	v_pk_fma_f32 v[120:121], v[176:177], v[110:111], v[120:121] op_sel_hi:[0,1,1]
	ds_read_b128 v[224:227], v25 offset:3072
	v_pk_fma_f32 v[120:121], v[122:123], v[96:97], v[120:121] op_sel_hi:[0,1,1]
	s_waitcnt lgkmcnt(8)
; #define LAS __attribute__((address_space(3)))
; __global__ void __launch_bounds__(NTHREADS, 2) hybrid_fwd(Args a) {
;     ...
;                     for (int j = 0; j < 8; ++j) {
; #pragma unroll
;                         for (int e = 0; e < 16; ++e) { const f32x4 w = *(const LAS f32x4*)(rwT + e * 2052 + j * 256 + lane * 4);
;                             acc2[e] += y2[j][0] * (f32x2){w[0], w[0]}; acc2[e] += y2[j][1] * (f32x2){w[1], w[1]};
;                             acc2[e] += y2[j][2] * (f32x2){w[2], w[2]}; acc2[e] += y2[j][3] * (f32x2){w[3], w[3]}; }
;                         __builtin_amdgcn_sched_barrier(0);
	v_pk_fma_f32 v[122:123], v[108:109], v[178:179], v[124:125] op_sel_hi:[1,0,1]
	s_nop 0
	v_pk_fma_f32 v[122:123], v[178:179], v[98:99], v[122:123] op_sel:[1,0,0]
	v_mov_b32_e32 v124, v181
	v_pk_fma_f32 v[122:123], v[180:181], v[110:111], v[122:123] op_sel_hi:[0,1,1]
	ds_read_b128 v[228:231], v25 offset:11280
	v_pk_fma_f32 v[122:123], v[124:125], v[96:97], v[122:123] op_sel_hi:[0,1,1]
	s_waitcnt lgkmcnt(8)
	v_pk_fma_f32 v[124:125], v[108:109], v[182:183], v[126:127] op_sel_hi:[1,0,1]
	s_nop 0
	v_pk_fma_f32 v[124:125], v[182:183], v[98:99], v[124:125] op_sel:[1,0,0]
	v_mov_b32_e32 v126, v185
	v_pk_fma_f32 v[124:125], v[184:185], v[110:111], v[124:125] op_sel_hi:[0,1,1]
	v_pk_fma_f32 v[124:125], v[126:127], v[96:97], v[124:125] op_sel_hi:[0,1,1]
	ds_read_b128 v[232:235], v25 offset:19488
	s_waitcnt lgkmcnt(8)
	v_pk_fma_f32 v[130:131], v[108:109], v[186:187], v[130:131] op_sel_hi:[1,0,1]
	s_nop 0
	v_pk_fma_f32 v[126:127], v[186:187], v[98:99], v[130:131] op_sel:[1,0,0]
	s_nop 0
	v_pk_fma_f32 v[126:127], v[188:189], v[110:111], v[126:127] op_sel_hi:[0,1,1]
	v_mov_b32_e32 v128, v189
	v_pk_fma_f32 v[126:127], v[128:129], v[96:97], v[126:127] op_sel_hi:[0,1,1]
	ds_read_b128 v[242:245], v25 offset:27696
	s_waitcnt lgkmcnt(8)
	v_pk_fma_f32 v[132:133], v[108:109], v[158:159], v[136:137] op_sel_hi:[1,0,1]
	s_nop 0
	v_pk_fma_f32 v[128:129], v[158:159], v[98:99], v[132:133] op_sel:[1,0,0]
	s_nop 0
	v_pk_fma_f32 v[128:129], v[160:161], v[110:111], v[128:129] op_sel_hi:[0,1,1]
	v_mov_b32_e32 v130, v161
	v_pk_fma_f32 v[128:129], v[130:131], v[96:97], v[128:129] op_sel_hi:[0,1,1]
	ds_read_b128 v[246:249], v25 offset:35904
	s_waitcnt lgkmcnt(8)
	v_pk_fma_f32 v[134:135], v[108:109], v[198:199], v[138:139] op_sel_hi:[1,0,1]
	s_nop 0
	v_pk_fma_f32 v[130:131], v[198:199], v[98:99], v[134:135] op_sel:[1,0,0]
	s_nop 0
	v_pk_fma_f32 v[130:131], v[200:201], v[110:111], v[130:131] op_sel_hi:[0,1,1]
	v_mov_b32_e32 v132, v201
	v_pk_fma_f32 v[130:131], v[132:133], v[96:97], v[130:131] op_sel_hi:[0,1,1]
	ds_read_b128 v[250:253], v25 offset:44112
	s_waitcnt lgkmcnt(8)
	v_pk_fma_f32 v[136:137], v[108:109], v[202:203], v[140:141] op_sel_hi:[1,0,1]
	s_nop 0
	v_pk_fma_f32 v[132:133], v[202:203], v[98:99], v[136:137] op_sel:[1,0,0]
	s_nop 0
	v_pk_fma_f32 v[132:133], v[204:205], v[110:111], v[132:133] op_sel_hi:[0,1,1]
	v_mov_b32_e32 v134, v205
	v_pk_fma_f32 v[132:133], v[134:135], v[96:97], v[132:133] op_sel_hi:[0,1,1]
	ds_read_b128 v[162:165], v25 offset:52320
	s_waitcnt lgkmcnt(8)
	v_pk_fma_f32 v[138:139], v[108:109], v[216:217], v[142:143] op_sel_hi:[1,0,1]
	s_nop 0
	v_pk_fma_f32 v[134:135], v[216:217], v[98:99], v[138:139] op_sel:[1,0,0]
	s_nop 0
	v_pk_fma_f32 v[134:135], v[218:219], v[110:111], v[134:135] op_sel_hi:[0,1,1]
	v_mov_b32_e32 v136, v219
	v_pk_fma_f32 v[134:135], v[136:137], v[96:97], v[134:135] op_sel_hi:[0,1,1]
	ds_read_b128 v[166:169], v25 offset:60528
	s_waitcnt lgkmcnt(8)
	v_pk_fma_f32 v[108:109], v[108:109], v[220:221], v[144:145] op_sel_hi:[1,0,1]
	s_nop 0
	v_pk_fma_f32 v[98:99], v[220:221], v[98:99], v[108:109] op_sel:[1,0,0]
	v_mov_b32_e32 v108, v223
	v_pk_fma_f32 v[98:99], v[222:223], v[110:111], v[98:99] op_sel_hi:[0,1,1]
	v_pk_fma_f32 v[136:137], v[108:109], v[96:97], v[98:99] op_sel_hi:[0,1,1]
	ds_read_b128 v[170:173], v238 offset:3200
	ds_read_b128 v[174:177], v238 offset:11408
	s_waitcnt lgkmcnt(8)
	v_pk_fma_f32 v[104:105], v[100:101], v[224:225], v[104:105] op_sel_hi:[1,0,1]
	s_nop 0
	v_pk_fma_f32 v[96:97], v[224:225], v[90:91], v[104:105] op_sel:[1,0,0]
	v_mov_b32_e32 v104, v231
	v_pk_fma_f32 v[96:97], v[226:227], v[102:103], v[96:97] op_sel_hi:[0,1,1]
	v_mov_b32_e32 v98, v227
	v_pk_fma_f32 v[96:97], v[98:99], v[88:89], v[96:97] op_sel_hi:[0,1,1]
	v_pk_fma_f32 v[98:99], v[100:101], v[228:229], v[146:147] op_sel_hi:[1,0,1]
	s_nop 0
	v_pk_fma_f32 v[98:99], v[228:229], v[90:91], v[98:99] op_sel:[1,0,0]
	s_nop 0
	v_pk_fma_f32 v[98:99], v[230:231], v[102:103], v[98:99] op_sel_hi:[0,1,1]
	ds_read_b128 v[178:181], v238 offset:19616
	v_pk_fma_f32 v[138:139], v[104:105], v[88:89], v[98:99] op_sel_hi:[0,1,1]
	s_waitcnt lgkmcnt(8)
	v_pk_fma_f32 v[98:99], v[100:101], v[232:233], v[106:107] op_sel_hi:[1,0,1]
	s_nop 0
	v_pk_fma_f32 v[98:99], v[232:233], v[90:91], v[98:99] op_sel:[1,0,0]
	v_mov_b32_e32 v104, v235
	v_pk_fma_f32 v[98:99], v[234:235], v[102:103], v[98:99] op_sel_hi:[0,1,1]
	v_pk_fma_f32 v[98:99], v[104:105], v[88:89], v[98:99] op_sel_hi:[0,1,1]
	ds_read_b128 v[182:185], v238 offset:27824
	s_waitcnt lgkmcnt(8)
	v_pk_fma_f32 v[108:109], v[100:101], v[242:243], v[112:113] op_sel_hi:[1,0,1]
	s_nop 0
	v_pk_fma_f32 v[104:105], v[242:243], v[90:91], v[108:109] op_sel:[1,0,0]
	s_nop 0
	v_pk_fma_f32 v[104:105], v[244:245], v[102:103], v[104:105] op_sel_hi:[0,1,1]
	v_mov_b32_e32 v106, v245
	v_pk_fma_f32 v[104:105], v[106:107], v[88:89], v[104:105] op_sel_hi:[0,1,1]
	ds_read_b128 v[186:189], v238 offset:36032
	s_waitcnt lgkmcnt(8)
	v_pk_fma_f32 v[110:111], v[100:101], v[246:247], v[114:115] op_sel_hi:[1,0,1]
	s_nop 0
	v_pk_fma_f32 v[106:107], v[246:247], v[90:91], v[110:111] op_sel:[1,0,0]
	s_nop 0
	v_pk_fma_f32 v[106:107], v[248:249], v[102:103], v[106:107] op_sel_hi:[0,1,1]
	v_mov_b32_e32 v108, v249
	v_pk_fma_f32 v[106:107], v[108:109], v[88:89], v[106:107] op_sel_hi:[0,1,1]
	ds_read_b128 v[158:161], v238 offset:44240
	s_waitcnt lgkmcnt(8)
	v_pk_fma_f32 v[112:113], v[100:101], v[250:251], v[116:117] op_sel_hi:[1,0,1]
	s_nop 0
	v_pk_fma_f32 v[108:109], v[250:251], v[90:91], v[112:113] op_sel:[1,0,0]
	s_nop 0
	v_pk_fma_f32 v[108:109], v[252:253], v[102:103], v[108:109] op_sel_hi:[0,1,1]
	v_mov_b32_e32 v110, v253
	v_pk_fma_f32 v[108:109], v[110:111], v[88:89], v[108:109] op_sel_hi:[0,1,1]
	ds_read_b128 v[198:201], v238 offset:52448
	s_waitcnt lgkmcnt(8)
; #define LAS __attribute__((address_space(3)))
; __global__ void __launch_bounds__(NTHREADS, 2) hybrid_fwd(Args a) {
;     ...
;                     for (int j = 0; j < 8; ++j) {
; #pragma unroll
;                         for (int e = 0; e < 16; ++e) { const f32x4 w = *(const LAS f32x4*)(rwT + e * 2052 + j * 256 + lane * 4);
;                             acc2[e] += y2[j][0] * (f32x2){w[0], w[0]}; acc2[e] += y2[j][1] * (f32x2){w[1], w[1]};
;                             acc2[e] += y2[j][2] * (f32x2){w[2], w[2]}; acc2[e] += y2[j][3] * (f32x2){w[3], w[3]}; }
;                         __builtin_amdgcn_sched_barrier(0);
	v_pk_fma_f32 v[114:115], v[100:101], v[162:163], v[118:119] op_sel_hi:[1,0,1]
	s_nop 0
	v_pk_fma_f32 v[110:111], v[162:163], v[90:91], v[114:115] op_sel:[1,0,0]
	s_nop 0
	v_pk_fma_f32 v[110:111], v[164:165], v[102:103], v[110:111] op_sel_hi:[0,1,1]
	v_mov_b32_e32 v112, v165
	v_pk_fma_f32 v[110:111], v[112:113], v[88:89], v[110:111] op_sel_hi:[0,1,1]
	ds_read_b128 v[202:205], v238 offset:60656
	s_waitcnt lgkmcnt(8)
	v_pk_fma_f32 v[116:117], v[100:101], v[166:167], v[120:121] op_sel_hi:[1,0,1]
	s_nop 0
	v_pk_fma_f32 v[112:113], v[166:167], v[90:91], v[116:117] op_sel:[1,0,0]
	s_nop 0
	v_pk_fma_f32 v[112:113], v[168:169], v[102:103], v[112:113] op_sel_hi:[0,1,1]
	v_mov_b32_e32 v114, v169
	v_pk_fma_f32 v[112:113], v[114:115], v[88:89], v[112:113] op_sel_hi:[0,1,1]
	ds_read_b128 v[216:219], v25 offset:4096
	s_waitcnt lgkmcnt(8)
	v_pk_fma_f32 v[118:119], v[100:101], v[170:171], v[122:123] op_sel_hi:[1,0,1]
	s_nop 0
	v_pk_fma_f32 v[114:115], v[170:171], v[90:91], v[118:119] op_sel:[1,0,0]
	s_nop 0
	v_pk_fma_f32 v[114:115], v[172:173], v[102:103], v[114:115] op_sel_hi:[0,1,1]
	v_mov_b32_e32 v116, v173
	v_pk_fma_f32 v[114:115], v[116:117], v[88:89], v[114:115] op_sel_hi:[0,1,1]
	ds_read_b128 v[220:223], v25 offset:12304
	s_waitcnt lgkmcnt(8)
	v_pk_fma_f32 v[120:121], v[100:101], v[174:175], v[124:125] op_sel_hi:[1,0,1]
	s_nop 0
	v_pk_fma_f32 v[116:117], v[174:175], v[90:91], v[120:121] op_sel:[1,0,0]
	s_nop 0
	v_pk_fma_f32 v[116:117], v[176:177], v[102:103], v[116:117] op_sel_hi:[0,1,1]
	v_mov_b32_e32 v118, v177
	v_pk_fma_f32 v[116:117], v[118:119], v[88:89], v[116:117] op_sel_hi:[0,1,1]
	ds_read_b128 v[224:227], v25 offset:20512
	s_waitcnt lgkmcnt(8)
	v_pk_fma_f32 v[122:123], v[100:101], v[178:179], v[126:127] op_sel_hi:[1,0,1]
	s_nop 0
	v_pk_fma_f32 v[118:119], v[178:179], v[90:91], v[122:123] op_sel:[1,0,0]
	s_nop 0
	v_pk_fma_f32 v[118:119], v[180:181], v[102:103], v[118:119] op_sel_hi:[0,1,1]
	v_mov_b32_e32 v120, v181
	v_pk_fma_f32 v[118:119], v[120:121], v[88:89], v[118:119] op_sel_hi:[0,1,1]
	ds_read_b128 v[228:231], v25 offset:28720
	s_waitcnt lgkmcnt(8)
	v_pk_fma_f32 v[124:125], v[100:101], v[182:183], v[128:129] op_sel_hi:[1,0,1]
	s_nop 0
	v_pk_fma_f32 v[120:121], v[182:183], v[90:91], v[124:125] op_sel:[1,0,0]
	s_nop 0
	v_pk_fma_f32 v[120:121], v[184:185], v[102:103], v[120:121] op_sel_hi:[0,1,1]
	v_mov_b32_e32 v122, v185
	v_pk_fma_f32 v[120:121], v[122:123], v[88:89], v[120:121] op_sel_hi:[0,1,1]
	ds_read_b128 v[232:235], v25 offset:36928
	s_waitcnt lgkmcnt(8)
	v_pk_fma_f32 v[126:127], v[100:101], v[186:187], v[130:131] op_sel_hi:[1,0,1]
	s_nop 0
	v_pk_fma_f32 v[122:123], v[186:187], v[90:91], v[126:127] op_sel:[1,0,0]
	s_nop 0
	v_pk_fma_f32 v[122:123], v[188:189], v[102:103], v[122:123] op_sel_hi:[0,1,1]
	v_mov_b32_e32 v124, v189
	v_pk_fma_f32 v[122:123], v[124:125], v[88:89], v[122:123] op_sel_hi:[0,1,1]
	ds_read_b128 v[242:245], v25 offset:45136
	s_waitcnt lgkmcnt(8)
	v_pk_fma_f32 v[128:129], v[100:101], v[158:159], v[132:133] op_sel_hi:[1,0,1]
	s_nop 0
	v_pk_fma_f32 v[124:125], v[158:159], v[90:91], v[128:129] op_sel:[1,0,0]
	s_nop 0
	v_pk_fma_f32 v[124:125], v[160:161], v[102:103], v[124:125] op_sel_hi:[0,1,1]
	v_mov_b32_e32 v126, v161
	v_pk_fma_f32 v[124:125], v[126:127], v[88:89], v[124:125] op_sel_hi:[0,1,1]
	ds_read_b128 v[246:249], v25 offset:53344
	s_waitcnt lgkmcnt(8)
	v_pk_fma_f32 v[130:131], v[100:101], v[198:199], v[134:135] op_sel_hi:[1,0,1]
	s_nop 0
	v_pk_fma_f32 v[126:127], v[198:199], v[90:91], v[130:131] op_sel:[1,0,0]
	s_nop 0
	v_pk_fma_f32 v[126:127], v[200:201], v[102:103], v[126:127] op_sel_hi:[0,1,1]
	v_mov_b32_e32 v128, v201
	v_pk_fma_f32 v[126:127], v[128:129], v[88:89], v[126:127] op_sel_hi:[0,1,1]
	ds_read_b128 v[250:253], v25 offset:61552
	s_waitcnt lgkmcnt(8)
	v_pk_fma_f32 v[100:101], v[100:101], v[202:203], v[136:137] op_sel_hi:[1,0,1]
	s_nop 0
	v_pk_fma_f32 v[90:91], v[202:203], v[90:91], v[100:101] op_sel:[1,0,0]
	v_mov_b32_e32 v100, v205
	v_pk_fma_f32 v[90:91], v[204:205], v[102:103], v[90:91] op_sel_hi:[0,1,1]
	v_pk_fma_f32 v[128:129], v[100:101], v[88:89], v[90:91] op_sel_hi:[0,1,1]
	ds_read_b128 v[162:165], v238 offset:4224
	ds_read_b128 v[166:169], v238 offset:12432
	s_waitcnt lgkmcnt(8)
	v_pk_fma_f32 v[96:97], v[92:93], v[216:217], v[96:97] op_sel_hi:[1,0,1]
	s_nop 0
	v_pk_fma_f32 v[88:89], v[216:217], v[86:87], v[96:97] op_sel:[1,0,0]
	v_mov_b32_e32 v96, v223
	v_pk_fma_f32 v[88:89], v[218:219], v[94:95], v[88:89] op_sel_hi:[0,1,1]
	v_mov_b32_e32 v90, v219
	v_pk_fma_f32 v[88:89], v[90:91], v[84:85], v[88:89] op_sel_hi:[0,1,1]
	v_pk_fma_f32 v[90:91], v[92:93], v[220:221], v[138:139] op_sel_hi:[1,0,1]
	s_nop 0
	v_pk_fma_f32 v[90:91], v[220:221], v[86:87], v[90:91] op_sel:[1,0,0]
	s_nop 0
	v_pk_fma_f32 v[90:91], v[222:223], v[94:95], v[90:91] op_sel_hi:[0,1,1]
	ds_read_b128 v[170:173], v238 offset:20640
	v_pk_fma_f32 v[130:131], v[96:97], v[84:85], v[90:91] op_sel_hi:[0,1,1]
	s_waitcnt lgkmcnt(8)
	v_pk_fma_f32 v[90:91], v[92:93], v[224:225], v[98:99] op_sel_hi:[1,0,1]
	s_nop 0
	v_pk_fma_f32 v[90:91], v[224:225], v[86:87], v[90:91] op_sel:[1,0,0]
	v_mov_b32_e32 v96, v227
	v_pk_fma_f32 v[90:91], v[226:227], v[94:95], v[90:91] op_sel_hi:[0,1,1]
	v_pk_fma_f32 v[90:91], v[96:97], v[84:85], v[90:91] op_sel_hi:[0,1,1]
	ds_read_b128 v[174:177], v238 offset:28848
	s_waitcnt lgkmcnt(8)
	v_pk_fma_f32 v[100:101], v[92:93], v[228:229], v[104:105] op_sel_hi:[1,0,1]
	s_nop 0
	v_pk_fma_f32 v[96:97], v[228:229], v[86:87], v[100:101] op_sel:[1,0,0]
	s_nop 0
	v_pk_fma_f32 v[96:97], v[230:231], v[94:95], v[96:97] op_sel_hi:[0,1,1]
	v_mov_b32_e32 v98, v231
	v_pk_fma_f32 v[96:97], v[98:99], v[84:85], v[96:97] op_sel_hi:[0,1,1]
	ds_read_b128 v[178:181], v238 offset:37056
	s_waitcnt lgkmcnt(8)
; #define LAS __attribute__((address_space(3)))
; __global__ void __launch_bounds__(NTHREADS, 2) hybrid_fwd(Args a) {
;     ...
;                     for (int j = 0; j < 8; ++j) {
; #pragma unroll
;                         for (int e = 0; e < 16; ++e) { const f32x4 w = *(const LAS f32x4*)(rwT + e * 2052 + j * 256 + lane * 4);
;                             acc2[e] += y2[j][0] * (f32x2){w[0], w[0]}; acc2[e] += y2[j][1] * (f32x2){w[1], w[1]};
;                             acc2[e] += y2[j][2] * (f32x2){w[2], w[2]}; acc2[e] += y2[j][3] * (f32x2){w[3], w[3]}; }
;                         __builtin_amdgcn_sched_barrier(0);
	v_pk_fma_f32 v[102:103], v[92:93], v[232:233], v[106:107] op_sel_hi:[1,0,1]
	s_nop 0
	v_pk_fma_f32 v[98:99], v[232:233], v[86:87], v[102:103] op_sel:[1,0,0]
	s_nop 0
	v_pk_fma_f32 v[98:99], v[234:235], v[94:95], v[98:99] op_sel_hi:[0,1,1]
	v_mov_b32_e32 v100, v235
	v_pk_fma_f32 v[98:99], v[100:101], v[84:85], v[98:99] op_sel_hi:[0,1,1]
	ds_read_b128 v[182:185], v238 offset:45264
	s_waitcnt lgkmcnt(8)
	v_pk_fma_f32 v[104:105], v[92:93], v[242:243], v[108:109] op_sel_hi:[1,0,1]
	s_nop 0
	v_pk_fma_f32 v[100:101], v[242:243], v[86:87], v[104:105] op_sel:[1,0,0]
	s_nop 0
	v_pk_fma_f32 v[100:101], v[244:245], v[94:95], v[100:101] op_sel_hi:[0,1,1]
	v_mov_b32_e32 v102, v245
	v_pk_fma_f32 v[100:101], v[102:103], v[84:85], v[100:101] op_sel_hi:[0,1,1]
	ds_read_b128 v[186:189], v238 offset:53472
	s_waitcnt lgkmcnt(8)
	v_pk_fma_f32 v[106:107], v[92:93], v[246:247], v[110:111] op_sel_hi:[1,0,1]
	s_nop 0
	v_pk_fma_f32 v[102:103], v[246:247], v[86:87], v[106:107] op_sel:[1,0,0]
	s_nop 0
	v_pk_fma_f32 v[102:103], v[248:249], v[94:95], v[102:103] op_sel_hi:[0,1,1]
	v_mov_b32_e32 v104, v249
	v_pk_fma_f32 v[102:103], v[104:105], v[84:85], v[102:103] op_sel_hi:[0,1,1]
	ds_read_b128 v[158:161], v238 offset:61680
	s_waitcnt lgkmcnt(8)
	v_pk_fma_f32 v[108:109], v[92:93], v[250:251], v[112:113] op_sel_hi:[1,0,1]
	s_nop 0
	v_pk_fma_f32 v[104:105], v[250:251], v[86:87], v[108:109] op_sel:[1,0,0]
	s_nop 0
	v_pk_fma_f32 v[104:105], v[252:253], v[94:95], v[104:105] op_sel_hi:[0,1,1]
	v_mov_b32_e32 v106, v253
	v_pk_fma_f32 v[104:105], v[106:107], v[84:85], v[104:105] op_sel_hi:[0,1,1]
	ds_read_b128 v[198:201], v25 offset:5120
	s_waitcnt lgkmcnt(8)
	v_pk_fma_f32 v[110:111], v[92:93], v[162:163], v[114:115] op_sel_hi:[1,0,1]
	s_nop 0
	v_pk_fma_f32 v[106:107], v[162:163], v[86:87], v[110:111] op_sel:[1,0,0]
	s_nop 0
	v_pk_fma_f32 v[106:107], v[164:165], v[94:95], v[106:107] op_sel_hi:[0,1,1]
	v_mov_b32_e32 v108, v165
	v_pk_fma_f32 v[106:107], v[108:109], v[84:85], v[106:107] op_sel_hi:[0,1,1]
	ds_read_b128 v[202:205], v25 offset:13328
	s_waitcnt lgkmcnt(8)
	v_pk_fma_f32 v[112:113], v[92:93], v[166:167], v[116:117] op_sel_hi:[1,0,1]
	s_nop 0
	v_pk_fma_f32 v[108:109], v[166:167], v[86:87], v[112:113] op_sel:[1,0,0]
	s_nop 0
	v_pk_fma_f32 v[108:109], v[168:169], v[94:95], v[108:109] op_sel_hi:[0,1,1]
	v_mov_b32_e32 v110, v169
	v_pk_fma_f32 v[108:109], v[110:111], v[84:85], v[108:109] op_sel_hi:[0,1,1]
	ds_read_b128 v[216:219], v25 offset:21536
	s_waitcnt lgkmcnt(8)
	v_pk_fma_f32 v[114:115], v[92:93], v[170:171], v[118:119] op_sel_hi:[1,0,1]
	s_nop 0
	v_pk_fma_f32 v[110:111], v[170:171], v[86:87], v[114:115] op_sel:[1,0,0]
	s_nop 0
	v_pk_fma_f32 v[110:111], v[172:173], v[94:95], v[110:111] op_sel_hi:[0,1,1]
	v_mov_b32_e32 v112, v173
	v_pk_fma_f32 v[110:111], v[112:113], v[84:85], v[110:111] op_sel_hi:[0,1,1]
	ds_read_b128 v[220:223], v25 offset:29744
	s_waitcnt lgkmcnt(8)
	v_pk_fma_f32 v[116:117], v[92:93], v[174:175], v[120:121] op_sel_hi:[1,0,1]
	s_nop 0
	v_pk_fma_f32 v[112:113], v[174:175], v[86:87], v[116:117] op_sel:[1,0,0]
	s_nop 0
	v_pk_fma_f32 v[112:113], v[176:177], v[94:95], v[112:113] op_sel_hi:[0,1,1]
	v_mov_b32_e32 v114, v177
	v_pk_fma_f32 v[112:113], v[114:115], v[84:85], v[112:113] op_sel_hi:[0,1,1]
	ds_read_b128 v[224:227], v25 offset:37952
	s_waitcnt lgkmcnt(8)
	v_pk_fma_f32 v[118:119], v[92:93], v[178:179], v[122:123] op_sel_hi:[1,0,1]
	s_nop 0
	v_pk_fma_f32 v[114:115], v[178:179], v[86:87], v[118:119] op_sel:[1,0,0]
	s_nop 0
	v_pk_fma_f32 v[114:115], v[180:181], v[94:95], v[114:115] op_sel_hi:[0,1,1]
	v_mov_b32_e32 v116, v181
	v_pk_fma_f32 v[114:115], v[116:117], v[84:85], v[114:115] op_sel_hi:[0,1,1]
	ds_read_b128 v[228:231], v25 offset:46160
	s_waitcnt lgkmcnt(8)
	v_pk_fma_f32 v[120:121], v[92:93], v[182:183], v[124:125] op_sel_hi:[1,0,1]
	s_nop 0
	v_pk_fma_f32 v[116:117], v[182:183], v[86:87], v[120:121] op_sel:[1,0,0]
	s_nop 0
	v_pk_fma_f32 v[116:117], v[184:185], v[94:95], v[116:117] op_sel_hi:[0,1,1]
	v_mov_b32_e32 v118, v185
	v_pk_fma_f32 v[116:117], v[118:119], v[84:85], v[116:117] op_sel_hi:[0,1,1]
	ds_read_b128 v[232:235], v25 offset:54368
	s_waitcnt lgkmcnt(8)
	v_pk_fma_f32 v[122:123], v[92:93], v[186:187], v[126:127] op_sel_hi:[1,0,1]
	s_nop 0
	v_pk_fma_f32 v[118:119], v[186:187], v[86:87], v[122:123] op_sel:[1,0,0]
	s_nop 0
	v_pk_fma_f32 v[118:119], v[188:189], v[94:95], v[118:119] op_sel_hi:[0,1,1]
	v_mov_b32_e32 v120, v189
	v_pk_fma_f32 v[118:119], v[120:121], v[84:85], v[118:119] op_sel_hi:[0,1,1]
	ds_read_b128 v[242:245], v25 offset:62576
	s_waitcnt lgkmcnt(8)
	v_pk_fma_f32 v[92:93], v[92:93], v[158:159], v[128:129] op_sel_hi:[1,0,1]
	s_nop 0
	v_pk_fma_f32 v[86:87], v[158:159], v[86:87], v[92:93] op_sel:[1,0,0]
	v_mov_b32_e32 v92, v161
	v_pk_fma_f32 v[86:87], v[160:161], v[94:95], v[86:87] op_sel_hi:[0,1,1]
	v_pk_fma_f32 v[120:121], v[92:93], v[84:85], v[86:87] op_sel_hi:[0,1,1]
	ds_read_b128 v[246:249], v238 offset:5248
	s_waitcnt lgkmcnt(8)
	v_pk_fma_f32 v[88:89], v[80:81], v[198:199], v[88:89] op_sel_hi:[1,0,1]
	s_nop 0
	v_pk_fma_f32 v[84:85], v[198:199], v[78:79], v[88:89] op_sel:[1,0,0]
	s_nop 0
	v_pk_fma_f32 v[84:85], v[200:201], v[82:83], v[84:85] op_sel_hi:[0,1,1]
	v_mov_b32_e32 v86, v201
	v_pk_fma_f32 v[84:85], v[86:87], v[76:77], v[84:85] op_sel_hi:[0,1,1]
	ds_read_b128 v[250:253], v238 offset:13456
	s_waitcnt lgkmcnt(8)
	v_pk_fma_f32 v[92:93], v[80:81], v[202:203], v[130:131] op_sel_hi:[1,0,1]
	s_nop 0
	v_pk_fma_f32 v[86:87], v[202:203], v[78:79], v[92:93] op_sel:[1,0,0]
	s_nop 0
	v_pk_fma_f32 v[86:87], v[204:205], v[82:83], v[86:87] op_sel_hi:[0,1,1]
	v_mov_b32_e32 v88, v205
	v_pk_fma_f32 v[122:123], v[88:89], v[76:77], v[86:87] op_sel_hi:[0,1,1]
	ds_read_b128 v[162:165], v238 offset:21664
	s_waitcnt lgkmcnt(8)
; #define LAS __attribute__((address_space(3)))
; __global__ void __launch_bounds__(NTHREADS, 2) hybrid_fwd(Args a) {
;     ...
;                     for (int j = 0; j < 8; ++j) {
; #pragma unroll
;                         for (int e = 0; e < 16; ++e) { const f32x4 w = *(const LAS f32x4*)(rwT + e * 2052 + j * 256 + lane * 4);
;                             acc2[e] += y2[j][0] * (f32x2){w[0], w[0]}; acc2[e] += y2[j][1] * (f32x2){w[1], w[1]};
;                             acc2[e] += y2[j][2] * (f32x2){w[2], w[2]}; acc2[e] += y2[j][3] * (f32x2){w[3], w[3]}; }
;                         __builtin_amdgcn_sched_barrier(0);
	v_pk_fma_f32 v[90:91], v[80:81], v[216:217], v[90:91] op_sel_hi:[1,0,1]
	s_nop 0
	v_pk_fma_f32 v[86:87], v[216:217], v[78:79], v[90:91] op_sel:[1,0,0]
	s_nop 0
	v_pk_fma_f32 v[86:87], v[218:219], v[82:83], v[86:87] op_sel_hi:[0,1,1]
	v_mov_b32_e32 v88, v219
	v_pk_fma_f32 v[86:87], v[88:89], v[76:77], v[86:87] op_sel_hi:[0,1,1]
	ds_read_b128 v[166:169], v238 offset:29872
	s_waitcnt lgkmcnt(8)
	v_pk_fma_f32 v[92:93], v[80:81], v[220:221], v[96:97] op_sel_hi:[1,0,1]
	s_nop 0
	v_pk_fma_f32 v[88:89], v[220:221], v[78:79], v[92:93] op_sel:[1,0,0]
	s_nop 0
	v_pk_fma_f32 v[88:89], v[222:223], v[82:83], v[88:89] op_sel_hi:[0,1,1]
	v_mov_b32_e32 v90, v223
	v_pk_fma_f32 v[88:89], v[90:91], v[76:77], v[88:89] op_sel_hi:[0,1,1]
	ds_read_b128 v[170:173], v238 offset:38080
	s_waitcnt lgkmcnt(8)
	v_pk_fma_f32 v[94:95], v[80:81], v[224:225], v[98:99] op_sel_hi:[1,0,1]
	s_nop 0
	v_pk_fma_f32 v[90:91], v[224:225], v[78:79], v[94:95] op_sel:[1,0,0]
	s_nop 0
	v_pk_fma_f32 v[90:91], v[226:227], v[82:83], v[90:91] op_sel_hi:[0,1,1]
	v_mov_b32_e32 v92, v227
	v_pk_fma_f32 v[90:91], v[92:93], v[76:77], v[90:91] op_sel_hi:[0,1,1]
	ds_read_b128 v[174:177], v238 offset:46288
	s_waitcnt lgkmcnt(8)
	v_pk_fma_f32 v[96:97], v[80:81], v[228:229], v[100:101] op_sel_hi:[1,0,1]
	s_nop 0
	v_pk_fma_f32 v[92:93], v[228:229], v[78:79], v[96:97] op_sel:[1,0,0]
	s_nop 0
	v_pk_fma_f32 v[92:93], v[230:231], v[82:83], v[92:93] op_sel_hi:[0,1,1]
	v_mov_b32_e32 v94, v231
	v_pk_fma_f32 v[92:93], v[94:95], v[76:77], v[92:93] op_sel_hi:[0,1,1]
	ds_read_b128 v[178:181], v238 offset:54496
	s_waitcnt lgkmcnt(8)
	v_pk_fma_f32 v[98:99], v[80:81], v[232:233], v[102:103] op_sel_hi:[1,0,1]
	s_nop 0
	v_pk_fma_f32 v[94:95], v[232:233], v[78:79], v[98:99] op_sel:[1,0,0]
	s_nop 0
	v_pk_fma_f32 v[94:95], v[234:235], v[82:83], v[94:95] op_sel_hi:[0,1,1]
	v_mov_b32_e32 v96, v235
	v_pk_fma_f32 v[94:95], v[96:97], v[76:77], v[94:95] op_sel_hi:[0,1,1]
	ds_read_b128 v[182:185], v238 offset:62704
	s_waitcnt lgkmcnt(8)
	v_pk_fma_f32 v[100:101], v[80:81], v[242:243], v[104:105] op_sel_hi:[1,0,1]
	s_nop 0
	v_pk_fma_f32 v[96:97], v[242:243], v[78:79], v[100:101] op_sel:[1,0,0]
	s_nop 0
	v_pk_fma_f32 v[96:97], v[244:245], v[82:83], v[96:97] op_sel_hi:[0,1,1]
	v_mov_b32_e32 v98, v245
	v_pk_fma_f32 v[96:97], v[98:99], v[76:77], v[96:97] op_sel_hi:[0,1,1]
	ds_read_b128 v[186:189], v25 offset:6144
	s_waitcnt lgkmcnt(8)
	v_pk_fma_f32 v[102:103], v[80:81], v[246:247], v[106:107] op_sel_hi:[1,0,1]
	s_nop 0
	v_pk_fma_f32 v[98:99], v[246:247], v[78:79], v[102:103] op_sel:[1,0,0]
	s_nop 0
	v_pk_fma_f32 v[98:99], v[248:249], v[82:83], v[98:99] op_sel_hi:[0,1,1]
	v_mov_b32_e32 v100, v249
	v_pk_fma_f32 v[98:99], v[100:101], v[76:77], v[98:99] op_sel_hi:[0,1,1]
	ds_read_b128 v[158:161], v25 offset:14352
	s_waitcnt lgkmcnt(8)
	v_pk_fma_f32 v[104:105], v[80:81], v[250:251], v[108:109] op_sel_hi:[1,0,1]
	s_nop 0
	v_pk_fma_f32 v[100:101], v[250:251], v[78:79], v[104:105] op_sel:[1,0,0]
	s_nop 0
	v_pk_fma_f32 v[100:101], v[252:253], v[82:83], v[100:101] op_sel_hi:[0,1,1]
	v_mov_b32_e32 v102, v253
	v_pk_fma_f32 v[100:101], v[102:103], v[76:77], v[100:101] op_sel_hi:[0,1,1]
	ds_read_b128 v[198:201], v25 offset:22560
	s_waitcnt lgkmcnt(8)
	v_pk_fma_f32 v[106:107], v[80:81], v[162:163], v[110:111] op_sel_hi:[1,0,1]
	s_nop 0
	v_pk_fma_f32 v[102:103], v[162:163], v[78:79], v[106:107] op_sel:[1,0,0]
	s_nop 0
	v_pk_fma_f32 v[102:103], v[164:165], v[82:83], v[102:103] op_sel_hi:[0,1,1]
	v_mov_b32_e32 v104, v165
	v_pk_fma_f32 v[102:103], v[104:105], v[76:77], v[102:103] op_sel_hi:[0,1,1]
	ds_read_b128 v[202:205], v25 offset:30768
	s_waitcnt lgkmcnt(8)
	v_pk_fma_f32 v[108:109], v[80:81], v[166:167], v[112:113] op_sel_hi:[1,0,1]
	s_nop 0
	v_pk_fma_f32 v[104:105], v[166:167], v[78:79], v[108:109] op_sel:[1,0,0]
	s_nop 0
	v_pk_fma_f32 v[104:105], v[168:169], v[82:83], v[104:105] op_sel_hi:[0,1,1]
	v_mov_b32_e32 v106, v169
	v_pk_fma_f32 v[104:105], v[106:107], v[76:77], v[104:105] op_sel_hi:[0,1,1]
	ds_read_b128 v[216:219], v25 offset:38976
	s_waitcnt lgkmcnt(8)
	v_pk_fma_f32 v[110:111], v[80:81], v[170:171], v[114:115] op_sel_hi:[1,0,1]
	s_nop 0
	v_pk_fma_f32 v[106:107], v[170:171], v[78:79], v[110:111] op_sel:[1,0,0]
	s_nop 0
	v_pk_fma_f32 v[106:107], v[172:173], v[82:83], v[106:107] op_sel_hi:[0,1,1]
	v_mov_b32_e32 v108, v173
	v_pk_fma_f32 v[106:107], v[108:109], v[76:77], v[106:107] op_sel_hi:[0,1,1]
	ds_read_b128 v[220:223], v25 offset:47184
	s_waitcnt lgkmcnt(8)
	v_pk_fma_f32 v[112:113], v[80:81], v[174:175], v[116:117] op_sel_hi:[1,0,1]
	s_nop 0
	v_pk_fma_f32 v[108:109], v[174:175], v[78:79], v[112:113] op_sel:[1,0,0]
	s_nop 0
	v_pk_fma_f32 v[108:109], v[176:177], v[82:83], v[108:109] op_sel_hi:[0,1,1]
	v_mov_b32_e32 v110, v177
	v_pk_fma_f32 v[108:109], v[110:111], v[76:77], v[108:109] op_sel_hi:[0,1,1]
	ds_read_b128 v[224:227], v25 offset:55392
	s_waitcnt lgkmcnt(8)
	v_pk_fma_f32 v[114:115], v[80:81], v[178:179], v[118:119] op_sel_hi:[1,0,1]
	s_nop 0
	v_pk_fma_f32 v[110:111], v[178:179], v[78:79], v[114:115] op_sel:[1,0,0]
	s_nop 0
	v_pk_fma_f32 v[110:111], v[180:181], v[82:83], v[110:111] op_sel_hi:[0,1,1]
	v_mov_b32_e32 v112, v181
	v_pk_fma_f32 v[110:111], v[112:113], v[76:77], v[110:111] op_sel_hi:[0,1,1]
	ds_read_b128 v[228:231], v25 offset:63600
	s_waitcnt lgkmcnt(8)
	v_pk_fma_f32 v[80:81], v[80:81], v[182:183], v[120:121] op_sel_hi:[1,0,1]
	s_nop 0
	v_pk_fma_f32 v[78:79], v[182:183], v[78:79], v[80:81] op_sel:[1,0,0]
	v_mov_b32_e32 v80, v185
	v_pk_fma_f32 v[78:79], v[184:185], v[82:83], v[78:79] op_sel_hi:[0,1,1]
	v_pk_fma_f32 v[112:113], v[80:81], v[76:77], v[78:79] op_sel_hi:[0,1,1]
	ds_read_b128 v[232:235], v238 offset:6272
	s_waitcnt lgkmcnt(8)
; #define LAS __attribute__((address_space(3)))
; __global__ void __launch_bounds__(NTHREADS, 2) hybrid_fwd(Args a) {
;     ...
;                     for (int j = 0; j < 8; ++j) {
; #pragma unroll
;                         for (int e = 0; e < 16; ++e) { const f32x4 w = *(const LAS f32x4*)(rwT + e * 2052 + j * 256 + lane * 4);
;                             acc2[e] += y2[j][0] * (f32x2){w[0], w[0]}; acc2[e] += y2[j][1] * (f32x2){w[1], w[1]};
;                             acc2[e] += y2[j][2] * (f32x2){w[2], w[2]}; acc2[e] += y2[j][3] * (f32x2){w[3], w[3]}; }
;                         __builtin_amdgcn_sched_barrier(0);
	v_pk_fma_f32 v[80:81], v[72:73], v[186:187], v[84:85] op_sel_hi:[1,0,1]
	s_nop 0
	v_pk_fma_f32 v[76:77], v[186:187], v[70:71], v[80:81] op_sel:[1,0,0]
	s_nop 0
	v_pk_fma_f32 v[76:77], v[188:189], v[74:75], v[76:77] op_sel_hi:[0,1,1]
	v_mov_b32_e32 v78, v189
	v_pk_fma_f32 v[76:77], v[78:79], v[68:69], v[76:77] op_sel_hi:[0,1,1]
	ds_read_b128 v[242:245], v238 offset:14480
	s_waitcnt lgkmcnt(8)
	v_pk_fma_f32 v[82:83], v[72:73], v[158:159], v[122:123] op_sel_hi:[1,0,1]
	s_nop 0
	v_pk_fma_f32 v[78:79], v[158:159], v[70:71], v[82:83] op_sel:[1,0,0]
	s_nop 0
	v_pk_fma_f32 v[78:79], v[160:161], v[74:75], v[78:79] op_sel_hi:[0,1,1]
	v_mov_b32_e32 v80, v161
	v_pk_fma_f32 v[114:115], v[80:81], v[68:69], v[78:79] op_sel_hi:[0,1,1]
	ds_read_b128 v[246:249], v238 offset:22688
	s_waitcnt lgkmcnt(8)
	v_pk_fma_f32 v[82:83], v[72:73], v[198:199], v[86:87] op_sel_hi:[1,0,1]
	s_nop 0
	v_pk_fma_f32 v[78:79], v[198:199], v[70:71], v[82:83] op_sel:[1,0,0]
	s_nop 0
	v_pk_fma_f32 v[78:79], v[200:201], v[74:75], v[78:79] op_sel_hi:[0,1,1]
	v_mov_b32_e32 v80, v201
	v_pk_fma_f32 v[78:79], v[80:81], v[68:69], v[78:79] op_sel_hi:[0,1,1]
	ds_read_b128 v[250:253], v238 offset:30896
	s_waitcnt lgkmcnt(8)
	v_pk_fma_f32 v[84:85], v[72:73], v[202:203], v[88:89] op_sel_hi:[1,0,1]
	s_nop 0
	v_pk_fma_f32 v[80:81], v[202:203], v[70:71], v[84:85] op_sel:[1,0,0]
	s_nop 0
	v_pk_fma_f32 v[80:81], v[204:205], v[74:75], v[80:81] op_sel_hi:[0,1,1]
	v_mov_b32_e32 v82, v205
	v_pk_fma_f32 v[80:81], v[82:83], v[68:69], v[80:81] op_sel_hi:[0,1,1]
	ds_read_b128 v[162:165], v238 offset:39104
	s_waitcnt lgkmcnt(8)
	v_pk_fma_f32 v[86:87], v[72:73], v[216:217], v[90:91] op_sel_hi:[1,0,1]
	s_nop 0
	v_pk_fma_f32 v[82:83], v[216:217], v[70:71], v[86:87] op_sel:[1,0,0]
	s_nop 0
	v_pk_fma_f32 v[82:83], v[218:219], v[74:75], v[82:83] op_sel_hi:[0,1,1]
	v_mov_b32_e32 v84, v219
	v_pk_fma_f32 v[82:83], v[84:85], v[68:69], v[82:83] op_sel_hi:[0,1,1]
	ds_read_b128 v[166:169], v238 offset:47312
	s_waitcnt lgkmcnt(8)
	v_pk_fma_f32 v[88:89], v[72:73], v[220:221], v[92:93] op_sel_hi:[1,0,1]
	s_nop 0
	v_pk_fma_f32 v[84:85], v[220:221], v[70:71], v[88:89] op_sel:[1,0,0]
	s_nop 0
	v_pk_fma_f32 v[84:85], v[222:223], v[74:75], v[84:85] op_sel_hi:[0,1,1]
	v_mov_b32_e32 v86, v223
	v_pk_fma_f32 v[84:85], v[86:87], v[68:69], v[84:85] op_sel_hi:[0,1,1]
	ds_read_b128 v[170:173], v238 offset:55520
	s_waitcnt lgkmcnt(8)
	v_pk_fma_f32 v[90:91], v[72:73], v[224:225], v[94:95] op_sel_hi:[1,0,1]
	s_nop 0
	v_pk_fma_f32 v[86:87], v[224:225], v[70:71], v[90:91] op_sel:[1,0,0]
	s_nop 0
	v_pk_fma_f32 v[86:87], v[226:227], v[74:75], v[86:87] op_sel_hi:[0,1,1]
	v_mov_b32_e32 v88, v227
	v_pk_fma_f32 v[86:87], v[88:89], v[68:69], v[86:87] op_sel_hi:[0,1,1]
	ds_read_b128 v[174:177], v238 offset:63728
	s_waitcnt lgkmcnt(8)
	v_pk_fma_f32 v[92:93], v[72:73], v[228:229], v[96:97] op_sel_hi:[1,0,1]
	s_nop 0
	v_pk_fma_f32 v[88:89], v[228:229], v[70:71], v[92:93] op_sel:[1,0,0]
	s_nop 0
	v_pk_fma_f32 v[88:89], v[230:231], v[74:75], v[88:89] op_sel_hi:[0,1,1]
	v_mov_b32_e32 v90, v231
	v_pk_fma_f32 v[88:89], v[90:91], v[68:69], v[88:89] op_sel_hi:[0,1,1]
	ds_read_b128 v[178:181], v25 offset:7168
	s_waitcnt lgkmcnt(8)
	v_pk_fma_f32 v[94:95], v[72:73], v[232:233], v[98:99] op_sel_hi:[1,0,1]
	s_nop 0
	v_pk_fma_f32 v[90:91], v[232:233], v[70:71], v[94:95] op_sel:[1,0,0]
	s_nop 0
	v_pk_fma_f32 v[90:91], v[234:235], v[74:75], v[90:91] op_sel_hi:[0,1,1]
	v_mov_b32_e32 v92, v235
	v_pk_fma_f32 v[90:91], v[92:93], v[68:69], v[90:91] op_sel_hi:[0,1,1]
	ds_read_b128 v[182:185], v25 offset:15376
	s_waitcnt lgkmcnt(8)
	v_pk_fma_f32 v[96:97], v[72:73], v[242:243], v[100:101] op_sel_hi:[1,0,1]
	s_nop 0
	v_pk_fma_f32 v[92:93], v[242:243], v[70:71], v[96:97] op_sel:[1,0,0]
	s_nop 0
	v_pk_fma_f32 v[92:93], v[244:245], v[74:75], v[92:93] op_sel_hi:[0,1,1]
	v_mov_b32_e32 v94, v245
	v_pk_fma_f32 v[92:93], v[94:95], v[68:69], v[92:93] op_sel_hi:[0,1,1]
	ds_read_b128 v[186:189], v25 offset:23584
	s_waitcnt lgkmcnt(8)
	v_pk_fma_f32 v[98:99], v[72:73], v[246:247], v[102:103] op_sel_hi:[1,0,1]
	s_nop 0
	v_pk_fma_f32 v[94:95], v[246:247], v[70:71], v[98:99] op_sel:[1,0,0]
	s_nop 0
	v_pk_fma_f32 v[94:95], v[248:249], v[74:75], v[94:95] op_sel_hi:[0,1,1]
	v_mov_b32_e32 v96, v249
	v_pk_fma_f32 v[94:95], v[96:97], v[68:69], v[94:95] op_sel_hi:[0,1,1]
	ds_read_b128 v[158:161], v25 offset:31792
	s_waitcnt lgkmcnt(8)
	v_pk_fma_f32 v[100:101], v[72:73], v[250:251], v[104:105] op_sel_hi:[1,0,1]
	s_nop 0
	v_pk_fma_f32 v[96:97], v[250:251], v[70:71], v[100:101] op_sel:[1,0,0]
	s_nop 0
	v_pk_fma_f32 v[96:97], v[252:253], v[74:75], v[96:97] op_sel_hi:[0,1,1]
	v_mov_b32_e32 v98, v253
	v_pk_fma_f32 v[96:97], v[98:99], v[68:69], v[96:97] op_sel_hi:[0,1,1]
	ds_read_b128 v[198:201], v25 offset:40000
	s_waitcnt lgkmcnt(8)
	v_pk_fma_f32 v[102:103], v[72:73], v[162:163], v[106:107] op_sel_hi:[1,0,1]
	s_nop 0
	v_pk_fma_f32 v[98:99], v[162:163], v[70:71], v[102:103] op_sel:[1,0,0]
	s_nop 0
	v_pk_fma_f32 v[98:99], v[164:165], v[74:75], v[98:99] op_sel_hi:[0,1,1]
	v_mov_b32_e32 v100, v165
	v_pk_fma_f32 v[98:99], v[100:101], v[68:69], v[98:99] op_sel_hi:[0,1,1]
	ds_read_b128 v[202:205], v25 offset:48208
	s_waitcnt lgkmcnt(8)
	v_pk_fma_f32 v[104:105], v[72:73], v[166:167], v[108:109] op_sel_hi:[1,0,1]
	s_nop 0
	v_pk_fma_f32 v[100:101], v[166:167], v[70:71], v[104:105] op_sel:[1,0,0]
	s_nop 0
	v_pk_fma_f32 v[100:101], v[168:169], v[74:75], v[100:101] op_sel_hi:[0,1,1]
	v_mov_b32_e32 v102, v169
	v_pk_fma_f32 v[100:101], v[102:103], v[68:69], v[100:101] op_sel_hi:[0,1,1]
	ds_read_b128 v[216:219], v25 offset:56416
	s_waitcnt lgkmcnt(8)
; #define LAS __attribute__((address_space(3)))
; __global__ void __launch_bounds__(NTHREADS, 2) hybrid_fwd(Args a) {
;     ...
;                     for (int j = 0; j < 8; ++j) {
; #pragma unroll
;                         for (int e = 0; e < 16; ++e) { const f32x4 w = *(const LAS f32x4*)(rwT + e * 2052 + j * 256 + lane * 4);
;                             acc2[e] += y2[j][0] * (f32x2){w[0], w[0]}; acc2[e] += y2[j][1] * (f32x2){w[1], w[1]};
;                             acc2[e] += y2[j][2] * (f32x2){w[2], w[2]}; acc2[e] += y2[j][3] * (f32x2){w[3], w[3]}; }
;                         __builtin_amdgcn_sched_barrier(0);
	v_pk_fma_f32 v[106:107], v[72:73], v[170:171], v[110:111] op_sel_hi:[1,0,1]
	s_nop 0
	v_pk_fma_f32 v[102:103], v[170:171], v[70:71], v[106:107] op_sel:[1,0,0]
	s_nop 0
	v_pk_fma_f32 v[102:103], v[172:173], v[74:75], v[102:103] op_sel_hi:[0,1,1]
	v_mov_b32_e32 v104, v173
	v_pk_fma_f32 v[102:103], v[104:105], v[68:69], v[102:103] op_sel_hi:[0,1,1]
	ds_read_b128 v[220:223], v25 offset:64624
	s_waitcnt lgkmcnt(8)
	v_pk_fma_f32 v[72:73], v[72:73], v[174:175], v[112:113] op_sel_hi:[1,0,1]
	s_nop 0
	v_pk_fma_f32 v[70:71], v[174:175], v[70:71], v[72:73] op_sel:[1,0,0]
	v_mov_b32_e32 v72, v177
	v_pk_fma_f32 v[70:71], v[176:177], v[74:75], v[70:71] op_sel_hi:[0,1,1]
	v_pk_fma_f32 v[104:105], v[72:73], v[68:69], v[70:71] op_sel_hi:[0,1,1]
	ds_read_b128 v[224:227], v238 offset:7296
	s_waitcnt lgkmcnt(8)
	v_pk_fma_f32 v[72:73], v[66:67], v[178:179], v[76:77] op_sel_hi:[1,0,1]
	s_nop 0
	v_pk_fma_f32 v[68:69], v[178:179], v[62:63], v[72:73] op_sel:[1,0,0]
	s_nop 0
	v_pk_fma_f32 v[68:69], v[180:181], v[64:65], v[68:69] op_sel_hi:[0,1,1]
	v_mov_b32_e32 v70, v181
	v_pk_fma_f32 v[68:69], v[70:71], v[60:61], v[68:69] op_sel_hi:[0,1,1]
	ds_read_b128 v[228:231], v238 offset:15504
	s_waitcnt lgkmcnt(8)
	v_pk_fma_f32 v[74:75], v[66:67], v[182:183], v[114:115] op_sel_hi:[1,0,1]
	s_nop 0
	v_pk_fma_f32 v[70:71], v[182:183], v[62:63], v[74:75] op_sel:[1,0,0]
	s_nop 0
	v_pk_fma_f32 v[70:71], v[184:185], v[64:65], v[70:71] op_sel_hi:[0,1,1]
	v_mov_b32_e32 v72, v185
	v_pk_fma_f32 v[70:71], v[72:73], v[60:61], v[70:71] op_sel_hi:[0,1,1]
	ds_read_b128 v[232:235], v238 offset:23712
	s_waitcnt lgkmcnt(8)
	v_pk_fma_f32 v[76:77], v[66:67], v[186:187], v[78:79] op_sel_hi:[1,0,1]
	s_nop 0
	v_pk_fma_f32 v[72:73], v[186:187], v[62:63], v[76:77] op_sel:[1,0,0]
	s_nop 0
	v_pk_fma_f32 v[72:73], v[188:189], v[64:65], v[72:73] op_sel_hi:[0,1,1]
	v_mov_b32_e32 v74, v189
	v_pk_fma_f32 v[72:73], v[74:75], v[60:61], v[72:73] op_sel_hi:[0,1,1]
	ds_read_b128 v[242:245], v238 offset:31920
	s_waitcnt lgkmcnt(8)
	v_pk_fma_f32 v[78:79], v[66:67], v[158:159], v[80:81] op_sel_hi:[1,0,1]
	s_nop 0
	v_pk_fma_f32 v[74:75], v[158:159], v[62:63], v[78:79] op_sel:[1,0,0]
	ds_read_b128 v[246:249], v238 offset:40128
	v_pk_fma_f32 v[74:75], v[160:161], v[64:65], v[74:75] op_sel_hi:[0,1,1]
	v_mov_b32_e32 v76, v161
	v_pk_fma_f32 v[76:77], v[76:77], v[60:61], v[74:75] op_sel_hi:[0,1,1]
	s_waitcnt lgkmcnt(8)
	v_pk_fma_f32 v[74:75], v[66:67], v[198:199], v[82:83] op_sel_hi:[1,0,1]
	s_nop 0
	v_pk_fma_f32 v[74:75], v[198:199], v[62:63], v[74:75] op_sel:[1,0,0]
	v_mov_b32_e32 v78, v201
	v_pk_fma_f32 v[74:75], v[200:201], v[64:65], v[74:75] op_sel_hi:[0,1,1]
	v_pk_fma_f32 v[74:75], v[78:79], v[60:61], v[74:75] op_sel_hi:[0,1,1]
	ds_read_b128 v[250:253], v238 offset:48336
	s_waitcnt lgkmcnt(8)
	v_pk_fma_f32 v[82:83], v[66:67], v[202:203], v[84:85] op_sel_hi:[1,0,1]
	s_nop 0
	v_pk_fma_f32 v[78:79], v[202:203], v[62:63], v[82:83] op_sel:[1,0,0]
	s_nop 0
	v_pk_fma_f32 v[78:79], v[204:205], v[64:65], v[78:79] op_sel_hi:[0,1,1]
	v_mov_b32_e32 v80, v205
	v_pk_fma_f32 v[78:79], v[80:81], v[60:61], v[78:79] op_sel_hi:[0,1,1]
	ds_read_b128 v[162:165], v238 offset:56544
	s_waitcnt lgkmcnt(8)
	v_pk_fma_f32 v[84:85], v[66:67], v[216:217], v[86:87] op_sel_hi:[1,0,1]
	s_nop 0
	v_pk_fma_f32 v[80:81], v[216:217], v[62:63], v[84:85] op_sel:[1,0,0]
	s_nop 0
	v_pk_fma_f32 v[80:81], v[218:219], v[64:65], v[80:81] op_sel_hi:[0,1,1]
	v_mov_b32_e32 v82, v219
	v_pk_fma_f32 v[80:81], v[82:83], v[60:61], v[80:81] op_sel_hi:[0,1,1]
	ds_read_b128 v[166:169], v238 offset:64752
	s_waitcnt lgkmcnt(8)
	v_pk_fma_f32 v[86:87], v[66:67], v[220:221], v[88:89] op_sel_hi:[1,0,1]
	s_nop 0
	v_pk_fma_f32 v[82:83], v[220:221], v[62:63], v[86:87] op_sel:[1,0,0]
	s_nop 0
	v_pk_fma_f32 v[82:83], v[222:223], v[64:65], v[82:83] op_sel_hi:[0,1,1]
	v_mov_b32_e32 v84, v223
	v_pk_fma_f32 v[82:83], v[84:85], v[60:61], v[82:83] op_sel_hi:[0,1,1]
	s_waitcnt lgkmcnt(7)
	v_pk_fma_f32 v[88:89], v[66:67], v[224:225], v[90:91] op_sel_hi:[1,0,1]
	s_nop 0
	v_pk_fma_f32 v[84:85], v[224:225], v[62:63], v[88:89] op_sel:[1,0,0]
	s_nop 0
	v_pk_fma_f32 v[84:85], v[226:227], v[64:65], v[84:85] op_sel_hi:[0,1,1]
	v_mov_b32_e32 v86, v227
	v_pk_fma_f32 v[84:85], v[86:87], v[60:61], v[84:85] op_sel_hi:[0,1,1]
	s_waitcnt lgkmcnt(6)
	v_pk_fma_f32 v[90:91], v[66:67], v[228:229], v[92:93] op_sel_hi:[1,0,1]
	s_nop 0
	v_pk_fma_f32 v[86:87], v[228:229], v[62:63], v[90:91] op_sel:[1,0,0]
	s_nop 0
	v_pk_fma_f32 v[86:87], v[230:231], v[64:65], v[86:87] op_sel_hi:[0,1,1]
	v_mov_b32_e32 v88, v231
	v_pk_fma_f32 v[86:87], v[88:89], v[60:61], v[86:87] op_sel_hi:[0,1,1]
	s_waitcnt lgkmcnt(5)
	v_pk_fma_f32 v[92:93], v[66:67], v[232:233], v[94:95] op_sel_hi:[1,0,1]
	s_nop 0
	v_pk_fma_f32 v[88:89], v[232:233], v[62:63], v[92:93] op_sel:[1,0,0]
	s_nop 0
	v_pk_fma_f32 v[88:89], v[234:235], v[64:65], v[88:89] op_sel_hi:[0,1,1]
	v_mov_b32_e32 v90, v235
	v_pk_fma_f32 v[88:89], v[90:91], v[60:61], v[88:89] op_sel_hi:[0,1,1]
	s_waitcnt lgkmcnt(4)
	v_pk_fma_f32 v[94:95], v[66:67], v[242:243], v[96:97] op_sel_hi:[1,0,1]
	s_nop 0
	v_pk_fma_f32 v[90:91], v[242:243], v[62:63], v[94:95] op_sel:[1,0,0]
	s_nop 0
	v_pk_fma_f32 v[90:91], v[244:245], v[64:65], v[90:91] op_sel_hi:[0,1,1]
	v_mov_b32_e32 v92, v245
	v_pk_fma_f32 v[90:91], v[92:93], v[60:61], v[90:91] op_sel_hi:[0,1,1]
	s_waitcnt lgkmcnt(3)
	v_pk_fma_f32 v[96:97], v[66:67], v[246:247], v[98:99] op_sel_hi:[1,0,1]
	s_nop 0
	v_pk_fma_f32 v[92:93], v[246:247], v[62:63], v[96:97] op_sel:[1,0,0]
	s_nop 0
	v_pk_fma_f32 v[92:93], v[248:249], v[64:65], v[92:93] op_sel_hi:[0,1,1]
	v_mov_b32_e32 v94, v249
	v_pk_fma_f32 v[92:93], v[94:95], v[60:61], v[92:93] op_sel_hi:[0,1,1]
	s_waitcnt lgkmcnt(2)
; #define WS_STEP(ctrl) v += __int_as_float(__builtin_amdgcn_update_dpp(0, __float_as_int(v), (ctrl), 0xf, 0xf, true))
; __device__ __forceinline__ float wave_sum(float v) {
;     ...
;     WS_STEP(0xB1); WS_STEP(0x4E); WS_STEP(0x124); WS_STEP(0x128);
;     ...
;     const auto r16 = __builtin_amdgcn_permlane16_swap(__float_as_uint(v), __float_as_uint(v), false, false);
;     v = __uint_as_float(r16[0]) + __uint_as_float(r16[1]);
;     const auto rr = __builtin_amdgcn_permlane32_swap(__float_as_uint(v), __float_as_uint(v), false, false);
;     return __uint_as_float(rr[0]) + __uint_as_float(rr[1]);
; }
	v_pk_fma_f32 v[98:99], v[66:67], v[250:251], v[100:101] op_sel_hi:[1,0,1]
	s_nop 0
	v_pk_fma_f32 v[94:95], v[250:251], v[62:63], v[98:99] op_sel:[1,0,0]
	s_nop 0
	v_pk_fma_f32 v[94:95], v[252:253], v[64:65], v[94:95] op_sel_hi:[0,1,1]
	v_mov_b32_e32 v96, v253
	v_pk_fma_f32 v[94:95], v[96:97], v[60:61], v[94:95] op_sel_hi:[0,1,1]
	s_waitcnt lgkmcnt(1)
	v_pk_fma_f32 v[100:101], v[66:67], v[162:163], v[102:103] op_sel_hi:[1,0,1]
	s_nop 0
	v_pk_fma_f32 v[96:97], v[162:163], v[62:63], v[100:101] op_sel:[1,0,0]
	s_nop 0
	v_pk_fma_f32 v[96:97], v[164:165], v[64:65], v[96:97] op_sel_hi:[0,1,1]
	v_mov_b32_e32 v98, v165
	v_pk_fma_f32 v[96:97], v[98:99], v[60:61], v[96:97] op_sel_hi:[0,1,1]
	s_waitcnt lgkmcnt(0)
	v_pk_fma_f32 v[66:67], v[66:67], v[166:167], v[104:105] op_sel_hi:[1,0,1]
	s_nop 0
	v_pk_fma_f32 v[62:63], v[166:167], v[62:63], v[66:67] op_sel:[1,0,0]
	s_nop 0
	v_pk_fma_f32 v[62:63], v[168:169], v[64:65], v[62:63] op_sel_hi:[0,1,1]
	v_mov_b32_e32 v64, v169
	v_pk_fma_f32 v[60:61], v[64:65], v[60:61], v[62:63] op_sel_hi:[0,1,1]
	s_nop 1
	v_permlane32_swap_b32_e32 v60, v61
	v_permlane32_swap_b32_e32 v68, v69
	v_permlane32_swap_b32_e32 v70, v71
	v_permlane32_swap_b32_e32 v72, v73
	v_permlane32_swap_b32_e32 v74, v75
	v_permlane32_swap_b32_e32 v76, v77
	v_permlane32_swap_b32_e32 v78, v79
	v_permlane32_swap_b32_e32 v80, v81
	v_permlane32_swap_b32_e32 v82, v83
	v_permlane32_swap_b32_e32 v84, v85
	v_permlane32_swap_b32_e32 v86, v87
	v_permlane32_swap_b32_e32 v88, v89
	v_permlane32_swap_b32_e32 v90, v91
	v_permlane32_swap_b32_e32 v92, v93
	v_permlane32_swap_b32_e32 v94, v95
	v_permlane32_swap_b32_e32 v96, v97
	v_add_f32_e32 v60, v60, v61
	v_add_f32_e32 v68, v68, v69
	v_add_f32_e32 v70, v70, v71
	v_add_f32_e32 v72, v72, v73
	v_add_f32_e32 v74, v74, v75
	v_add_f32_e32 v76, v76, v77
	v_add_f32_e32 v78, v78, v79
	v_add_f32_e32 v80, v80, v81
	v_add_f32_e32 v82, v82, v83
	v_add_f32_e32 v84, v84, v85
	v_add_f32_e32 v86, v86, v87
	v_add_f32_e32 v88, v88, v89
	v_add_f32_e32 v90, v90, v91
	v_add_f32_e32 v92, v92, v93
	v_add_f32_e32 v94, v94, v95
	v_add_f32_e32 v96, v96, v97
	s_nop 1
	v_add_f32_dpp v62, v68, v68 quad_perm:[1,0,3,2] row_mask:0xf bank_mask:0xf bound_ctrl:1
	s_nop 0
	v_add_f32_dpp v60, v60, v60 quad_perm:[1,0,3,2] row_mask:0xf bank_mask:0xf bound_ctrl:1
	v_add_f32_dpp v68, v94, v94 quad_perm:[1,0,3,2] row_mask:0xf bank_mask:0xf bound_ctrl:1
	v_add_f32_dpp v62, v62, v62 quad_perm:[2,3,0,1] row_mask:0xf bank_mask:0xf bound_ctrl:1
	v_add_f32_dpp v60, v60, v60 quad_perm:[2,3,0,1] row_mask:0xf bank_mask:0xf bound_ctrl:1
	v_add_f32_dpp v68, v68, v68 quad_perm:[2,3,0,1] row_mask:0xf bank_mask:0xf bound_ctrl:1
	v_add_f32_dpp v62, v62, v62 row_ror:4 row_mask:0xf bank_mask:0xf bound_ctrl:1
	v_add_f32_dpp v60, v60, v60 row_ror:4 row_mask:0xf bank_mask:0xf bound_ctrl:1
	v_add_f32_dpp v68, v68, v68 row_ror:4 row_mask:0xf bank_mask:0xf bound_ctrl:1
	v_add_f32_dpp v62, v62, v62 row_ror:8 row_mask:0xf bank_mask:0xf bound_ctrl:1
	v_mov_b32_e32 v63, v62
	s_nop 1
	v_permlane16_swap_b32_e32 v62, v63
	v_add_f32_e32 v62, v62, v63
	v_mov_b32_e32 v63, v62
	s_nop 1
	s_nop 0
	v_mov_b32_e32 v62, v62
	s_nop 0
	v_add_f32_dpp v63, v70, v70 quad_perm:[1,0,3,2] row_mask:0xf bank_mask:0xf bound_ctrl:1
	v_mul_f32_e32 v62, 0xbfb8aa3b, v62
	v_exp_f32_e32 v62, v62
	v_add_f32_dpp v63, v63, v63 quad_perm:[2,3,0,1] row_mask:0xf bank_mask:0xf bound_ctrl:1
	v_add_f32_dpp v60, v60, v60 row_ror:8 row_mask:0xf bank_mask:0xf bound_ctrl:1
	v_add_f32_dpp v68, v68, v68 row_ror:8 row_mask:0xf bank_mask:0xf bound_ctrl:1
	v_add_f32_dpp v63, v63, v63 row_ror:4 row_mask:0xf bank_mask:0xf bound_ctrl:1
	v_add_f32_e32 v62, 1.0, v62
	v_rcp_f32_e32 v62, v62
	v_add_f32_dpp v63, v63, v63 row_ror:8 row_mask:0xf bank_mask:0xf bound_ctrl:1
	v_mov_b32_e32 v64, v63
	s_nop 1
	v_permlane16_swap_b32_e32 v63, v64
	v_add_f32_e32 v63, v63, v64
	v_mov_b32_e32 v64, v63
	s_nop 1
	s_nop 0
	v_mov_b32_e32 v63, v63
	s_nop 0
	v_add_f32_dpp v64, v72, v72 quad_perm:[1,0,3,2] row_mask:0xf bank_mask:0xf bound_ctrl:1
	v_mul_f32_e32 v63, 0xbfb8aa3b, v63
	v_exp_f32_e32 v63, v63
	v_add_f32_dpp v64, v64, v64 quad_perm:[2,3,0,1] row_mask:0xf bank_mask:0xf bound_ctrl:1
	v_add_f32_dpp v72, v96, v96 quad_perm:[1,0,3,2] row_mask:0xf bank_mask:0xf bound_ctrl:1
	v_mov_b32_e32 v70, v68
	v_add_f32_dpp v64, v64, v64 row_ror:4 row_mask:0xf bank_mask:0xf bound_ctrl:1
	v_add_f32_e32 v63, 1.0, v63
	v_rcp_f32_e32 v63, v63
	v_add_f32_dpp v64, v64, v64 row_ror:8 row_mask:0xf bank_mask:0xf bound_ctrl:1
	v_mov_b32_e32 v65, v64
	s_nop 1
	v_permlane16_swap_b32_e32 v64, v65
	v_add_f32_e32 v64, v64, v65
	v_mov_b32_e32 v65, v64
	s_nop 1
	s_nop 0
	v_mov_b32_e32 v64, v64
	s_nop 0
	v_add_f32_dpp v65, v76, v76 quad_perm:[1,0,3,2] row_mask:0xf bank_mask:0xf bound_ctrl:1
	v_mul_f32_e32 v64, 0xbfb8aa3b, v64
	v_exp_f32_e32 v64, v64
	v_add_f32_dpp v65, v65, v65 quad_perm:[2,3,0,1] row_mask:0xf bank_mask:0xf bound_ctrl:1
	v_mov_b32_e32 v76, v60
	s_nop 1
	v_permlane16_swap_b32_e32 v60, v76
	v_add_f32_dpp v65, v65, v65 row_ror:4 row_mask:0xf bank_mask:0xf bound_ctrl:1
	v_add_f32_e32 v64, 1.0, v64
	v_rcp_f32_e32 v102, v64
	v_add_f32_dpp v65, v65, v65 row_ror:8 row_mask:0xf bank_mask:0xf bound_ctrl:1
	v_mov_b32_e32 v66, v65
	s_nop 1
	v_permlane16_swap_b32_e32 v65, v66
	v_add_f32_e32 v65, v65, v66
	v_mov_b32_e32 v66, v65
	s_nop 1
	s_nop 0
	v_mov_b32_e32 v65, v65
	s_nop 0
	v_add_f32_dpp v66, v74, v74 quad_perm:[1,0,3,2] row_mask:0xf bank_mask:0xf bound_ctrl:1
	v_mul_f32_e32 v65, 0xbfb8aa3b, v65
	v_exp_f32_e32 v65, v65
	v_add_f32_dpp v66, v66, v66 quad_perm:[2,3,0,1] row_mask:0xf bank_mask:0xf bound_ctrl:1
	v_add_f32_e32 v111, v14, v102
	v_add_f32_e32 v76, v60, v76
	v_add_f32_dpp v66, v66, v66 row_ror:4 row_mask:0xf bank_mask:0xf bound_ctrl:1
	v_add_f32_e32 v64, 1.0, v65
	v_rcp_f32_e32 v104, v64
	v_add_f32_dpp v66, v66, v66 row_ror:8 row_mask:0xf bank_mask:0xf bound_ctrl:1
	v_mov_b32_e32 v67, v66
	s_nop 1
	v_permlane16_swap_b32_e32 v66, v67
	v_add_f32_e32 v101, v66, v67
	s_nop 0
	v_add_f32_dpp v66, v78, v78 quad_perm:[1,0,3,2] row_mask:0xf bank_mask:0xf bound_ctrl:1
	v_pk_add_f32 v[64:65], v[12:13], v[62:63]
	v_add_f32_e32 v112, v15, v104
	v_add_f32_dpp v66, v66, v66 quad_perm:[2,3,0,1] row_mask:0xf bank_mask:0xf bound_ctrl:1
	v_cmp_gt_f32_e32 vcc, v65, v64
	v_add_f32_dpp v72, v72, v72 quad_perm:[2,3,0,1] row_mask:0xf bank_mask:0xf bound_ctrl:1
	v_add_f32_dpp v66, v66, v66 row_ror:4 row_mask:0xf bank_mask:0xf bound_ctrl:1
	v_cndmask_b32_e32 v60, v64, v65, vcc
	v_cmp_gt_f32_e64 s[6:7], v111, v60
	v_add_f32_dpp v66, v66, v66 row_ror:8 row_mask:0xf bank_mask:0xf bound_ctrl:1
	v_mov_b32_e32 v67, v66
	s_nop 1
	v_permlane16_swap_b32_e32 v66, v67
	v_add_f32_e32 v105, v66, v67
	s_nop 0
	v_add_f32_dpp v66, v80, v80 quad_perm:[1,0,3,2] row_mask:0xf bank_mask:0xf bound_ctrl:1
	v_cndmask_b32_e64 v80, 0, 1, vcc
	v_cndmask_b32_e64 v60, v60, v111, s[6:7]
	v_add_f32_dpp v66, v66, v66 quad_perm:[2,3,0,1] row_mask:0xf bank_mask:0xf bound_ctrl:1
	v_cndmask_b32_e64 v80, v80, 2, s[6:7]
	v_cmp_ngt_f32_e64 s[8:9], v112, v60
	v_add_f32_dpp v66, v66, v66 row_ror:4 row_mask:0xf bank_mask:0xf bound_ctrl:1
	v_add_f32_dpp v72, v72, v72 row_ror:4 row_mask:0xf bank_mask:0xf bound_ctrl:1
	v_permlane16_swap_b32_e32 v68, v70
	v_add_f32_dpp v66, v66, v66 row_ror:8 row_mask:0xf bank_mask:0xf bound_ctrl:1
	v_mov_b32_e32 v67, v66
	s_nop 1
	v_permlane16_swap_b32_e32 v66, v67
	v_add_f32_e32 v107, v66, v67
	s_nop 0
	v_add_f32_dpp v66, v82, v82 quad_perm:[1,0,3,2] row_mask:0xf bank_mask:0xf bound_ctrl:1
	v_add_f32_dpp v72, v72, v72 row_ror:8 row_mask:0xf bank_mask:0xf bound_ctrl:1
	v_mov_b32_e32 v74, v72
	v_add_f32_dpp v66, v66, v66 quad_perm:[2,3,0,1] row_mask:0xf bank_mask:0xf bound_ctrl:1
	s_nop 0
	v_permlane16_swap_b32_e32 v72, v74
	v_add_f32_dpp v66, v66, v66 row_ror:4 row_mask:0xf bank_mask:0xf bound_ctrl:1
	v_add_f32_e32 v68, v68, v70
	v_add_f32_e32 v72, v72, v74
	v_add_f32_dpp v66, v66, v66 row_ror:8 row_mask:0xf bank_mask:0xf bound_ctrl:1
	v_mov_b32_e32 v67, v66
	s_nop 1
	v_permlane16_swap_b32_e32 v66, v67
	v_add_f32_e32 v109, v66, v67
	s_nop 0
	v_add_f32_dpp v66, v84, v84 quad_perm:[1,0,3,2] row_mask:0xf bank_mask:0xf bound_ctrl:1
	v_cndmask_b32_e64 v94, v112, v60, s[8:9]
	v_mov_b32_e32 v103, v101
	v_add_f32_dpp v66, v66, v66 quad_perm:[2,3,0,1] row_mask:0xf bank_mask:0xf bound_ctrl:1
	v_mov_b32_e32 v106, v105
	v_mov_b32_e32 v108, v107
	v_add_f32_dpp v66, v66, v66 row_ror:4 row_mask:0xf bank_mask:0xf bound_ctrl:1
	v_mov_b32_e32 v110, v109
	v_mov_b32_e32 v70, v68
	v_add_f32_dpp v66, v66, v66 row_ror:8 row_mask:0xf bank_mask:0xf bound_ctrl:1
	v_mov_b32_e32 v67, v66
	s_nop 1
	v_permlane16_swap_b32_e32 v66, v67
	v_add_f32_e32 v82, v66, v67
	s_nop 0
	v_add_f32_dpp v66, v86, v86 quad_perm:[1,0,3,2] row_mask:0xf bank_mask:0xf bound_ctrl:1
	v_mov_b32_e32 v84, v82
	v_mov_b32_e32 v74, v72
	v_add_f32_dpp v66, v66, v66 quad_perm:[2,3,0,1] row_mask:0xf bank_mask:0xf bound_ctrl:1
	v_mov_b32_e32 v78, v76
	s_nop 0
	v_add_f32_dpp v66, v66, v66 row_ror:4 row_mask:0xf bank_mask:0xf bound_ctrl:1
	s_nop 0
	s_nop 0
	v_add_f32_dpp v66, v66, v66 row_ror:8 row_mask:0xf bank_mask:0xf bound_ctrl:1
	v_mov_b32_e32 v67, v66
	s_nop 1
	v_permlane16_swap_b32_e32 v66, v67
	v_add_f32_e32 v86, v66, v67
	s_nop 0
	v_add_f32_dpp v66, v88, v88 quad_perm:[1,0,3,2] row_mask:0xf bank_mask:0xf bound_ctrl:1
	v_mov_b32_e32 v98, v86
	s_nop 0
	v_add_f32_dpp v66, v66, v66 quad_perm:[2,3,0,1] row_mask:0xf bank_mask:0xf bound_ctrl:1
	s_nop 0
	s_nop 0
	v_add_f32_dpp v66, v66, v66 row_ror:4 row_mask:0xf bank_mask:0xf bound_ctrl:1
	s_nop 0
	s_nop 0
	v_add_f32_dpp v66, v66, v66 row_ror:8 row_mask:0xf bank_mask:0xf bound_ctrl:1
	v_mov_b32_e32 v67, v66
	s_nop 1
	v_permlane16_swap_b32_e32 v66, v67
	v_add_f32_e32 v88, v66, v67
	s_nop 0
	v_add_f32_dpp v66, v90, v90 quad_perm:[1,0,3,2] row_mask:0xf bank_mask:0xf bound_ctrl:1
	v_mov_b32_e32 v99, v88
	s_nop 0
	v_add_f32_dpp v66, v66, v66 quad_perm:[2,3,0,1] row_mask:0xf bank_mask:0xf bound_ctrl:1
	s_nop 0
	s_nop 0
	v_add_f32_dpp v66, v66, v66 row_ror:4 row_mask:0xf bank_mask:0xf bound_ctrl:1
	s_nop 0
	s_nop 0
	v_add_f32_dpp v66, v66, v66 row_ror:8 row_mask:0xf bank_mask:0xf bound_ctrl:1
	v_mov_b32_e32 v67, v66
	s_nop 1
	v_permlane16_swap_b32_e32 v66, v67
	v_add_f32_e32 v90, v66, v67
	s_nop 0
	v_add_f32_dpp v66, v92, v92 quad_perm:[1,0,3,2] row_mask:0xf bank_mask:0xf bound_ctrl:1
	v_cndmask_b32_e64 v92, 3, v80, s[8:9]
	v_mov_b32_e32 v80, 0xff800000
	v_cmp_eq_u32_e64 s[10:11], 0, v92
	v_cmp_nlg_f32_e64 s[12:13], v64, v80
	s_or_b64 s[10:11], s[10:11], s[12:13]
	v_cndmask_b32_e64 v64, v64, v80, s[10:11]
	v_cmp_ne_u32_e64 s[12:13], 1, v92
	v_cmp_gt_f32_e64 s[14:15], v65, v64
	s_and_b64 s[12:13], s[12:13], s[14:15]
	v_cndmask_b32_e64 v64, v64, v65, s[12:13]
	v_add_f32_dpp v66, v66, v66 quad_perm:[2,3,0,1] row_mask:0xf bank_mask:0xf bound_ctrl:1
	v_cmp_ne_u32_e64 s[14:15], 2, v92
	v_cmp_gt_f32_e64 s[16:17], v111, v64
	v_add_f32_dpp v66, v66, v66 row_ror:4 row_mask:0xf bank_mask:0xf bound_ctrl:1
	s_and_b64 s[14:15], s[14:15], s[16:17]
	v_cndmask_b32_e64 v64, v64, v111, s[14:15]
	v_add_f32_dpp v66, v66, v66 row_ror:8 row_mask:0xf bank_mask:0xf bound_ctrl:1
	v_mov_b32_e32 v67, v66
	v_cmp_gt_f32_e64 s[16:17], v112, v64
	s_nop 0
	v_permlane16_swap_b32_e32 v66, v67
	s_and_b64 s[16:17], s[8:9], s[16:17]
	v_add_f32_e32 v66, v66, v67
	v_cndmask_b32_e64 v64, v64, v112, s[16:17]
	v_mov_b32_e32 v100, v90
	v_mov_b32_e32 v67, v66
	v_add_f32_e32 v94, v94, v64
	s_nop 0
	s_nop 0
	s_nop 0
	s_nop 0
	v_mov_b32_e32 v60, 1
	v_cmp_lg_f32_e64 s[18:19], v94, v80
	v_mov_b32_e32 v65, 0
	v_mov_b32_e32 v64, 0
	s_and_saveexec_b64 s[46:47], s[18:19]
	s_cbranch_execz .LBB0_891
	v_cndmask_b32_e64 v35, 0, 1, s[12:13]
	v_cndmask_b32_e64 v35, v35, 2, s[14:15]
	v_cndmask_b32_e64 v60, v35, 3, s[16:17]
	v_cndmask_b32_e64 v35, v62, 0, s[10:11]
	v_cndmask_b32_e64 v35, v35, v63, s[12:13]
	v_cndmask_b32_e32 v62, v62, v63, vcc
	v_cndmask_b32_e64 v35, v35, v102, s[14:15]
	v_cndmask_b32_e64 v62, v62, v102, s[6:7]
	v_cndmask_b32_e64 v35, v35, v104, s[16:17]
	v_cndmask_b32_e64 v65, v104, v62, s[8:9]
	v_mov_b32_e32 v64, v92
	v_mov_b32_e32 v80, v94
.LBB0_891:
	s_or_b64 exec, exec, s[46:47]
	v_mov_b32_e32 v62, v101
	v_mov_b32_e32 v63, v105
	v_mul_f32_e32 v62, 0xbfb8aa3b, v62
	v_mul_f32_e32 v63, 0xbfb8aa3b, v63
	v_exp_f32_e32 v62, v62
	v_exp_f32_e32 v63, v63
	v_mov_b32_e32 v92, v107
	v_mul_f32_e32 v92, 0xbfb8aa3b, v92
	v_exp_f32_e32 v92, v92
	v_mov_b32_e32 v94, v109
	v_mul_f32_e32 v94, 0xbfb8aa3b, v94
	v_add_f32_e32 v62, 1.0, v62
	v_add_f32_e32 v63, 1.0, v63
	v_exp_f32_e32 v94, v94
	v_rcp_f32_e32 v62, v62
	v_rcp_f32_e32 v63, v63
	v_add_f32_e32 v92, 1.0, v92
	v_rcp_f32_e32 v92, v92
	v_add_f32_e32 v94, 1.0, v94
	v_rcp_f32_e32 v94, v94
	v_add_f32_e32 v101, v8, v62
	v_add_f32_e32 v102, v9, v63
	v_cmp_gt_f32_e32 vcc, v102, v101
	v_add_f32_e32 v103, v10, v92
	v_add_f32_e32 v104, v11, v94
	v_cndmask_b32_e32 v96, v101, v102, vcc
	v_cmp_gt_f32_e64 s[6:7], v103, v96
	v_cndmask_b32_e64 v105, 0, 1, vcc
	v_cmp_nlg_f32_e64 s[12:13], s89, v101
	v_cndmask_b32_e64 v96, v96, v103, s[6:7]
	v_cndmask_b32_e64 v105, v105, 2, s[6:7]
	v_cmp_ngt_f32_e64 s[8:9], v104, v96
	s_nop 1
	v_cndmask_b32_e64 v106, v104, v96, s[8:9]
	v_cndmask_b32_e64 v96, 3, v105, s[8:9]
	v_cmp_eq_u32_e64 s[10:11], 0, v96
	s_or_b64 s[10:11], s[10:11], s[12:13]
	v_cmp_ne_u32_e64 s[12:13], 1, v96
	v_cndmask_b32_e64 v101, v101, v210, s[10:11]
	v_cmp_gt_f32_e64 s[14:15], v102, v101
	s_and_b64 s[12:13], s[12:13], s[14:15]
	v_cndmask_b32_e64 v101, v101, v102, s[12:13]
	v_cmp_ne_u32_e64 s[14:15], 2, v96
	v_cmp_gt_f32_e64 s[16:17], v103, v101
	s_and_b64 s[14:15], s[14:15], s[16:17]
	v_cndmask_b32_e64 v101, v101, v103, s[14:15]
	v_cmp_gt_f32_e64 s[16:17], v104, v101
	s_and_b64 s[16:17], s[8:9], s[16:17]
	s_nop 0
	v_cndmask_b32_e64 v101, v101, v104, s[16:17]
	v_add_f32_e32 v101, v106, v101
	v_cmp_gt_f32_e64 s[18:19], v101, v80
	s_and_saveexec_b64 s[46:47], s[18:19]
	s_cbranch_execz .LBB0_893
	v_cndmask_b32_e64 v35, 0, 1, s[12:13]
	v_or_b32_e32 v35, 4, v35
	v_cndmask_b32_e64 v35, v35, 6, s[14:15]
	v_cndmask_b32_e64 v60, v35, 7, s[16:17]
	v_cndmask_b32_e64 v35, v62, 0, s[10:11]
	v_cndmask_b32_e64 v35, v35, v63, s[12:13]
	v_cndmask_b32_e32 v62, v62, v63, vcc
	v_cndmask_b32_e64 v35, v35, v92, s[14:15]
	v_cndmask_b32_e64 v62, v62, v92, s[6:7]
	v_or_b32_e32 v64, 4, v96
	v_cndmask_b32_e64 v35, v35, v94, s[16:17]
	v_cndmask_b32_e64 v65, v94, v62, s[8:9]
	v_mov_b32_e32 v80, v101
.LBB0_893:
	s_or_b64 exec, exec, s[46:47]
	v_mov_b32_e32 v62, v82
	v_mov_b32_e32 v63, v86
	v_mul_f32_e32 v62, 0xbfb8aa3b, v62
	v_mul_f32_e32 v63, 0xbfb8aa3b, v63
	v_exp_f32_e32 v62, v62
	v_exp_f32_e32 v63, v63
	v_mov_b32_e32 v82, v88
	v_mul_f32_e32 v82, 0xbfb8aa3b, v82
	v_exp_f32_e32 v82, v82
	v_mov_b32_e32 v84, v90
	v_mul_f32_e32 v84, 0xbfb8aa3b, v84
	v_add_f32_e32 v62, 1.0, v62
	v_add_f32_e32 v63, 1.0, v63
	v_exp_f32_e32 v84, v84
	v_rcp_f32_e32 v62, v62
	v_rcp_f32_e32 v63, v63
	v_add_f32_e32 v82, 1.0, v82
	v_rcp_f32_e32 v82, v82
	v_add_f32_e32 v84, 1.0, v84
	v_rcp_f32_e32 v84, v84
	v_add_f32_e32 v88, v4, v62
	v_add_f32_e32 v90, v5, v63
	v_cmp_gt_f32_e32 vcc, v90, v88
	v_add_f32_e32 v92, v6, v82
	v_add_f32_e32 v94, v7, v84
	v_cndmask_b32_e32 v86, v88, v90, vcc
	v_cmp_gt_f32_e64 s[6:7], v92, v86
	v_cndmask_b32_e64 v96, 0, 1, vcc
	v_cmp_nlg_f32_e64 s[12:13], s89, v88
	v_cndmask_b32_e64 v86, v86, v92, s[6:7]
	v_cndmask_b32_e64 v96, v96, 2, s[6:7]
	v_cmp_ngt_f32_e64 s[8:9], v94, v86
	s_nop 1
	v_cndmask_b32_e64 v98, v94, v86, s[8:9]
	v_cndmask_b32_e64 v86, 3, v96, s[8:9]
	v_cmp_eq_u32_e64 s[10:11], 0, v86
	s_or_b64 s[10:11], s[10:11], s[12:13]
	v_cmp_ne_u32_e64 s[12:13], 1, v86
	v_cndmask_b32_e64 v88, v88, v210, s[10:11]
	v_cmp_gt_f32_e64 s[14:15], v90, v88
	s_and_b64 s[12:13], s[12:13], s[14:15]
	v_cndmask_b32_e64 v88, v88, v90, s[12:13]
	v_cmp_ne_u32_e64 s[14:15], 2, v86
	v_cmp_gt_f32_e64 s[16:17], v92, v88
	s_and_b64 s[14:15], s[14:15], s[16:17]
	v_cndmask_b32_e64 v88, v88, v92, s[14:15]
	v_cmp_gt_f32_e64 s[16:17], v94, v88
	s_and_b64 s[16:17], s[8:9], s[16:17]
	s_nop 0
	v_cndmask_b32_e64 v88, v88, v94, s[16:17]
	v_add_f32_e32 v88, v98, v88
	v_cmp_gt_f32_e64 s[18:19], v88, v80
	s_and_saveexec_b64 s[46:47], s[18:19]
	s_cbranch_execz .LBB0_895
	v_cndmask_b32_e64 v35, 0, 1, s[12:13]
	v_or_b32_e32 v35, 8, v35
	v_cndmask_b32_e64 v35, v35, 10, s[14:15]
	v_cndmask_b32_e64 v60, v35, 11, s[16:17]
	v_cndmask_b32_e64 v35, v62, 0, s[10:11]
	v_cndmask_b32_e64 v35, v35, v63, s[12:13]
	v_cndmask_b32_e32 v62, v62, v63, vcc
	v_cndmask_b32_e64 v35, v35, v82, s[14:15]
	v_cndmask_b32_e64 v62, v62, v82, s[6:7]
	v_or_b32_e32 v64, 8, v86
	v_cndmask_b32_e64 v35, v35, v84, s[16:17]
	v_cndmask_b32_e64 v65, v84, v62, s[8:9]
	v_mov_b32_e32 v80, v88
.LBB0_895:
	s_or_b64 exec, exec, s[46:47]
	v_mov_b32_e32 v62, v66
	v_mov_b32_e32 v63, v68
	v_mul_f32_e32 v62, 0xbfb8aa3b, v62
	v_mul_f32_e32 v63, 0xbfb8aa3b, v63
	v_exp_f32_e32 v62, v62
	v_exp_f32_e32 v63, v63
	v_mov_b32_e32 v66, v72
	v_mul_f32_e32 v66, 0xbfb8aa3b, v66
	v_exp_f32_e32 v66, v66
	v_mov_b32_e32 v67, v76
	v_mul_f32_e32 v67, 0xbfb8aa3b, v67
	v_add_f32_e32 v62, 1.0, v62
	v_add_f32_e32 v63, 1.0, v63
	v_exp_f32_e32 v67, v67
	v_rcp_f32_e32 v62, v62
	v_rcp_f32_e32 v63, v63
	v_add_f32_e32 v66, 1.0, v66
	v_rcp_f32_e32 v66, v66
	v_add_f32_e32 v67, 1.0, v67
	v_rcp_f32_e32 v67, v67
	v_add_f32_e32 v70, v0, v62
	v_add_f32_e32 v72, v1, v63
	v_cmp_gt_f32_e32 vcc, v72, v70
	v_add_f32_e32 v74, v2, v66
	v_add_f32_e32 v76, v3, v67
	v_cndmask_b32_e32 v68, v70, v72, vcc
	v_cmp_gt_f32_e64 s[6:7], v74, v68
	v_cndmask_b32_e64 v78, 0, 1, vcc
	v_cmp_nlg_f32_e64 s[12:13], s89, v70
	v_cndmask_b32_e64 v68, v68, v74, s[6:7]
	v_cndmask_b32_e64 v78, v78, 2, s[6:7]
	v_cmp_ngt_f32_e64 s[8:9], v76, v68
	s_nop 1
	v_cndmask_b32_e64 v82, v76, v68, s[8:9]
	v_cndmask_b32_e64 v68, 3, v78, s[8:9]
	v_cmp_eq_u32_e64 s[10:11], 0, v68
	s_or_b64 s[10:11], s[10:11], s[12:13]
	v_cmp_ne_u32_e64 s[12:13], 1, v68
	v_cndmask_b32_e64 v70, v70, v210, s[10:11]
	v_cmp_gt_f32_e64 s[14:15], v72, v70
	s_and_b64 s[12:13], s[12:13], s[14:15]
	v_cndmask_b32_e64 v70, v70, v72, s[12:13]
	v_cmp_ne_u32_e64 s[14:15], 2, v68
	v_cmp_gt_f32_e64 s[16:17], v74, v70
	s_and_b64 s[14:15], s[14:15], s[16:17]
	v_cndmask_b32_e64 v70, v70, v74, s[14:15]
	v_cmp_gt_f32_e64 s[16:17], v76, v70
	s_and_b64 s[16:17], s[8:9], s[16:17]
	s_nop 0
	v_cndmask_b32_e64 v70, v70, v76, s[16:17]
	v_add_f32_e32 v70, v82, v70
	v_cmp_gt_f32_e64 s[18:19], v70, v80
	s_and_saveexec_b64 s[46:47], s[18:19]
	s_cbranch_execz .LBB0_897
	v_cndmask_b32_e64 v35, 0, 1, s[12:13]
	v_or_b32_e32 v35, 12, v35
	v_cndmask_b32_e64 v35, v35, 14, s[14:15]
	v_cndmask_b32_e64 v60, v35, 15, s[16:17]
	v_cndmask_b32_e64 v35, v62, 0, s[10:11]
	v_cndmask_b32_e64 v35, v35, v63, s[12:13]
	v_cndmask_b32_e32 v62, v62, v63, vcc
	v_cndmask_b32_e64 v35, v35, v66, s[14:15]
	v_cndmask_b32_e64 v62, v62, v66, s[6:7]
	v_or_b32_e32 v64, 12, v68
	v_cndmask_b32_e64 v35, v35, v67, s[16:17]
	v_cndmask_b32_e64 v65, v67, v62, s[8:9]
.LBB0_897:
	s_or_b64 exec, exec, s[46:47]
	s_mov_b64 s[6:7], exec
	s_mov_b32 exec_lo, 1
	s_mov_b32 exec_hi, 1
	s_cbranch_execz .LBB0_899
	v_add_f32_e32 v62, v35, v65
	v_div_scale_f32 v63, s[8:9], v62, v62, 1.0
	v_rcp_f32_e32 v66, v63
	v_div_scale_f32 v67, vcc, 1.0, v62, 1.0
	s_add_i32 s8, s49, s50
	v_fma_f32 v68, -v63, v66, 1.0
	v_fmac_f32_e32 v66, v68, v66
	v_mul_f32_e32 v68, v67, v66
	v_fma_f32 v70, -v63, v68, v67
	v_fmac_f32_e32 v68, v70, v66
	v_fma_f32 v63, -v63, v68, v67
	v_div_fmas_f32 v63, v63, v66, v68
	v_div_fixup_f32 v62, v63, v62, 1.0
	v_lshl_add_u32 v63, v64, 2, s23
	ds_add_rtn_u32 v63, v63, v206
	v_lshl_add_u32 v66, v60, 2, s23
	ds_add_rtn_u32 v66, v66, v206
	v_mbcnt_lo_u32_b32 v67, -1, 0
	v_mul_u32_u24_e32 v67, 6, v67
	v_add_u32_e32 v67, s8, v67
	v_mul_f32_e32 v35, v35, v62
	s_waitcnt lgkmcnt(0)
	ds_write2_b32 v67, v64, v63 offset1:1
	v_mul_f32_e32 v63, v65, v62
	ds_write2_b32 v67, v63, v60 offset0:2 offset1:3
	ds_write2_b32 v67, v66, v35 offset0:4 offset1:5
.LBB0_899:
	s_or_b64 exec, exec, s[6:7]
	s_waitcnt vmcnt(0)
	v_lshlrev_b32_e32 v80, 16, v58
	v_and_b32_e32 v81, 0xffff0000, v58
	v_lshlrev_b32_e32 v78, 16, v59
	v_and_b32_e32 v79, 0xffff0000, v59
	v_add_f32_e32 v35, v80, v81
	v_add_f32_e32 v58, v78, v79
	v_lshlrev_b32_e32 v62, 16, v56
	v_and_b32_e32 v63, 0xffff0000, v56
	v_lshlrev_b32_e32 v60, 16, v57
	v_and_b32_e32 v61, 0xffff0000, v57
	v_add_f32_e32 v35, v35, v58
	v_add_f32_e32 v56, v62, v63
	v_add_f32_e32 v57, v60, v61
	v_lshlrev_b32_e32 v68, 16, v54
	v_and_b32_e32 v69, 0xffff0000, v54
	v_lshlrev_b32_e32 v70, 16, v55
	v_and_b32_e32 v71, 0xffff0000, v55
	v_add_f32_e32 v35, 0, v35
	v_add_f32_e32 v56, v56, v57
	v_add_f32_e32 v54, v68, v69
	v_add_f32_e32 v55, v70, v71
	v_lshlrev_b32_e32 v72, 16, v52
	v_and_b32_e32 v73, 0xffff0000, v52
	v_lshlrev_b32_e32 v74, 16, v53
	v_and_b32_e32 v75, 0xffff0000, v53
	v_add_f32_e32 v35, v35, v56
	v_add_f32_e32 v54, v54, v55
	v_add_f32_e32 v52, v72, v73
	v_add_f32_e32 v53, v74, v75
	v_lshlrev_b32_e32 v64, 16, v50
	v_and_b32_e32 v65, 0xffff0000, v50
	v_lshlrev_b32_e32 v66, 16, v51
	v_and_b32_e32 v67, 0xffff0000, v51
	v_add_f32_e32 v35, v35, v54
	v_add_f32_e32 v52, v52, v53
	v_add_f32_e32 v50, v64, v65
	v_add_f32_e32 v51, v66, v67
	v_lshlrev_b32_e32 v56, 16, v48
	v_and_b32_e32 v57, 0xffff0000, v48
	v_lshlrev_b32_e32 v58, 16, v49
	v_and_b32_e32 v59, 0xffff0000, v49
	v_add_f32_e32 v35, v35, v52
	v_add_f32_e32 v50, v50, v51
	v_add_f32_e32 v48, v56, v57
	v_add_f32_e32 v49, v58, v59
	v_lshlrev_b32_e32 v52, 16, v46
	v_and_b32_e32 v53, 0xffff0000, v46
	v_lshlrev_b32_e32 v54, 16, v47
	v_and_b32_e32 v55, 0xffff0000, v47
	v_add_f32_e32 v35, v35, v50
	v_add_f32_e32 v48, v48, v49
	v_add_f32_e32 v46, v52, v53
	v_add_f32_e32 v47, v54, v55
	v_add_f32_e32 v35, v35, v48
	v_add_f32_e32 v46, v46, v47
	v_add_f32_e32 v35, v35, v46
	v_lshlrev_b32_e32 v46, 16, v44
	v_and_b32_e32 v47, 0xffff0000, v44
	v_lshlrev_b32_e32 v44, 16, v45
	v_and_b32_e32 v45, 0xffff0000, v45
	v_add_f32_e32 v48, v46, v47
	v_add_f32_e32 v49, v44, v45
	v_add_f32_e32 v48, v48, v49
	v_add_f32_e32 v35, v35, v48
	s_mov_b64 s[6:7], s[34:35]
	s_mov_b64 s[8:9], s[36:37]
	v_add_f32_dpp v35, v35, v35 quad_perm:[1,0,3,2] row_mask:0xf bank_mask:0xf bound_ctrl:1
	v_lshl_add_u64 v[92:93], s[6:7], 0, v[192:193]
	s_lshl_b64 s[6:7], s[38:39], 11
	v_add_f32_dpp v35, v35, v35 quad_perm:[2,3,0,1] row_mask:0xf bank_mask:0xf bound_ctrl:1
	v_lshl_add_u64 v[94:95], s[8:9], 0, v[192:193]
	v_add_co_u32_e32 v98, vcc, s33, v92
	v_add_f32_dpp v35, v35, v35 row_ror:4 row_mask:0xf bank_mask:0xf bound_ctrl:1
	s_nop 0
	v_addc_co_u32_e32 v99, vcc, 0, v93, vcc
	v_add_f32_dpp v35, v35, v35 row_ror:8 row_mask:0xf bank_mask:0xf bound_ctrl:1
	v_mov_b32_e32 v48, v35
	s_nop 1
	v_permlane16_swap_b32_e32 v35, v48
	v_add_f32_e32 v35, v35, v48
	v_mov_b32_e32 v48, v35
	s_nop 1
	v_permlane32_swap_b32_e32 v35, v48
	v_add_f32_e32 v35, v35, v48
	v_fmac_f32_e32 v79, 0xba000000, v35
	v_fmac_f32_e32 v81, 0xba000000, v35
	v_fmac_f32_e32 v78, 0xba000000, v35
	v_fmac_f32_e32 v80, 0xba000000, v35
	v_mul_f32_e32 v48, v81, v81
	v_mul_f32_e32 v49, v79, v79
	v_fmac_f32_e32 v48, v80, v80
	v_fmac_f32_e32 v49, v78, v78
	v_fmac_f32_e32 v61, 0xba000000, v35
	v_fmac_f32_e32 v63, 0xba000000, v35
	v_add_f32_e32 v48, v48, v49
	v_fmac_f32_e32 v60, 0xba000000, v35
	v_fmac_f32_e32 v62, 0xba000000, v35
	v_mul_f32_e32 v49, v63, v63
	v_mul_f32_e32 v50, v61, v61
	v_fmac_f32_e32 v49, v62, v62
	v_fmac_f32_e32 v50, v60, v60
	v_add_f32_e32 v49, v49, v50
	v_add_f32_e32 v76, v48, v49
	flat_load_dwordx4 v[48:51], v[92:93]
	flat_load_dwordx4 v[84:87], v[94:95]
	v_fmac_f32_e32 v71, 0xba000000, v35
	v_fmac_f32_e32 v69, 0xba000000, v35
	v_fmac_f32_e32 v70, 0xba000000, v35
	v_fmac_f32_e32 v68, 0xba000000, v35
	v_mul_f32_e32 v77, v69, v69
	v_mul_f32_e32 v82, v71, v71
	v_fmac_f32_e32 v77, v68, v68
	v_fmac_f32_e32 v82, v70, v70
	v_add_f32_e32 v77, v77, v82
	v_fmac_f32_e32 v75, 0xba000000, v35
	v_fmac_f32_e32 v73, 0xba000000, v35
	v_add_f32_e32 v76, v76, v77
	v_fmac_f32_e32 v74, 0xba000000, v35
	v_fmac_f32_e32 v72, 0xba000000, v35
	v_mul_f32_e32 v77, v73, v73
	v_mul_f32_e32 v82, v75, v75
	v_fmac_f32_e32 v77, v72, v72
	v_fmac_f32_e32 v82, v74, v74
	v_add_f32_e32 v77, v77, v82
	v_fmac_f32_e32 v67, 0xba000000, v35
	v_fmac_f32_e32 v65, 0xba000000, v35
	v_add_f32_e32 v76, v76, v77
	v_fmac_f32_e32 v66, 0xba000000, v35
	v_fmac_f32_e32 v64, 0xba000000, v35
	v_mul_f32_e32 v77, v65, v65
	v_mul_f32_e32 v82, v67, v67
	v_fmac_f32_e32 v77, v64, v64
	v_fmac_f32_e32 v82, v66, v66
	v_add_f32_e32 v77, v77, v82
	v_fmac_f32_e32 v59, 0xba000000, v35
	v_fmac_f32_e32 v57, 0xba000000, v35
	v_add_f32_e32 v76, v76, v77
	v_fmac_f32_e32 v58, 0xba000000, v35
	v_fmac_f32_e32 v56, 0xba000000, v35
	v_mul_f32_e32 v77, v57, v57
	v_mul_f32_e32 v82, v59, v59
	v_fmac_f32_e32 v77, v56, v56
	v_fmac_f32_e32 v82, v58, v58
	v_add_f32_e32 v77, v77, v82
	v_fmac_f32_e32 v55, 0xba000000, v35
	v_fmac_f32_e32 v53, 0xba000000, v35
	v_add_f32_e32 v76, v76, v77
	v_fmac_f32_e32 v54, 0xba000000, v35
	v_fmac_f32_e32 v52, 0xba000000, v35
	v_mul_f32_e32 v77, v53, v53
	v_mul_f32_e32 v82, v55, v55
	v_fmac_f32_e32 v77, v52, v52
	v_fmac_f32_e32 v82, v54, v54
	v_add_f32_e32 v77, v77, v82
	v_fmac_f32_e32 v45, 0xba000000, v35
	v_fmac_f32_e32 v47, 0xba000000, v35
	v_add_f32_e32 v76, v76, v77
	v_fmac_f32_e32 v44, 0xba000000, v35
	v_fmac_f32_e32 v46, 0xba000000, v35
	v_mul_f32_e32 v35, v47, v47
	v_mul_f32_e32 v77, v45, v45
	v_fmac_f32_e32 v35, v46, v46
	v_fmac_f32_e32 v77, v44, v44
	v_add_f32_e32 v35, v35, v77
	v_add_f32_e32 v35, v76, v35
	v_lshl_add_u64 v[82:83], v[30:31], 0, s[6:7]
	v_add_co_u32_e32 v100, vcc, s33, v94
	v_add_f32_dpp v35, v35, v35 quad_perm:[1,0,3,2] row_mask:0xf bank_mask:0xf bound_ctrl:1
	s_nop 0
	v_addc_co_u32_e32 v101, vcc, 0, v95, vcc
	v_add_f32_dpp v35, v35, v35 quad_perm:[2,3,0,1] row_mask:0xf bank_mask:0xf bound_ctrl:1
	s_nop 1
	v_add_f32_dpp v35, v35, v35 row_ror:4 row_mask:0xf bank_mask:0xf bound_ctrl:1
	s_nop 1
	v_add_f32_dpp v35, v35, v35 row_ror:8 row_mask:0xf bank_mask:0xf bound_ctrl:1
	v_mov_b32_e32 v76, v35
	s_nop 1
	v_permlane16_swap_b32_e32 v35, v76
	v_add_f32_e32 v35, v35, v76
	v_mov_b32_e32 v76, v35
	s_nop 1
	v_permlane32_swap_b32_e32 v35, v76
	v_add_f32_e32 v35, v35, v76
	v_fmamk_f32 v35, v35, 0x3a000000, v207
	v_rsq_f32_e32 v96, v35
	v_lshl_add_u64 v[76:77], v[28:29], 0, s[44:45]
	v_pk_mul_f32 v[80:81], v[96:97], v[80:81] op_sel_hi:[0,1]
	s_waitcnt vmcnt(0) lgkmcnt(0)
	v_pk_fma_f32 v[48:49], v[48:49], v[80:81], v[84:85]
	v_mov_b32_e32 v81, 0
	v_med3_f32 v35, v48, s69, v208
	v_med3_f32 v80, v49, s69, v208
	v_cvt_pk_fp8_f32 v81, v35, v80
	v_pk_mul_f32 v[78:79], v[96:97], v[78:79] op_sel_hi:[0,1]
	v_pk_fma_f32 v[50:51], v[50:51], v[78:79], v[86:87]
	v_pk_mul_f32 v[62:63], v[96:97], v[62:63] op_sel_hi:[0,1]
	v_med3_f32 v35, v50, s69, v208
	v_med3_f32 v78, v51, s69, v208
	v_cvt_pk_fp8_f32 v81, v35, v78 op_sel:[0,0,1]
	v_cvt_pk_bf16_f32 v78, v48, v49
	v_cvt_pk_bf16_f32 v79, v50, v51
	flat_store_dwordx2 v[76:77], v[78:79] nt
	flat_store_dword v[82:83], v81 nt
	flat_load_dwordx4 v[78:81], v[92:93] offset:1024
	s_nop 0
	flat_load_dwordx4 v[84:87], v[94:95] offset:1024
	v_pk_mul_f32 v[88:89], v[96:97], v[60:61] op_sel_hi:[0,1]
	v_pk_mul_f32 v[68:69], v[96:97], v[68:69] op_sel_hi:[0,1]
	v_pk_mul_f32 v[72:73], v[96:97], v[72:73] op_sel_hi:[0,1]
	v_pk_mul_f32 v[74:75], v[96:97], v[74:75] op_sel_hi:[0,1]
	v_pk_mul_f32 v[64:65], v[96:97], v[64:65] op_sel_hi:[0,1]
	v_pk_mul_f32 v[66:67], v[96:97], v[66:67] op_sel_hi:[0,1]
	v_pk_mul_f32 v[56:57], v[96:97], v[56:57] op_sel_hi:[0,1]
	v_pk_mul_f32 v[58:59], v[96:97], v[58:59] op_sel_hi:[0,1]
	v_pk_mul_f32 v[52:53], v[96:97], v[52:53] op_sel_hi:[0,1]
	v_pk_mul_f32 v[54:55], v[96:97], v[54:55] op_sel_hi:[0,1]
	v_pk_mul_f32 v[46:47], v[96:97], v[46:47] op_sel_hi:[0,1]
	v_pk_mul_f32 v[44:45], v[96:97], v[44:45] op_sel_hi:[0,1]
	s_waitcnt vmcnt(0) lgkmcnt(0)
	v_pk_fma_f32 v[60:61], v[78:79], v[62:63], v[84:85]
	s_nop 0
	v_med3_f32 v35, v60, s69, v208
	v_med3_f32 v62, v61, s69, v208
	v_mov_b32_e32 v84, 0
	v_cvt_pk_fp8_f32 v84, v35, v62
	v_pk_fma_f32 v[62:63], v[80:81], v[88:89], v[86:87]
	v_pk_mul_f32 v[88:89], v[96:97], v[70:71] op_sel_hi:[0,1]
	v_med3_f32 v35, v62, s69, v208
	v_med3_f32 v78, v63, s69, v208
	v_cvt_pk_fp8_f32 v84, v35, v78 op_sel:[0,0,1]
	v_cvt_pk_bf16_f32 v78, v60, v61
	v_cvt_pk_bf16_f32 v79, v62, v63
	flat_store_dwordx2 v[76:77], v[78:79] offset:512 nt
	flat_store_dword v[82:83], v84 offset:256 nt
	flat_load_dwordx4 v[78:81], v[92:93] offset:2048
	s_nop 0
	flat_load_dwordx4 v[84:87], v[94:95] offset:2048
	v_mov_b32_e32 v35, 0
	s_waitcnt vmcnt(0) lgkmcnt(0)
	v_pk_fma_f32 v[70:71], v[78:79], v[68:69], v[84:85]
	s_nop 0
	v_med3_f32 v68, v70, s69, v208
	v_med3_f32 v69, v71, s69, v208
	v_cvt_pk_fp8_f32 v35, v68, v69
	v_pk_fma_f32 v[68:69], v[80:81], v[88:89], v[86:87]
	s_nop 0
	v_med3_f32 v78, v68, s69, v208
	v_med3_f32 v79, v69, s69, v208
	v_cvt_pk_fp8_f32 v35, v78, v79 op_sel:[0,0,1]
	v_cvt_pk_bf16_f32 v78, v70, v71
	v_cvt_pk_bf16_f32 v79, v68, v69
	flat_store_dwordx2 v[76:77], v[78:79] offset:1024 nt
	flat_store_dword v[82:83], v35 offset:512 nt
	flat_load_dwordx4 v[84:87], v[92:93] offset:3072
	flat_load_dwordx4 v[88:91], v[94:95] offset:3072
	v_mov_b32_e32 v35, 0
	s_waitcnt vmcnt(0) lgkmcnt(0)
	v_pk_fma_f32 v[80:81], v[84:85], v[72:73], v[88:89]
	s_nop 0
	v_med3_f32 v72, v80, s69, v208
	v_med3_f32 v73, v81, s69, v208
	v_cvt_pk_fp8_f32 v35, v72, v73
	v_pk_fma_f32 v[78:79], v[86:87], v[74:75], v[90:91]
	s_nop 0
	v_med3_f32 v72, v78, s69, v208
	v_med3_f32 v73, v79, s69, v208
	v_cvt_pk_fp8_f32 v35, v72, v73 op_sel:[0,0,1]
	v_cvt_pk_bf16_f32 v72, v80, v81
	v_cvt_pk_bf16_f32 v73, v78, v79
	flat_store_dwordx2 v[76:77], v[72:73] offset:1536 nt
	flat_store_dword v[82:83], v35 offset:768 nt
	flat_load_dwordx4 v[72:75], v[98:99]
	s_nop 0
	flat_load_dwordx4 v[86:89], v[100:101]
	v_mov_b32_e32 v35, 0
	s_waitcnt vmcnt(0) lgkmcnt(0)
	v_pk_fma_f32 v[86:87], v[72:73], v[64:65], v[86:87]
	s_nop 0
	v_med3_f32 v64, v86, s69, v208
	v_med3_f32 v65, v87, s69, v208
	v_cvt_pk_fp8_f32 v35, v64, v65
	v_pk_fma_f32 v[84:85], v[74:75], v[66:67], v[88:89]
	s_nop 0
	v_med3_f32 v64, v84, s69, v208
	v_med3_f32 v65, v85, s69, v208
	v_cvt_pk_fp8_f32 v35, v64, v65 op_sel:[0,0,1]
	v_cvt_pk_bf16_f32 v64, v86, v87
	v_cvt_pk_bf16_f32 v65, v84, v85
	flat_store_dwordx2 v[76:77], v[64:65] offset:2048 nt
	flat_store_dword v[82:83], v35 offset:1024 nt
	flat_load_dwordx4 v[64:67], v[98:99] offset:1024
	s_nop 0
	flat_load_dwordx4 v[72:75], v[100:101] offset:1024
	v_mov_b32_e32 v35, 0
	s_waitcnt vmcnt(0) lgkmcnt(0)
	v_pk_fma_f32 v[90:91], v[64:65], v[56:57], v[72:73]
	s_nop 0
	v_med3_f32 v56, v90, s69, v208
	v_med3_f32 v57, v91, s69, v208
	v_cvt_pk_fp8_f32 v35, v56, v57
	v_pk_fma_f32 v[88:89], v[66:67], v[58:59], v[74:75]
	s_nop 0
	v_med3_f32 v56, v88, s69, v208
	v_med3_f32 v57, v89, s69, v208
	v_cvt_pk_fp8_f32 v35, v56, v57 op_sel:[0,0,1]
	v_cvt_pk_bf16_f32 v56, v90, v91
	v_cvt_pk_bf16_f32 v57, v88, v89
	flat_store_dwordx2 v[76:77], v[56:57] offset:2560 nt
	flat_store_dword v[82:83], v35 offset:1280 nt
	flat_load_dwordx4 v[56:59], v[98:99] offset:2048
	s_nop 0
	flat_load_dwordx4 v[64:67], v[100:101] offset:2048
	v_mov_b32_e32 v35, 0
	s_waitcnt vmcnt(0) lgkmcnt(0)
	v_pk_fma_f32 v[94:95], v[56:57], v[52:53], v[64:65]
	s_nop 0
	v_med3_f32 v52, v94, s69, v208
	v_med3_f32 v53, v95, s69, v208
	v_cvt_pk_fp8_f32 v35, v52, v53
	v_pk_fma_f32 v[92:93], v[58:59], v[54:55], v[66:67]
	s_nop 0
	v_med3_f32 v52, v92, s69, v208
	v_med3_f32 v53, v93, s69, v208
	v_cvt_pk_fp8_f32 v35, v52, v53 op_sel:[0,0,1]
	v_cvt_pk_bf16_f32 v52, v94, v95
	v_cvt_pk_bf16_f32 v53, v92, v93
	flat_store_dwordx2 v[76:77], v[52:53] offset:3072 nt
	flat_store_dword v[82:83], v35 offset:1536 nt
	flat_load_dwordx4 v[52:55], v[98:99] offset:3072
	s_nop 0
	flat_load_dwordx4 v[56:59], v[100:101] offset:3072
	v_mov_b32_e32 v35, 0
	s_waitcnt vmcnt(0) lgkmcnt(0)
	v_pk_fma_f32 v[96:97], v[52:53], v[46:47], v[56:57]
	s_nop 0
	v_med3_f32 v46, v96, s69, v208
	v_med3_f32 v47, v97, s69, v208
	v_mov_b32_e32 v52, 0
	v_cvt_pk_fp8_f32 v52, v46, v47
	v_pk_fma_f32 v[98:99], v[54:55], v[44:45], v[58:59]
	s_nop 0
	v_med3_f32 v44, v98, s69, v208
	v_med3_f32 v45, v99, s69, v208
	v_cvt_pk_fp8_f32 v52, v44, v45 op_sel:[0,0,1]
	v_cvt_pk_bf16_f32 v44, v96, v97
	v_cvt_pk_bf16_f32 v45, v98, v99
	flat_store_dwordx2 v[76:77], v[44:45] offset:3584 nt
	flat_store_dword v[82:83], v52 offset:1792 nt
	v_lshlrev_b32_e32 v102, 16, v42
	v_and_b32_e32 v103, 0xffff0000, v42
	v_lshlrev_b32_e32 v100, 16, v43
	v_and_b32_e32 v101, 0xffff0000, v43
	v_add_f32_e32 v42, v102, v103
	v_add_f32_e32 v43, v100, v101
	v_lshlrev_b32_e32 v74, 16, v40
	v_and_b32_e32 v75, 0xffff0000, v40
	v_lshlrev_b32_e32 v72, 16, v41
	v_and_b32_e32 v73, 0xffff0000, v41
	v_add_f32_e32 v42, v42, v43
	v_add_f32_e32 v40, v74, v75
	v_add_f32_e32 v41, v72, v73
	v_lshlrev_b32_e32 v64, 16, v38
	v_and_b32_e32 v65, 0xffff0000, v38
	v_lshlrev_b32_e32 v66, 16, v39
	v_and_b32_e32 v67, 0xffff0000, v39
	v_add_f32_e32 v42, 0, v42
	v_add_f32_e32 v40, v40, v41
	v_add_f32_e32 v38, v64, v65
	v_add_f32_e32 v39, v66, v67
	v_lshlrev_b32_e32 v56, 16, v36
	v_and_b32_e32 v57, 0xffff0000, v36
	v_lshlrev_b32_e32 v58, 16, v37
	v_and_b32_e32 v59, 0xffff0000, v37
	v_add_f32_e32 v40, v42, v40
	v_add_f32_e32 v38, v38, v39
	v_add_f32_e32 v36, v56, v57
	v_add_f32_e32 v37, v58, v59
	v_lshlrev_b32_e32 v52, 16, v22
	v_and_b32_e32 v53, 0xffff0000, v22
	v_lshlrev_b32_e32 v54, 16, v23
	v_and_b32_e32 v55, 0xffff0000, v23
	v_add_f32_e32 v38, v40, v38
	v_add_f32_e32 v36, v36, v37
	v_add_f32_e32 v22, v52, v53
	v_add_f32_e32 v23, v54, v55
	v_add_f32_e32 v36, v38, v36
	v_add_f32_e32 v22, v22, v23
	v_lshlrev_b32_e32 v44, 16, v20
	v_and_b32_e32 v45, 0xffff0000, v20
	v_lshlrev_b32_e32 v46, 16, v21
	v_and_b32_e32 v47, 0xffff0000, v21
	v_add_f32_e32 v22, v36, v22
	v_add_f32_e32 v20, v44, v45
	v_add_f32_e32 v21, v46, v47
	v_lshlrev_b32_e32 v36, 16, v18
	v_and_b32_e32 v37, 0xffff0000, v18
	v_lshlrev_b32_e32 v38, 16, v19
	v_and_b32_e32 v39, 0xffff0000, v19
	v_add_f32_e32 v20, v20, v21
	v_add_f32_e32 v18, v36, v37
	v_add_f32_e32 v19, v38, v39
	v_lshlrev_b32_e32 v42, 16, v16
	v_and_b32_e32 v43, 0xffff0000, v16
	v_lshlrev_b32_e32 v40, 16, v17
	v_and_b32_e32 v41, 0xffff0000, v17
	v_add_f32_e32 v20, v22, v20
	v_add_f32_e32 v18, v18, v19
	v_add_f32_e32 v16, v42, v43
	v_add_f32_e32 v17, v40, v41
	v_add_f32_e32 v18, v20, v18
	v_add_f32_e32 v16, v16, v17
	v_add_f32_e32 v16, v18, v16
	s_mov_b64 s[6:7], s[34:35]
	s_mov_b64 s[8:9], s[36:37]
	v_add_f32_dpp v16, v16, v16 quad_perm:[1,0,3,2] row_mask:0xf bank_mask:0xf bound_ctrl:1
	v_lshl_add_u64 v[108:109], s[6:7], 0, v[192:193]
	v_lshl_add_u64 v[104:105], v[28:29], 0, s[42:43]
	v_add_f32_dpp v16, v16, v16 quad_perm:[2,3,0,1] row_mask:0xf bank_mask:0xf bound_ctrl:1
	v_lshl_add_u64 v[106:107], s[8:9], 0, v[192:193]
	s_lshl_b64 s[6:7], s[40:41], 11
	v_add_f32_dpp v16, v16, v16 row_ror:4 row_mask:0xf bank_mask:0xf bound_ctrl:1
	v_lshl_add_u64 v[82:83], v[30:31], 0, s[6:7]
	s_nop 0
	v_add_f32_dpp v16, v16, v16 row_ror:8 row_mask:0xf bank_mask:0xf bound_ctrl:1
	v_mov_b32_e32 v17, v16
	s_nop 1
	v_permlane16_swap_b32_e32 v16, v17
	v_add_f32_e32 v16, v16, v17
	v_mov_b32_e32 v17, v16
	s_nop 1
	v_permlane32_swap_b32_e32 v16, v17
	v_add_f32_e32 v16, v16, v17
	v_fmac_f32_e32 v101, 0xba000000, v16
	v_fmac_f32_e32 v103, 0xba000000, v16
	v_fmac_f32_e32 v100, 0xba000000, v16
	v_fmac_f32_e32 v102, 0xba000000, v16
	v_mul_f32_e32 v17, v103, v103
	v_mul_f32_e32 v18, v101, v101
	v_fmac_f32_e32 v17, v102, v102
	v_fmac_f32_e32 v18, v100, v100
	v_fmac_f32_e32 v73, 0xba000000, v16
	v_fmac_f32_e32 v75, 0xba000000, v16
	v_add_f32_e32 v17, v17, v18
	v_fmac_f32_e32 v72, 0xba000000, v16
	v_fmac_f32_e32 v74, 0xba000000, v16
	v_mul_f32_e32 v18, v75, v75
	v_mul_f32_e32 v19, v73, v73
	v_fmac_f32_e32 v18, v74, v74
	v_fmac_f32_e32 v19, v72, v72
	v_add_f32_e32 v18, v18, v19
	v_fmac_f32_e32 v67, 0xba000000, v16
	v_fmac_f32_e32 v65, 0xba000000, v16
	v_add_f32_e32 v17, v17, v18
	v_fmac_f32_e32 v66, 0xba000000, v16
	v_fmac_f32_e32 v64, 0xba000000, v16
	v_mul_f32_e32 v18, v65, v65
	v_mul_f32_e32 v19, v67, v67
	v_fmac_f32_e32 v18, v64, v64
	v_fmac_f32_e32 v19, v66, v66
	v_add_f32_e32 v18, v18, v19
	v_fmac_f32_e32 v59, 0xba000000, v16
	v_fmac_f32_e32 v57, 0xba000000, v16
	v_add_f32_e32 v17, v17, v18
	v_fmac_f32_e32 v58, 0xba000000, v16
	v_fmac_f32_e32 v56, 0xba000000, v16
	v_mul_f32_e32 v18, v57, v57
	v_mul_f32_e32 v19, v59, v59
	v_fmac_f32_e32 v18, v56, v56
	v_fmac_f32_e32 v19, v58, v58
	v_add_f32_e32 v18, v18, v19
	v_fmac_f32_e32 v55, 0xba000000, v16
	v_fmac_f32_e32 v53, 0xba000000, v16
	v_add_f32_e32 v17, v17, v18
	v_fmac_f32_e32 v54, 0xba000000, v16
	v_fmac_f32_e32 v52, 0xba000000, v16
	v_mul_f32_e32 v18, v53, v53
	v_mul_f32_e32 v19, v55, v55
	v_fmac_f32_e32 v18, v52, v52
	v_fmac_f32_e32 v19, v54, v54
	v_add_f32_e32 v18, v18, v19
	v_fmac_f32_e32 v47, 0xba000000, v16
	v_fmac_f32_e32 v45, 0xba000000, v16
	v_add_f32_e32 v17, v17, v18
	v_fmac_f32_e32 v46, 0xba000000, v16
	v_fmac_f32_e32 v44, 0xba000000, v16
	v_mul_f32_e32 v18, v45, v45
	v_mul_f32_e32 v19, v47, v47
	v_fmac_f32_e32 v18, v44, v44
	v_fmac_f32_e32 v19, v46, v46
	v_add_f32_e32 v18, v18, v19
	v_fmac_f32_e32 v39, 0xba000000, v16
	v_fmac_f32_e32 v37, 0xba000000, v16
	v_add_f32_e32 v17, v17, v18
	v_fmac_f32_e32 v38, 0xba000000, v16
	v_fmac_f32_e32 v36, 0xba000000, v16
	v_mul_f32_e32 v18, v37, v37
	v_mul_f32_e32 v19, v39, v39
	v_fmac_f32_e32 v18, v36, v36
	v_fmac_f32_e32 v19, v38, v38
	v_add_f32_e32 v18, v18, v19
	v_fmac_f32_e32 v41, 0xba000000, v16
	v_fmac_f32_e32 v43, 0xba000000, v16
	v_add_f32_e32 v17, v17, v18
	v_fmac_f32_e32 v40, 0xba000000, v16
	v_fmac_f32_e32 v42, 0xba000000, v16
	v_mul_f32_e32 v16, v43, v43
	v_mul_f32_e32 v18, v41, v41
	v_fmac_f32_e32 v16, v42, v42
	v_fmac_f32_e32 v18, v40, v40
	v_add_f32_e32 v16, v16, v18
	v_add_f32_e32 v16, v17, v16
	s_nop 1
	v_add_f32_dpp v16, v16, v16 quad_perm:[1,0,3,2] row_mask:0xf bank_mask:0xf bound_ctrl:1
	s_nop 1
	v_add_f32_dpp v16, v16, v16 quad_perm:[2,3,0,1] row_mask:0xf bank_mask:0xf bound_ctrl:1
	s_nop 1
	v_add_f32_dpp v16, v16, v16 row_ror:4 row_mask:0xf bank_mask:0xf bound_ctrl:1
	s_nop 1
	v_add_f32_dpp v16, v16, v16 row_ror:8 row_mask:0xf bank_mask:0xf bound_ctrl:1
	v_mov_b32_e32 v17, v16
	s_nop 1
	v_permlane16_swap_b32_e32 v16, v17
	v_add_f32_e32 v16, v16, v17
	v_mov_b32_e32 v17, v16
	s_nop 1
	v_permlane32_swap_b32_e32 v16, v17
	v_add_f32_e32 v16, v16, v17
	v_fmamk_f32 v16, v16, 0x3a000000, v207
	v_rsq_f32_e32 v76, v16
	flat_load_dwordx4 v[16:19], v[108:109]
	flat_load_dwordx4 v[20:23], v[106:107]
	v_pk_mul_f32 v[102:103], v[76:77], v[102:103] op_sel_hi:[0,1]
	v_pk_mul_f32 v[100:101], v[76:77], v[100:101] op_sel_hi:[0,1]
	v_pk_mul_f32 v[74:75], v[76:77], v[74:75] op_sel_hi:[0,1]
	v_pk_mul_f32 v[72:73], v[76:77], v[72:73] op_sel_hi:[0,1]
	v_pk_mul_f32 v[110:111], v[76:77], v[64:65] op_sel_hi:[0,1]
	v_pk_mul_f32 v[64:65], v[76:77], v[66:67] op_sel_hi:[0,1]
	s_waitcnt vmcnt(0) lgkmcnt(0)
	v_pk_fma_f32 v[100:101], v[18:19], v[100:101], v[22:23]
	v_pk_fma_f32 v[102:103], v[16:17], v[102:103], v[20:21]
	v_mov_b32_e32 v20, 0
	v_cvt_pk_bf16_f32 v16, v102, v103
	v_cvt_pk_bf16_f32 v17, v100, v101
	flat_store_dwordx2 v[104:105], v[16:17] nt
	v_med3_f32 v16, v102, s69, v208
	v_med3_f32 v17, v103, s69, v208
	v_cvt_pk_fp8_f32 v20, v16, v17
	v_med3_f32 v18, v100, s69, v208
	v_med3_f32 v19, v101, s69, v208
	v_cvt_pk_fp8_f32 v20, v18, v19 op_sel:[0,0,1]
	flat_store_dword v[82:83], v20 nt
	flat_load_dwordx4 v[16:19], v[108:109] offset:1024
	s_nop 0
	flat_load_dwordx4 v[20:23], v[106:107] offset:1024
	s_waitcnt vmcnt(0) lgkmcnt(0)
	v_pk_fma_f32 v[72:73], v[18:19], v[72:73], v[22:23]
	v_pk_fma_f32 v[74:75], v[16:17], v[74:75], v[20:21]
	v_mov_b32_e32 v20, 0
	v_cvt_pk_bf16_f32 v16, v74, v75
	v_cvt_pk_bf16_f32 v17, v72, v73
	flat_store_dwordx2 v[104:105], v[16:17] offset:512 nt
	v_med3_f32 v16, v74, s69, v208
	v_med3_f32 v17, v75, s69, v208
	v_cvt_pk_fp8_f32 v20, v16, v17
	v_med3_f32 v18, v72, s69, v208
	v_med3_f32 v19, v73, s69, v208
	v_cvt_pk_fp8_f32 v20, v18, v19 op_sel:[0,0,1]
	flat_store_dword v[82:83], v20 offset:256 nt
	flat_load_dwordx4 v[16:19], v[108:109] offset:2048
	s_nop 0
	flat_load_dwordx4 v[20:23], v[106:107] offset:2048
	s_waitcnt vmcnt(0) lgkmcnt(0)
	v_pk_fma_f32 v[64:65], v[18:19], v[64:65], v[22:23]
	v_pk_fma_f32 v[66:67], v[16:17], v[110:111], v[20:21]
	v_mov_b32_e32 v20, 0
	v_cvt_pk_bf16_f32 v16, v66, v67
	v_cvt_pk_bf16_f32 v17, v64, v65
	flat_store_dwordx2 v[104:105], v[16:17] offset:1024 nt
	v_med3_f32 v16, v66, s69, v208
	v_med3_f32 v17, v67, s69, v208
	v_cvt_pk_fp8_f32 v20, v16, v17
	v_med3_f32 v18, v64, s69, v208
	v_med3_f32 v19, v65, s69, v208
	v_pk_mul_f32 v[110:111], v[76:77], v[56:57] op_sel_hi:[0,1]
	v_cvt_pk_fp8_f32 v20, v18, v19 op_sel:[0,0,1]
	v_pk_mul_f32 v[56:57], v[76:77], v[58:59] op_sel_hi:[0,1]
	flat_store_dword v[82:83], v20 offset:512 nt
	flat_load_dwordx4 v[16:19], v[108:109] offset:3072
	s_nop 0
	flat_load_dwordx4 v[20:23], v[106:107] offset:3072
	s_waitcnt vmcnt(0) lgkmcnt(0)
	v_pk_fma_f32 v[56:57], v[18:19], v[56:57], v[22:23]
	v_pk_fma_f32 v[58:59], v[16:17], v[110:111], v[20:21]
	v_mov_b32_e32 v20, 0
	v_cvt_pk_bf16_f32 v16, v58, v59
	v_cvt_pk_bf16_f32 v17, v56, v57
	flat_store_dwordx2 v[104:105], v[16:17] offset:1536 nt
	v_med3_f32 v16, v58, s69, v208
	v_med3_f32 v17, v59, s69, v208
	v_cvt_pk_fp8_f32 v20, v16, v17
	v_med3_f32 v18, v56, s69, v208
	v_med3_f32 v19, v57, s69, v208
	v_add_co_u32_e32 v16, vcc, s33, v108
	v_cvt_pk_fp8_f32 v20, v18, v19 op_sel:[0,0,1]
	s_nop 0
	v_addc_co_u32_e32 v17, vcc, 0, v109, vcc
	v_add_co_u32_e32 v18, vcc, s33, v106
	flat_store_dword v[82:83], v20 offset:768 nt
	s_nop 0
	v_addc_co_u32_e32 v19, vcc, 0, v107, vcc
	flat_load_dwordx4 v[20:23], v[16:17]
	flat_load_dwordx4 v[106:109], v[18:19]
	v_pk_mul_f32 v[110:111], v[76:77], v[52:53] op_sel_hi:[0,1]
	v_pk_mul_f32 v[52:53], v[76:77], v[54:55] op_sel_hi:[0,1]
	v_mov_b32_e32 v77, 0
	s_waitcnt vmcnt(0) lgkmcnt(0)
	v_pk_fma_f32 v[52:53], v[22:23], v[52:53], v[108:109]
	v_pk_fma_f32 v[54:55], v[20:21], v[110:111], v[106:107]
	v_med3_f32 v22, v52, s69, v208
	v_cvt_pk_bf16_f32 v20, v54, v55
	v_cvt_pk_bf16_f32 v21, v52, v53
	flat_store_dwordx2 v[104:105], v[20:21] offset:2048 nt
	v_med3_f32 v20, v54, s69, v208
	v_med3_f32 v21, v55, s69, v208
	v_cvt_pk_fp8_f32 v77, v20, v21
	v_med3_f32 v23, v53, s69, v208
	v_cvt_pk_fp8_f32 v77, v22, v23 op_sel:[0,0,1]
	flat_store_dword v[82:83], v77 offset:1024 nt
	flat_load_dwordx4 v[20:23], v[16:17] offset:1024
	flat_load_dwordx4 v[106:109], v[18:19] offset:1024
	v_pk_mul_f32 v[110:111], v[76:77], v[44:45] op_sel_hi:[0,1]
	v_pk_mul_f32 v[44:45], v[76:77], v[46:47] op_sel_hi:[0,1]
	v_mov_b32_e32 v77, 0
	s_waitcnt vmcnt(0) lgkmcnt(0)
	v_pk_fma_f32 v[44:45], v[22:23], v[44:45], v[108:109]
	v_pk_fma_f32 v[46:47], v[20:21], v[110:111], v[106:107]
	v_med3_f32 v22, v44, s69, v208
	v_cvt_pk_bf16_f32 v20, v46, v47
	v_cvt_pk_bf16_f32 v21, v44, v45
	flat_store_dwordx2 v[104:105], v[20:21] offset:2560 nt
	v_med3_f32 v20, v46, s69, v208
	v_med3_f32 v21, v47, s69, v208
	v_cvt_pk_fp8_f32 v77, v20, v21
	v_med3_f32 v23, v45, s69, v208
	v_cvt_pk_fp8_f32 v77, v22, v23 op_sel:[0,0,1]
	flat_store_dword v[82:83], v77 offset:1280 nt
	flat_load_dwordx4 v[20:23], v[16:17] offset:2048
	flat_load_dwordx4 v[106:109], v[18:19] offset:2048
	v_pk_mul_f32 v[110:111], v[76:77], v[36:37] op_sel_hi:[0,1]
	v_pk_mul_f32 v[36:37], v[76:77], v[38:39] op_sel_hi:[0,1]
	v_mov_b32_e32 v77, 0
	s_waitcnt vmcnt(0) lgkmcnt(0)
	v_pk_fma_f32 v[36:37], v[22:23], v[36:37], v[108:109]
	v_pk_fma_f32 v[38:39], v[20:21], v[110:111], v[106:107]
	v_med3_f32 v22, v36, s69, v208
	v_cvt_pk_bf16_f32 v20, v38, v39
	v_cvt_pk_bf16_f32 v21, v36, v37
	flat_store_dwordx2 v[104:105], v[20:21] offset:3072 nt
	v_med3_f32 v20, v38, s69, v208
	v_med3_f32 v21, v39, s69, v208
	v_cvt_pk_fp8_f32 v77, v20, v21
	v_med3_f32 v23, v37, s69, v208
	v_cvt_pk_fp8_f32 v77, v22, v23 op_sel:[0,0,1]
	flat_store_dword v[82:83], v77 offset:1536 nt
	flat_load_dwordx4 v[20:23], v[16:17] offset:3072
	flat_load_dwordx4 v[106:109], v[18:19] offset:3072
	v_pk_mul_f32 v[18:19], v[76:77], v[42:43] op_sel_hi:[0,1]
	v_pk_mul_f32 v[16:17], v[76:77], v[40:41] op_sel_hi:[0,1]
	v_mov_b32_e32 v40, 0
	s_waitcnt vmcnt(0) lgkmcnt(0)
; #define LAS __attribute__((address_space(3)))
; __global__ void __launch_bounds__(NTHREADS, 2) hybrid_fwd(Args a) {
;     ...
;                     f32x2 y2[8][4];
; #pragma unroll
;                     for (int j = 0; j < 8; ++j)
; #pragma unroll
;                         for (int c = 0; c < 4; ++c) y2[j][c] = (f32x2){ya[j][c], yb[j][c]};
;                     f32x2 acc2[16];
; #pragma unroll
;                     for (int e = 0; e < 16; ++e) acc2[e] = (f32x2){0.f, 0.f};
; #pragma unroll
;                     for (int j = 0; j < 8; ++j) {
; #pragma unroll
;                         for (int e = 0; e < 16; ++e) { const f32x4 w = *(const LAS f32x4*)(rwT + e * 2052 + j * 256 + lane * 4);
;                             acc2[e] += y2[j][0] * (f32x2){w[0], w[0]}; acc2[e] += y2[j][1] * (f32x2){w[1], w[1]};
;                             acc2[e] += y2[j][2] * (f32x2){w[2], w[2]}; acc2[e] += y2[j][3] * (f32x2){w[3], w[3]}; }
;                         __builtin_amdgcn_sched_barrier(0);
;                     }
	v_pk_fma_f32 v[16:17], v[22:23], v[16:17], v[108:109]
	v_pk_fma_f32 v[18:19], v[20:21], v[18:19], v[106:107]
	v_med3_f32 v22, v16, s69, v208
	v_cvt_pk_bf16_f32 v20, v18, v19
	v_cvt_pk_bf16_f32 v21, v16, v17
	flat_store_dwordx2 v[104:105], v[20:21] offset:3584 nt
	v_med3_f32 v20, v18, s69, v208
	v_med3_f32 v21, v19, s69, v208
	v_cvt_pk_fp8_f32 v40, v20, v21
	v_med3_f32 v23, v17, s69, v208
	v_cvt_pk_fp8_f32 v40, v22, v23 op_sel:[0,0,1]
	flat_store_dword v[82:83], v40 offset:1792 nt
	v_add_u32_e32 v238, 0x10000, v25
	ds_read_b128 v[158:161], v25 offset:0
	ds_read_b128 v[162:165], v25 offset:8208
	ds_read_b128 v[166:169], v25 offset:16416
	ds_read_b128 v[170:173], v25 offset:24624
	ds_read_b128 v[174:177], v25 offset:32832
	ds_read_b128 v[178:181], v25 offset:41040
	ds_read_b128 v[182:185], v25 offset:49248
	ds_read_b128 v[186:189], v25 offset:57456
	v_mov_b32_e32 v76, v70
	v_mov_b32_e32 v77, v66
	v_mov_b32_e32 v66, v71
	v_mov_b32_e32 v82, v68
	v_mov_b32_e32 v83, v64
	v_mov_b32_e32 v64, v69
	v_mov_b32_e32 v68, v80
	v_mov_b32_e32 v69, v58
	v_mov_b32_e32 v58, v81
	v_mov_b32_e32 v70, v78
	v_mov_b32_e32 v71, v56
	v_mov_b32_e32 v56, v79
	ds_read_b128 v[198:201], v238 offset:128
	v_mov_b32_e32 v108, v48
	v_mov_b32_e32 v109, v102
	v_mov_b32_e32 v102, v49
	v_mov_b32_e32 v106, v62
	v_mov_b32_e32 v107, v72
	v_mov_b32_e32 v72, v63
	v_mov_b32_e32 v62, v84
	v_mov_b32_e32 v63, v52
	v_mov_b32_e32 v52, v85
	s_waitcnt lgkmcnt(8)
	v_pk_fma_f32 v[84:85], v[108:109], v[158:159], 0 op_sel_hi:[1,0,0]
	v_mov_b32_e32 v104, v60
	v_mov_b32_e32 v105, v74
	v_mov_b32_e32 v74, v61
	v_mov_b32_e32 v60, v86
	v_mov_b32_e32 v61, v54
	v_mov_b32_e32 v54, v87
	v_pk_fma_f32 v[78:79], v[158:159], v[102:103], v[84:85] op_sel:[1,0,0]
	ds_read_b128 v[202:205], v238 offset:8336
	v_mov_b32_e32 v110, v50
	v_mov_b32_e32 v111, v100
	v_mov_b32_e32 v100, v51
	v_pk_fma_f32 v[78:79], v[160:161], v[110:111], v[78:79] op_sel_hi:[0,1,1]
	v_mov_b32_e32 v80, v161
	v_pk_fma_f32 v[78:79], v[80:81], v[100:101], v[78:79] op_sel_hi:[0,1,1]
	s_waitcnt lgkmcnt(8)
	v_pk_fma_f32 v[80:81], v[108:109], v[162:163], 0 op_sel_hi:[1,0,0]
	v_mov_b32_e32 v50, v88
	v_pk_fma_f32 v[80:81], v[162:163], v[102:103], v[80:81] op_sel:[1,0,0]
	v_mov_b32_e32 v84, v165
	v_pk_fma_f32 v[80:81], v[164:165], v[110:111], v[80:81] op_sel_hi:[0,1,1]
	v_pk_fma_f32 v[120:121], v[84:85], v[100:101], v[80:81] op_sel_hi:[0,1,1]
	ds_read_b128 v[216:219], v238 offset:16544
	v_mov_b32_e32 v51, v44
	v_mov_b32_e32 v44, v89
	v_mov_b32_e32 v48, v90
	v_mov_b32_e32 v49, v46
	s_waitcnt lgkmcnt(8)
	v_pk_fma_f32 v[80:81], v[108:109], v[166:167], 0 op_sel_hi:[1,0,0]
	v_mov_b32_e32 v46, v91
	v_pk_fma_f32 v[80:81], v[166:167], v[102:103], v[80:81] op_sel:[1,0,0]
	v_mov_b32_e32 v84, v169
	v_pk_fma_f32 v[80:81], v[168:169], v[110:111], v[80:81] op_sel_hi:[0,1,1]
	v_pk_fma_f32 v[122:123], v[84:85], v[100:101], v[80:81] op_sel_hi:[0,1,1]
	ds_read_b128 v[220:223], v238 offset:24752
	v_mov_b32_e32 v42, v92
	v_mov_b32_e32 v43, v36
	v_mov_b32_e32 v36, v93
	v_mov_b32_e32 v40, v94
	s_waitcnt lgkmcnt(8)
	v_pk_fma_f32 v[80:81], v[108:109], v[170:171], 0 op_sel_hi:[1,0,0]
	v_mov_b32_e32 v41, v38
	v_pk_fma_f32 v[80:81], v[170:171], v[102:103], v[80:81] op_sel:[1,0,0]
	v_mov_b32_e32 v84, v173
	v_pk_fma_f32 v[80:81], v[172:173], v[110:111], v[80:81] op_sel_hi:[0,1,1]
	v_pk_fma_f32 v[80:81], v[84:85], v[100:101], v[80:81] op_sel_hi:[0,1,1]
	ds_read_b128 v[224:227], v238 offset:32960
	v_mov_b32_e32 v38, v95
	v_mov_b32_e32 v22, v96
	v_mov_b32_e32 v23, v18
	v_mov_b32_e32 v18, v97
	s_waitcnt lgkmcnt(8)
	v_pk_fma_f32 v[88:89], v[108:109], v[174:175], 0 op_sel_hi:[1,0,0]
	v_mov_b32_e32 v20, v98
	v_pk_fma_f32 v[84:85], v[174:175], v[102:103], v[88:89] op_sel:[1,0,0]
	v_mov_b32_e32 v21, v16
	v_pk_fma_f32 v[84:85], v[176:177], v[110:111], v[84:85] op_sel_hi:[0,1,1]
	v_mov_b32_e32 v86, v177
	v_pk_fma_f32 v[84:85], v[86:87], v[100:101], v[84:85] op_sel_hi:[0,1,1]
	ds_read_b128 v[228:231], v238 offset:41168
	v_mov_b32_e32 v16, v99
	s_waitcnt lgkmcnt(8)
	v_pk_fma_f32 v[90:91], v[108:109], v[178:179], 0 op_sel_hi:[1,0,0]
	s_nop 0
	v_pk_fma_f32 v[86:87], v[178:179], v[102:103], v[90:91] op_sel:[1,0,0]
	s_nop 0
	v_pk_fma_f32 v[86:87], v[180:181], v[110:111], v[86:87] op_sel_hi:[0,1,1]
	v_mov_b32_e32 v88, v181
	v_pk_fma_f32 v[86:87], v[88:89], v[100:101], v[86:87] op_sel_hi:[0,1,1]
	ds_read_b128 v[232:235], v238 offset:49376
	s_waitcnt lgkmcnt(8)
	v_pk_fma_f32 v[92:93], v[108:109], v[182:183], 0 op_sel_hi:[1,0,0]
	s_nop 0
	v_pk_fma_f32 v[88:89], v[182:183], v[102:103], v[92:93] op_sel:[1,0,0]
	s_nop 0
	v_pk_fma_f32 v[88:89], v[184:185], v[110:111], v[88:89] op_sel_hi:[0,1,1]
	v_mov_b32_e32 v90, v185
	v_pk_fma_f32 v[88:89], v[90:91], v[100:101], v[88:89] op_sel_hi:[0,1,1]
	ds_read_b128 v[242:245], v238 offset:57584
	s_waitcnt lgkmcnt(8)
	v_pk_fma_f32 v[94:95], v[108:109], v[186:187], 0 op_sel_hi:[1,0,0]
	s_nop 0
	v_pk_fma_f32 v[90:91], v[186:187], v[102:103], v[94:95] op_sel:[1,0,0]
	s_nop 0
	v_pk_fma_f32 v[90:91], v[188:189], v[110:111], v[90:91] op_sel_hi:[0,1,1]
	v_mov_b32_e32 v92, v189
	v_pk_fma_f32 v[90:91], v[92:93], v[100:101], v[90:91] op_sel_hi:[0,1,1]
	ds_read_b128 v[246:249], v25 offset:1024
	s_waitcnt lgkmcnt(8)
	v_pk_fma_f32 v[96:97], v[108:109], v[198:199], 0 op_sel_hi:[1,0,0]
	s_nop 0
	v_pk_fma_f32 v[92:93], v[198:199], v[102:103], v[96:97] op_sel:[1,0,0]
	s_nop 0
	v_pk_fma_f32 v[92:93], v[200:201], v[110:111], v[92:93] op_sel_hi:[0,1,1]
	v_mov_b32_e32 v94, v201
	v_pk_fma_f32 v[92:93], v[94:95], v[100:101], v[92:93] op_sel_hi:[0,1,1]
	ds_read_b128 v[250:253], v25 offset:9232
	s_waitcnt lgkmcnt(8)
; #define LAS __attribute__((address_space(3)))
; __global__ void __launch_bounds__(NTHREADS, 2) hybrid_fwd(Args a) {
;     ...
; #pragma unroll
;                     for (int j = 0; j < 8; ++j) {
; #pragma unroll
;                         for (int e = 0; e < 16; ++e) { const f32x4 w = *(const LAS f32x4*)(rwT + e * 2052 + j * 256 + lane * 4);
;                             acc2[e] += y2[j][0] * (f32x2){w[0], w[0]}; acc2[e] += y2[j][1] * (f32x2){w[1], w[1]};
;                             acc2[e] += y2[j][2] * (f32x2){w[2], w[2]}; acc2[e] += y2[j][3] * (f32x2){w[3], w[3]}; }
;                         __builtin_amdgcn_sched_barrier(0);
;                     }
	v_pk_fma_f32 v[98:99], v[108:109], v[202:203], 0 op_sel_hi:[1,0,0]
	s_nop 0
	v_pk_fma_f32 v[94:95], v[202:203], v[102:103], v[98:99] op_sel:[1,0,0]
	s_nop 0
	v_pk_fma_f32 v[94:95], v[204:205], v[110:111], v[94:95] op_sel_hi:[0,1,1]
	v_mov_b32_e32 v96, v205
	v_pk_fma_f32 v[94:95], v[96:97], v[100:101], v[94:95] op_sel_hi:[0,1,1]
	ds_read_b128 v[158:161], v25 offset:17440
	s_waitcnt lgkmcnt(8)
	v_pk_fma_f32 v[112:113], v[108:109], v[216:217], 0 op_sel_hi:[1,0,0]
	s_nop 0
	v_pk_fma_f32 v[96:97], v[216:217], v[102:103], v[112:113] op_sel:[1,0,0]
	ds_read_b128 v[162:165], v25 offset:25648
	v_pk_fma_f32 v[96:97], v[218:219], v[110:111], v[96:97] op_sel_hi:[0,1,1]
	v_mov_b32_e32 v98, v219
	v_pk_fma_f32 v[96:97], v[98:99], v[100:101], v[96:97] op_sel_hi:[0,1,1]
	s_waitcnt lgkmcnt(8)
	v_pk_fma_f32 v[98:99], v[108:109], v[220:221], 0 op_sel_hi:[1,0,0]
	s_nop 0
	v_pk_fma_f32 v[98:99], v[220:221], v[102:103], v[98:99] op_sel:[1,0,0]
	v_mov_b32_e32 v112, v223
	v_pk_fma_f32 v[98:99], v[222:223], v[110:111], v[98:99] op_sel_hi:[0,1,1]
	v_pk_fma_f32 v[98:99], v[112:113], v[100:101], v[98:99] op_sel_hi:[0,1,1]
	ds_read_b128 v[166:169], v25 offset:33856
	s_waitcnt lgkmcnt(8)
	v_pk_fma_f32 v[116:117], v[108:109], v[224:225], 0 op_sel_hi:[1,0,0]
	s_nop 0
	v_pk_fma_f32 v[112:113], v[224:225], v[102:103], v[116:117] op_sel:[1,0,0]
	s_nop 0
	v_pk_fma_f32 v[112:113], v[226:227], v[110:111], v[112:113] op_sel_hi:[0,1,1]
	v_mov_b32_e32 v114, v227
	v_pk_fma_f32 v[112:113], v[114:115], v[100:101], v[112:113] op_sel_hi:[0,1,1]
	ds_read_b128 v[170:173], v25 offset:42064
	s_waitcnt lgkmcnt(8)
	v_pk_fma_f32 v[118:119], v[108:109], v[228:229], 0 op_sel_hi:[1,0,0]
	s_nop 0
	v_pk_fma_f32 v[114:115], v[228:229], v[102:103], v[118:119] op_sel:[1,0,0]
	s_nop 0
	v_pk_fma_f32 v[114:115], v[230:231], v[110:111], v[114:115] op_sel_hi:[0,1,1]
	v_mov_b32_e32 v116, v231
	v_pk_fma_f32 v[114:115], v[116:117], v[100:101], v[114:115] op_sel_hi:[0,1,1]
	ds_read_b128 v[174:177], v25 offset:50272
	s_waitcnt lgkmcnt(8)
	v_pk_fma_f32 v[124:125], v[108:109], v[232:233], 0 op_sel_hi:[1,0,0]
	s_nop 0
	v_pk_fma_f32 v[116:117], v[232:233], v[102:103], v[124:125] op_sel:[1,0,0]
	ds_read_b128 v[178:181], v25 offset:58480
	v_pk_fma_f32 v[116:117], v[234:235], v[110:111], v[116:117] op_sel_hi:[0,1,1]
	v_mov_b32_e32 v118, v235
	v_pk_fma_f32 v[116:117], v[118:119], v[100:101], v[116:117] op_sel_hi:[0,1,1]
	s_waitcnt lgkmcnt(8)
	v_pk_fma_f32 v[108:109], v[108:109], v[242:243], 0 op_sel_hi:[1,0,0]
	s_nop 0
	v_pk_fma_f32 v[102:103], v[242:243], v[102:103], v[108:109] op_sel:[1,0,0]
	v_mov_b32_e32 v108, v245
	v_pk_fma_f32 v[102:103], v[244:245], v[110:111], v[102:103] op_sel_hi:[0,1,1]
	v_pk_fma_f32 v[118:119], v[108:109], v[100:101], v[102:103] op_sel_hi:[0,1,1]
	ds_read_b128 v[182:185], v238 offset:1152
	s_waitcnt lgkmcnt(8)
	v_pk_fma_f32 v[78:79], v[104:105], v[246:247], v[78:79] op_sel_hi:[1,0,1]
	s_nop 0
	v_pk_fma_f32 v[78:79], v[246:247], v[74:75], v[78:79] op_sel:[1,0,0]
	v_mov_b32_e32 v100, v249
	v_pk_fma_f32 v[78:79], v[248:249], v[106:107], v[78:79] op_sel_hi:[0,1,1]
	v_pk_fma_f32 v[78:79], v[100:101], v[72:73], v[78:79] op_sel_hi:[0,1,1]
	ds_read_b128 v[186:189], v238 offset:9360
	s_waitcnt lgkmcnt(8)
	v_pk_fma_f32 v[108:109], v[104:105], v[250:251], v[120:121] op_sel_hi:[1,0,1]
	s_nop 0
	v_pk_fma_f32 v[100:101], v[250:251], v[74:75], v[108:109] op_sel:[1,0,0]
	s_nop 0
	v_pk_fma_f32 v[100:101], v[252:253], v[106:107], v[100:101] op_sel_hi:[0,1,1]
	v_mov_b32_e32 v102, v253
	v_pk_fma_f32 v[120:121], v[102:103], v[72:73], v[100:101] op_sel_hi:[0,1,1]
	ds_read_b128 v[198:201], v238 offset:17568
	s_waitcnt lgkmcnt(8)
	v_pk_fma_f32 v[108:109], v[104:105], v[158:159], v[122:123] op_sel_hi:[1,0,1]
	s_nop 0
	v_pk_fma_f32 v[100:101], v[158:159], v[74:75], v[108:109] op_sel:[1,0,0]
	ds_read_b128 v[202:205], v238 offset:25776
	v_pk_fma_f32 v[100:101], v[160:161], v[106:107], v[100:101] op_sel_hi:[0,1,1]
	v_mov_b32_e32 v102, v161
	v_pk_fma_f32 v[100:101], v[102:103], v[72:73], v[100:101] op_sel_hi:[0,1,1]
	s_waitcnt lgkmcnt(8)
	v_pk_fma_f32 v[80:81], v[104:105], v[162:163], v[80:81] op_sel_hi:[1,0,1]
	s_nop 0
	v_pk_fma_f32 v[80:81], v[162:163], v[74:75], v[80:81] op_sel:[1,0,0]
	v_mov_b32_e32 v102, v165
	v_pk_fma_f32 v[80:81], v[164:165], v[106:107], v[80:81] op_sel_hi:[0,1,1]
	ds_read_b128 v[216:219], v238 offset:33984
	v_pk_fma_f32 v[80:81], v[102:103], v[72:73], v[80:81] op_sel_hi:[0,1,1]
	s_waitcnt lgkmcnt(8)
	v_pk_fma_f32 v[84:85], v[104:105], v[166:167], v[84:85] op_sel_hi:[1,0,1]
	s_nop 0
	v_pk_fma_f32 v[84:85], v[166:167], v[74:75], v[84:85] op_sel:[1,0,0]
	v_mov_b32_e32 v102, v169
	v_pk_fma_f32 v[84:85], v[168:169], v[106:107], v[84:85] op_sel_hi:[0,1,1]
	ds_read_b128 v[220:223], v238 offset:42192
	v_pk_fma_f32 v[84:85], v[102:103], v[72:73], v[84:85] op_sel_hi:[0,1,1]
	s_waitcnt lgkmcnt(8)
	v_pk_fma_f32 v[86:87], v[104:105], v[170:171], v[86:87] op_sel_hi:[1,0,1]
	s_nop 0
	v_pk_fma_f32 v[86:87], v[170:171], v[74:75], v[86:87] op_sel:[1,0,0]
	v_mov_b32_e32 v102, v173
	v_pk_fma_f32 v[86:87], v[172:173], v[106:107], v[86:87] op_sel_hi:[0,1,1]
	ds_read_b128 v[224:227], v238 offset:50400
	v_pk_fma_f32 v[86:87], v[102:103], v[72:73], v[86:87] op_sel_hi:[0,1,1]
	s_waitcnt lgkmcnt(8)
	v_pk_fma_f32 v[88:89], v[104:105], v[174:175], v[88:89] op_sel_hi:[1,0,1]
	s_nop 0
	v_pk_fma_f32 v[88:89], v[174:175], v[74:75], v[88:89] op_sel:[1,0,0]
	v_mov_b32_e32 v102, v177
	v_pk_fma_f32 v[88:89], v[176:177], v[106:107], v[88:89] op_sel_hi:[0,1,1]
	ds_read_b128 v[228:231], v238 offset:58608
	v_pk_fma_f32 v[88:89], v[102:103], v[72:73], v[88:89] op_sel_hi:[0,1,1]
	s_waitcnt lgkmcnt(8)
; #define LAS __attribute__((address_space(3)))
; __global__ void __launch_bounds__(NTHREADS, 2) hybrid_fwd(Args a) {
;     ...
; #pragma unroll
;                     for (int j = 0; j < 8; ++j) {
; #pragma unroll
;                         for (int e = 0; e < 16; ++e) { const f32x4 w = *(const LAS f32x4*)(rwT + e * 2052 + j * 256 + lane * 4);
;                             acc2[e] += y2[j][0] * (f32x2){w[0], w[0]}; acc2[e] += y2[j][1] * (f32x2){w[1], w[1]};
;                             acc2[e] += y2[j][2] * (f32x2){w[2], w[2]}; acc2[e] += y2[j][3] * (f32x2){w[3], w[3]}; }
;                         __builtin_amdgcn_sched_barrier(0);
;                     }
	v_pk_fma_f32 v[90:91], v[104:105], v[178:179], v[90:91] op_sel_hi:[1,0,1]
	s_nop 0
	v_pk_fma_f32 v[90:91], v[178:179], v[74:75], v[90:91] op_sel:[1,0,0]
	v_mov_b32_e32 v102, v181
	v_pk_fma_f32 v[90:91], v[180:181], v[106:107], v[90:91] op_sel_hi:[0,1,1]
	ds_read_b128 v[232:235], v25 offset:2048
	v_pk_fma_f32 v[90:91], v[102:103], v[72:73], v[90:91] op_sel_hi:[0,1,1]
	s_waitcnt lgkmcnt(8)
	v_pk_fma_f32 v[92:93], v[104:105], v[182:183], v[92:93] op_sel_hi:[1,0,1]
	s_nop 0
	v_pk_fma_f32 v[92:93], v[182:183], v[74:75], v[92:93] op_sel:[1,0,0]
	v_mov_b32_e32 v102, v185
	v_pk_fma_f32 v[92:93], v[184:185], v[106:107], v[92:93] op_sel_hi:[0,1,1]
	ds_read_b128 v[242:245], v25 offset:10256
	v_pk_fma_f32 v[92:93], v[102:103], v[72:73], v[92:93] op_sel_hi:[0,1,1]
	s_waitcnt lgkmcnt(8)
	v_pk_fma_f32 v[94:95], v[104:105], v[186:187], v[94:95] op_sel_hi:[1,0,1]
	s_nop 0
	v_pk_fma_f32 v[94:95], v[186:187], v[74:75], v[94:95] op_sel:[1,0,0]
	v_mov_b32_e32 v102, v189
	v_pk_fma_f32 v[94:95], v[188:189], v[106:107], v[94:95] op_sel_hi:[0,1,1]
	ds_read_b128 v[246:249], v25 offset:18464
	v_pk_fma_f32 v[94:95], v[102:103], v[72:73], v[94:95] op_sel_hi:[0,1,1]
	s_waitcnt lgkmcnt(8)
	v_pk_fma_f32 v[96:97], v[104:105], v[198:199], v[96:97] op_sel_hi:[1,0,1]
	s_nop 0
	v_pk_fma_f32 v[96:97], v[198:199], v[74:75], v[96:97] op_sel:[1,0,0]
	v_mov_b32_e32 v102, v201
	v_pk_fma_f32 v[96:97], v[200:201], v[106:107], v[96:97] op_sel_hi:[0,1,1]
	ds_read_b128 v[250:253], v25 offset:26672
	v_pk_fma_f32 v[96:97], v[102:103], v[72:73], v[96:97] op_sel_hi:[0,1,1]
	s_waitcnt lgkmcnt(8)
	v_pk_fma_f32 v[98:99], v[104:105], v[202:203], v[98:99] op_sel_hi:[1,0,1]
	s_nop 0
	v_pk_fma_f32 v[98:99], v[202:203], v[74:75], v[98:99] op_sel:[1,0,0]
	v_mov_b32_e32 v102, v205
	v_pk_fma_f32 v[98:99], v[204:205], v[106:107], v[98:99] op_sel_hi:[0,1,1]
	ds_read_b128 v[162:165], v25 offset:34880
	v_pk_fma_f32 v[98:99], v[102:103], v[72:73], v[98:99] op_sel_hi:[0,1,1]
	s_waitcnt lgkmcnt(8)
	v_pk_fma_f32 v[102:103], v[104:105], v[216:217], v[112:113] op_sel_hi:[1,0,1]
	s_nop 0
	v_pk_fma_f32 v[102:103], v[216:217], v[74:75], v[102:103] op_sel:[1,0,0]
	v_mov_b32_e32 v108, v219
	v_pk_fma_f32 v[102:103], v[218:219], v[106:107], v[102:103] op_sel_hi:[0,1,1]
	v_pk_fma_f32 v[102:103], v[108:109], v[72:73], v[102:103] op_sel_hi:[0,1,1]
	ds_read_b128 v[166:169], v25 offset:43088
	s_waitcnt lgkmcnt(8)
	v_pk_fma_f32 v[112:113], v[104:105], v[220:221], v[114:115] op_sel_hi:[1,0,1]
	s_nop 0
	v_pk_fma_f32 v[108:109], v[220:221], v[74:75], v[112:113] op_sel:[1,0,0]
	s_nop 0
	v_pk_fma_f32 v[108:109], v[222:223], v[106:107], v[108:109] op_sel_hi:[0,1,1]
	v_mov_b32_e32 v110, v223
	v_pk_fma_f32 v[108:109], v[110:111], v[72:73], v[108:109] op_sel_hi:[0,1,1]
	ds_read_b128 v[170:173], v25 offset:51296
	s_waitcnt lgkmcnt(8)
	v_pk_fma_f32 v[114:115], v[104:105], v[224:225], v[116:117] op_sel_hi:[1,0,1]
	s_nop 0
	v_pk_fma_f32 v[110:111], v[224:225], v[74:75], v[114:115] op_sel:[1,0,0]
	s_nop 0
	v_pk_fma_f32 v[110:111], v[226:227], v[106:107], v[110:111] op_sel_hi:[0,1,1]
	v_mov_b32_e32 v112, v227
	v_pk_fma_f32 v[110:111], v[112:113], v[72:73], v[110:111] op_sel_hi:[0,1,1]
	ds_read_b128 v[174:177], v25 offset:59504
	s_waitcnt lgkmcnt(8)
	v_pk_fma_f32 v[104:105], v[104:105], v[228:229], v[118:119] op_sel_hi:[1,0,1]
	s_nop 0
	v_pk_fma_f32 v[74:75], v[228:229], v[74:75], v[104:105] op_sel:[1,0,0]
	v_mov_b32_e32 v104, v231
	v_pk_fma_f32 v[74:75], v[230:231], v[106:107], v[74:75] op_sel_hi:[0,1,1]
	v_pk_fma_f32 v[104:105], v[104:105], v[72:73], v[74:75] op_sel_hi:[0,1,1]
	ds_read_b128 v[178:181], v238 offset:2176
	ds_read_b128 v[182:185], v238 offset:10384
	s_waitcnt lgkmcnt(8)
	v_pk_fma_f32 v[78:79], v[76:77], v[232:233], v[78:79] op_sel_hi:[1,0,1]
	s_nop 0
	v_pk_fma_f32 v[72:73], v[232:233], v[66:67], v[78:79] op_sel:[1,0,0]
	v_mov_b32_e32 v78, v245
	v_pk_fma_f32 v[72:73], v[234:235], v[82:83], v[72:73] op_sel_hi:[0,1,1]
	v_mov_b32_e32 v74, v235
	v_pk_fma_f32 v[72:73], v[74:75], v[64:65], v[72:73] op_sel_hi:[0,1,1]
	v_pk_fma_f32 v[74:75], v[76:77], v[242:243], v[120:121] op_sel_hi:[1,0,1]
	s_nop 0
	v_pk_fma_f32 v[74:75], v[242:243], v[66:67], v[74:75] op_sel:[1,0,0]
	s_nop 0
	v_pk_fma_f32 v[74:75], v[244:245], v[82:83], v[74:75] op_sel_hi:[0,1,1]
	ds_read_b128 v[186:189], v238 offset:18592
	v_pk_fma_f32 v[106:107], v[78:79], v[64:65], v[74:75] op_sel_hi:[0,1,1]
	s_waitcnt lgkmcnt(8)
	v_pk_fma_f32 v[74:75], v[76:77], v[246:247], v[100:101] op_sel_hi:[1,0,1]
	s_nop 0
	v_pk_fma_f32 v[74:75], v[246:247], v[66:67], v[74:75] op_sel:[1,0,0]
	v_mov_b32_e32 v78, v249
	v_pk_fma_f32 v[74:75], v[248:249], v[82:83], v[74:75] op_sel_hi:[0,1,1]
	ds_read_b128 v[198:201], v238 offset:26800
	v_pk_fma_f32 v[74:75], v[78:79], v[64:65], v[74:75] op_sel_hi:[0,1,1]
	s_waitcnt lgkmcnt(8)
	v_pk_fma_f32 v[78:79], v[76:77], v[250:251], v[80:81] op_sel_hi:[1,0,1]
	s_nop 0
	v_pk_fma_f32 v[78:79], v[250:251], v[66:67], v[78:79] op_sel:[1,0,0]
	v_mov_b32_e32 v80, v253
	v_pk_fma_f32 v[78:79], v[252:253], v[82:83], v[78:79] op_sel_hi:[0,1,1]
	ds_read_b128 v[202:205], v238 offset:35008
	v_pk_fma_f32 v[78:79], v[80:81], v[64:65], v[78:79] op_sel_hi:[0,1,1]
	s_waitcnt lgkmcnt(8)
	v_pk_fma_f32 v[80:81], v[76:77], v[162:163], v[84:85] op_sel_hi:[1,0,1]
	s_nop 0
	v_pk_fma_f32 v[80:81], v[162:163], v[66:67], v[80:81] op_sel:[1,0,0]
	v_mov_b32_e32 v84, v165
	v_pk_fma_f32 v[80:81], v[164:165], v[82:83], v[80:81] op_sel_hi:[0,1,1]
	ds_read_b128 v[158:161], v238 offset:51424
	v_pk_fma_f32 v[80:81], v[84:85], v[64:65], v[80:81] op_sel_hi:[0,1,1]
	s_waitcnt lgkmcnt(8)
; #define LAS __attribute__((address_space(3)))
; __global__ void __launch_bounds__(NTHREADS, 2) hybrid_fwd(Args a) {
;     ...
; #pragma unroll
;                     for (int j = 0; j < 8; ++j) {
; #pragma unroll
;                         for (int e = 0; e < 16; ++e) { const f32x4 w = *(const LAS f32x4*)(rwT + e * 2052 + j * 256 + lane * 4);
;                             acc2[e] += y2[j][0] * (f32x2){w[0], w[0]}; acc2[e] += y2[j][1] * (f32x2){w[1], w[1]};
;                             acc2[e] += y2[j][2] * (f32x2){w[2], w[2]}; acc2[e] += y2[j][3] * (f32x2){w[3], w[3]}; }
;                         __builtin_amdgcn_sched_barrier(0);
;                     }
	v_pk_fma_f32 v[84:85], v[76:77], v[166:167], v[86:87] op_sel_hi:[1,0,1]
	s_nop 0
	v_pk_fma_f32 v[84:85], v[166:167], v[66:67], v[84:85] op_sel:[1,0,0]
	v_mov_b32_e32 v86, v169
	v_pk_fma_f32 v[84:85], v[168:169], v[82:83], v[84:85] op_sel_hi:[0,1,1]
	ds_read_b128 v[216:219], v238 offset:43216
	v_pk_fma_f32 v[84:85], v[86:87], v[64:65], v[84:85] op_sel_hi:[0,1,1]
	s_waitcnt lgkmcnt(8)
	v_pk_fma_f32 v[86:87], v[76:77], v[170:171], v[88:89] op_sel_hi:[1,0,1]
	s_nop 0
	v_pk_fma_f32 v[86:87], v[170:171], v[66:67], v[86:87] op_sel:[1,0,0]
	v_mov_b32_e32 v88, v173
	v_pk_fma_f32 v[86:87], v[172:173], v[82:83], v[86:87] op_sel_hi:[0,1,1]
	ds_read_b128 v[220:223], v238 offset:59632
	v_pk_fma_f32 v[86:87], v[88:89], v[64:65], v[86:87] op_sel_hi:[0,1,1]
	s_waitcnt lgkmcnt(8)
	v_pk_fma_f32 v[88:89], v[76:77], v[174:175], v[90:91] op_sel_hi:[1,0,1]
	s_nop 0
	v_pk_fma_f32 v[88:89], v[174:175], v[66:67], v[88:89] op_sel:[1,0,0]
	v_mov_b32_e32 v90, v177
	v_pk_fma_f32 v[88:89], v[176:177], v[82:83], v[88:89] op_sel_hi:[0,1,1]
	ds_read_b128 v[224:227], v25 offset:3072
	v_pk_fma_f32 v[88:89], v[90:91], v[64:65], v[88:89] op_sel_hi:[0,1,1]
	s_waitcnt lgkmcnt(8)
	v_pk_fma_f32 v[90:91], v[76:77], v[178:179], v[92:93] op_sel_hi:[1,0,1]
	s_nop 0
	v_pk_fma_f32 v[90:91], v[178:179], v[66:67], v[90:91] op_sel:[1,0,0]
	v_mov_b32_e32 v92, v181
	v_pk_fma_f32 v[90:91], v[180:181], v[82:83], v[90:91] op_sel_hi:[0,1,1]
	ds_read_b128 v[228:231], v25 offset:11280
	v_pk_fma_f32 v[90:91], v[92:93], v[64:65], v[90:91] op_sel_hi:[0,1,1]
	s_waitcnt lgkmcnt(8)
	v_pk_fma_f32 v[92:93], v[76:77], v[182:183], v[94:95] op_sel_hi:[1,0,1]
	s_nop 0
	v_pk_fma_f32 v[92:93], v[182:183], v[66:67], v[92:93] op_sel:[1,0,0]
	v_mov_b32_e32 v94, v185
	v_pk_fma_f32 v[92:93], v[184:185], v[82:83], v[92:93] op_sel_hi:[0,1,1]
	ds_read_b128 v[232:235], v25 offset:19488
	v_pk_fma_f32 v[92:93], v[94:95], v[64:65], v[92:93] op_sel_hi:[0,1,1]
	s_waitcnt lgkmcnt(8)
	v_pk_fma_f32 v[94:95], v[76:77], v[186:187], v[96:97] op_sel_hi:[1,0,1]
	s_nop 0
	v_pk_fma_f32 v[94:95], v[186:187], v[66:67], v[94:95] op_sel:[1,0,0]
	v_mov_b32_e32 v96, v189
	v_pk_fma_f32 v[94:95], v[188:189], v[82:83], v[94:95] op_sel_hi:[0,1,1]
	ds_read_b128 v[242:245], v25 offset:27696
	v_pk_fma_f32 v[94:95], v[96:97], v[64:65], v[94:95] op_sel_hi:[0,1,1]
	s_waitcnt lgkmcnt(8)
	v_pk_fma_f32 v[96:97], v[76:77], v[198:199], v[98:99] op_sel_hi:[1,0,1]
	s_nop 0
	v_pk_fma_f32 v[96:97], v[198:199], v[66:67], v[96:97] op_sel:[1,0,0]
	v_mov_b32_e32 v98, v201
	v_pk_fma_f32 v[96:97], v[200:201], v[82:83], v[96:97] op_sel_hi:[0,1,1]
	v_pk_fma_f32 v[96:97], v[98:99], v[64:65], v[96:97] op_sel_hi:[0,1,1]
	ds_read_b128 v[246:249], v25 offset:35904
	ds_read_b128 v[250:253], v25 offset:44112
	s_waitcnt lgkmcnt(8)
	v_pk_fma_f32 v[102:103], v[76:77], v[202:203], v[102:103] op_sel_hi:[1,0,1]
	s_nop 0
	v_pk_fma_f32 v[98:99], v[202:203], v[66:67], v[102:103] op_sel:[1,0,0]
	s_nop 0
	v_pk_fma_f32 v[98:99], v[204:205], v[82:83], v[98:99] op_sel_hi:[0,1,1]
	v_mov_b32_e32 v100, v205
	v_pk_fma_f32 v[98:99], v[100:101], v[64:65], v[98:99] op_sel_hi:[0,1,1]
	ds_read_b128 v[162:165], v25 offset:52320
	s_waitcnt lgkmcnt(8)
	v_pk_fma_f32 v[108:109], v[76:77], v[216:217], v[108:109] op_sel_hi:[1,0,1]
	s_nop 0
	v_pk_fma_f32 v[100:101], v[216:217], v[66:67], v[108:109] op_sel:[1,0,0]
	v_mov_b32_e32 v108, v161
	v_pk_fma_f32 v[100:101], v[218:219], v[82:83], v[100:101] op_sel_hi:[0,1,1]
	v_mov_b32_e32 v102, v219
	v_pk_fma_f32 v[100:101], v[102:103], v[64:65], v[100:101] op_sel_hi:[0,1,1]
	v_pk_fma_f32 v[102:103], v[76:77], v[158:159], v[110:111] op_sel_hi:[1,0,1]
	s_nop 0
	v_pk_fma_f32 v[102:103], v[158:159], v[66:67], v[102:103] op_sel:[1,0,0]
	s_nop 0
	v_pk_fma_f32 v[102:103], v[160:161], v[82:83], v[102:103] op_sel_hi:[0,1,1]
	v_pk_fma_f32 v[102:103], v[108:109], v[64:65], v[102:103] op_sel_hi:[0,1,1]
	ds_read_b128 v[166:169], v25 offset:60528
	s_waitcnt lgkmcnt(8)
	v_pk_fma_f32 v[76:77], v[76:77], v[220:221], v[104:105] op_sel_hi:[1,0,1]
	s_nop 0
	v_pk_fma_f32 v[66:67], v[220:221], v[66:67], v[76:77] op_sel:[1,0,0]
	v_mov_b32_e32 v76, v223
	v_pk_fma_f32 v[66:67], v[222:223], v[82:83], v[66:67] op_sel_hi:[0,1,1]
	v_pk_fma_f32 v[104:105], v[76:77], v[64:65], v[66:67] op_sel_hi:[0,1,1]
	ds_read_b128 v[170:173], v238 offset:3200
	ds_read_b128 v[174:177], v238 offset:11408
	s_waitcnt lgkmcnt(8)
	v_pk_fma_f32 v[72:73], v[68:69], v[224:225], v[72:73] op_sel_hi:[1,0,1]
	s_nop 0
	v_pk_fma_f32 v[64:65], v[224:225], v[58:59], v[72:73] op_sel:[1,0,0]
	v_mov_b32_e32 v72, v231
	v_pk_fma_f32 v[64:65], v[226:227], v[70:71], v[64:65] op_sel_hi:[0,1,1]
	v_mov_b32_e32 v66, v227
	v_pk_fma_f32 v[64:65], v[66:67], v[56:57], v[64:65] op_sel_hi:[0,1,1]
	v_pk_fma_f32 v[66:67], v[68:69], v[228:229], v[106:107] op_sel_hi:[1,0,1]
	s_nop 0
	v_pk_fma_f32 v[66:67], v[228:229], v[58:59], v[66:67] op_sel:[1,0,0]
	s_nop 0
	v_pk_fma_f32 v[66:67], v[230:231], v[70:71], v[66:67] op_sel_hi:[0,1,1]
	ds_read_b128 v[178:181], v238 offset:19616
	v_pk_fma_f32 v[106:107], v[72:73], v[56:57], v[66:67] op_sel_hi:[0,1,1]
	s_waitcnt lgkmcnt(8)
	v_pk_fma_f32 v[66:67], v[68:69], v[232:233], v[74:75] op_sel_hi:[1,0,1]
	s_nop 0
	v_pk_fma_f32 v[66:67], v[232:233], v[58:59], v[66:67] op_sel:[1,0,0]
	v_mov_b32_e32 v72, v235
	v_pk_fma_f32 v[66:67], v[234:235], v[70:71], v[66:67] op_sel_hi:[0,1,1]
	v_pk_fma_f32 v[66:67], v[72:73], v[56:57], v[66:67] op_sel_hi:[0,1,1]
	ds_read_b128 v[182:185], v238 offset:27824
	s_waitcnt lgkmcnt(8)
; #define LAS __attribute__((address_space(3)))
; __global__ void __launch_bounds__(NTHREADS, 2) hybrid_fwd(Args a) {
;     ...
; #pragma unroll
;                     for (int j = 0; j < 8; ++j) {
; #pragma unroll
;                         for (int e = 0; e < 16; ++e) { const f32x4 w = *(const LAS f32x4*)(rwT + e * 2052 + j * 256 + lane * 4);
;                             acc2[e] += y2[j][0] * (f32x2){w[0], w[0]}; acc2[e] += y2[j][1] * (f32x2){w[1], w[1]};
;                             acc2[e] += y2[j][2] * (f32x2){w[2], w[2]}; acc2[e] += y2[j][3] * (f32x2){w[3], w[3]}; }
;                         __builtin_amdgcn_sched_barrier(0);
;                     }
	v_pk_fma_f32 v[76:77], v[68:69], v[242:243], v[78:79] op_sel_hi:[1,0,1]
	s_nop 0
	v_pk_fma_f32 v[72:73], v[242:243], v[58:59], v[76:77] op_sel:[1,0,0]
	s_nop 0
	v_pk_fma_f32 v[72:73], v[244:245], v[70:71], v[72:73] op_sel_hi:[0,1,1]
	v_mov_b32_e32 v74, v245
	v_pk_fma_f32 v[72:73], v[74:75], v[56:57], v[72:73] op_sel_hi:[0,1,1]
	ds_read_b128 v[186:189], v238 offset:36032
	s_waitcnt lgkmcnt(8)
	v_pk_fma_f32 v[78:79], v[68:69], v[246:247], v[80:81] op_sel_hi:[1,0,1]
	s_nop 0
	v_pk_fma_f32 v[74:75], v[246:247], v[58:59], v[78:79] op_sel:[1,0,0]
	s_nop 0
	v_pk_fma_f32 v[74:75], v[248:249], v[70:71], v[74:75] op_sel_hi:[0,1,1]
	v_mov_b32_e32 v76, v249
	v_pk_fma_f32 v[74:75], v[76:77], v[56:57], v[74:75] op_sel_hi:[0,1,1]
	ds_read_b128 v[198:201], v238 offset:44240
	s_waitcnt lgkmcnt(8)
	v_pk_fma_f32 v[80:81], v[68:69], v[250:251], v[84:85] op_sel_hi:[1,0,1]
	s_nop 0
	v_pk_fma_f32 v[76:77], v[250:251], v[58:59], v[80:81] op_sel:[1,0,0]
	s_nop 0
	v_pk_fma_f32 v[76:77], v[252:253], v[70:71], v[76:77] op_sel_hi:[0,1,1]
	v_mov_b32_e32 v78, v253
	v_pk_fma_f32 v[76:77], v[78:79], v[56:57], v[76:77] op_sel_hi:[0,1,1]
	ds_read_b128 v[202:205], v238 offset:52448
	s_waitcnt lgkmcnt(8)
	v_pk_fma_f32 v[82:83], v[68:69], v[162:163], v[86:87] op_sel_hi:[1,0,1]
	s_nop 0
	v_pk_fma_f32 v[78:79], v[162:163], v[58:59], v[82:83] op_sel:[1,0,0]
	s_nop 0
	v_pk_fma_f32 v[78:79], v[164:165], v[70:71], v[78:79] op_sel_hi:[0,1,1]
	v_mov_b32_e32 v80, v165
	v_pk_fma_f32 v[78:79], v[80:81], v[56:57], v[78:79] op_sel_hi:[0,1,1]
	ds_read_b128 v[216:219], v238 offset:60656
	s_waitcnt lgkmcnt(8)
	v_pk_fma_f32 v[84:85], v[68:69], v[166:167], v[88:89] op_sel_hi:[1,0,1]
	s_nop 0
	v_pk_fma_f32 v[80:81], v[166:167], v[58:59], v[84:85] op_sel:[1,0,0]
	s_nop 0
	v_pk_fma_f32 v[80:81], v[168:169], v[70:71], v[80:81] op_sel_hi:[0,1,1]
	v_mov_b32_e32 v82, v169
	v_pk_fma_f32 v[80:81], v[82:83], v[56:57], v[80:81] op_sel_hi:[0,1,1]
	ds_read_b128 v[158:161], v25 offset:4096
	s_waitcnt lgkmcnt(8)
	v_pk_fma_f32 v[86:87], v[68:69], v[170:171], v[90:91] op_sel_hi:[1,0,1]
	s_nop 0
	v_pk_fma_f32 v[82:83], v[170:171], v[58:59], v[86:87] op_sel:[1,0,0]
	s_nop 0
	v_pk_fma_f32 v[82:83], v[172:173], v[70:71], v[82:83] op_sel_hi:[0,1,1]
	v_mov_b32_e32 v84, v173
	v_pk_fma_f32 v[82:83], v[84:85], v[56:57], v[82:83] op_sel_hi:[0,1,1]
	ds_read_b128 v[220:223], v25 offset:12304
	s_waitcnt lgkmcnt(8)
	v_pk_fma_f32 v[88:89], v[68:69], v[174:175], v[92:93] op_sel_hi:[1,0,1]
	s_nop 0
	v_pk_fma_f32 v[84:85], v[174:175], v[58:59], v[88:89] op_sel:[1,0,0]
	s_nop 0
	v_pk_fma_f32 v[84:85], v[176:177], v[70:71], v[84:85] op_sel_hi:[0,1,1]
	v_mov_b32_e32 v86, v177
	v_pk_fma_f32 v[84:85], v[86:87], v[56:57], v[84:85] op_sel_hi:[0,1,1]
	ds_read_b128 v[224:227], v25 offset:20512
	s_waitcnt lgkmcnt(8)
	v_pk_fma_f32 v[90:91], v[68:69], v[178:179], v[94:95] op_sel_hi:[1,0,1]
	s_nop 0
	v_pk_fma_f32 v[86:87], v[178:179], v[58:59], v[90:91] op_sel:[1,0,0]
	s_nop 0
	v_pk_fma_f32 v[86:87], v[180:181], v[70:71], v[86:87] op_sel_hi:[0,1,1]
	v_mov_b32_e32 v88, v181
	v_pk_fma_f32 v[86:87], v[88:89], v[56:57], v[86:87] op_sel_hi:[0,1,1]
	ds_read_b128 v[228:231], v25 offset:28720
	s_waitcnt lgkmcnt(8)
	v_pk_fma_f32 v[92:93], v[68:69], v[182:183], v[96:97] op_sel_hi:[1,0,1]
	s_nop 0
	v_pk_fma_f32 v[88:89], v[182:183], v[58:59], v[92:93] op_sel:[1,0,0]
	s_nop 0
	v_pk_fma_f32 v[88:89], v[184:185], v[70:71], v[88:89] op_sel_hi:[0,1,1]
	v_mov_b32_e32 v90, v185
	v_pk_fma_f32 v[88:89], v[90:91], v[56:57], v[88:89] op_sel_hi:[0,1,1]
	ds_read_b128 v[232:235], v25 offset:36928
	s_waitcnt lgkmcnt(8)
	v_pk_fma_f32 v[94:95], v[68:69], v[186:187], v[98:99] op_sel_hi:[1,0,1]
	s_nop 0
	v_pk_fma_f32 v[90:91], v[186:187], v[58:59], v[94:95] op_sel:[1,0,0]
	s_nop 0
	v_pk_fma_f32 v[90:91], v[188:189], v[70:71], v[90:91] op_sel_hi:[0,1,1]
	v_mov_b32_e32 v92, v189
	v_pk_fma_f32 v[90:91], v[92:93], v[56:57], v[90:91] op_sel_hi:[0,1,1]
	ds_read_b128 v[242:245], v25 offset:45136
	s_waitcnt lgkmcnt(8)
	v_pk_fma_f32 v[96:97], v[68:69], v[198:199], v[100:101] op_sel_hi:[1,0,1]
	s_nop 0
	v_pk_fma_f32 v[92:93], v[198:199], v[58:59], v[96:97] op_sel:[1,0,0]
	s_nop 0
	v_pk_fma_f32 v[92:93], v[200:201], v[70:71], v[92:93] op_sel_hi:[0,1,1]
	v_mov_b32_e32 v94, v201
	v_pk_fma_f32 v[92:93], v[94:95], v[56:57], v[92:93] op_sel_hi:[0,1,1]
	ds_read_b128 v[246:249], v25 offset:53344
	s_waitcnt lgkmcnt(8)
	v_pk_fma_f32 v[98:99], v[68:69], v[202:203], v[102:103] op_sel_hi:[1,0,1]
	s_nop 0
	v_pk_fma_f32 v[94:95], v[202:203], v[58:59], v[98:99] op_sel:[1,0,0]
	s_nop 0
	v_pk_fma_f32 v[94:95], v[204:205], v[70:71], v[94:95] op_sel_hi:[0,1,1]
	v_mov_b32_e32 v96, v205
	v_pk_fma_f32 v[94:95], v[96:97], v[56:57], v[94:95] op_sel_hi:[0,1,1]
	ds_read_b128 v[250:253], v25 offset:61552
	s_waitcnt lgkmcnt(8)
	v_pk_fma_f32 v[68:69], v[68:69], v[216:217], v[104:105] op_sel_hi:[1,0,1]
	s_nop 0
	v_pk_fma_f32 v[58:59], v[216:217], v[58:59], v[68:69] op_sel:[1,0,0]
	v_mov_b32_e32 v68, v219
	v_pk_fma_f32 v[58:59], v[218:219], v[70:71], v[58:59] op_sel_hi:[0,1,1]
	v_pk_fma_f32 v[96:97], v[68:69], v[56:57], v[58:59] op_sel_hi:[0,1,1]
	ds_read_b128 v[162:165], v238 offset:4224
	ds_read_b128 v[166:169], v238 offset:12432
	s_waitcnt lgkmcnt(8)
	v_pk_fma_f32 v[64:65], v[60:61], v[158:159], v[64:65] op_sel_hi:[1,0,1]
	s_nop 0
	v_pk_fma_f32 v[56:57], v[158:159], v[54:55], v[64:65] op_sel:[1,0,0]
	v_mov_b32_e32 v64, v223
	v_pk_fma_f32 v[56:57], v[160:161], v[62:63], v[56:57] op_sel_hi:[0,1,1]
	v_mov_b32_e32 v58, v161
	v_pk_fma_f32 v[56:57], v[58:59], v[52:53], v[56:57] op_sel_hi:[0,1,1]
	v_pk_fma_f32 v[58:59], v[60:61], v[220:221], v[106:107] op_sel_hi:[1,0,1]
	s_nop 0
	v_pk_fma_f32 v[58:59], v[220:221], v[54:55], v[58:59] op_sel:[1,0,0]
	s_nop 0
	v_pk_fma_f32 v[58:59], v[222:223], v[62:63], v[58:59] op_sel_hi:[0,1,1]
	ds_read_b128 v[170:173], v238 offset:20640
	v_pk_fma_f32 v[98:99], v[64:65], v[52:53], v[58:59] op_sel_hi:[0,1,1]
	s_waitcnt lgkmcnt(8)
; #define LAS __attribute__((address_space(3)))
; __global__ void __launch_bounds__(NTHREADS, 2) hybrid_fwd(Args a) {
;     ...
; #pragma unroll
;                     for (int j = 0; j < 8; ++j) {
; #pragma unroll
;                         for (int e = 0; e < 16; ++e) { const f32x4 w = *(const LAS f32x4*)(rwT + e * 2052 + j * 256 + lane * 4);
;                             acc2[e] += y2[j][0] * (f32x2){w[0], w[0]}; acc2[e] += y2[j][1] * (f32x2){w[1], w[1]};
;                             acc2[e] += y2[j][2] * (f32x2){w[2], w[2]}; acc2[e] += y2[j][3] * (f32x2){w[3], w[3]}; }
;                         __builtin_amdgcn_sched_barrier(0);
;                     }
	v_pk_fma_f32 v[58:59], v[60:61], v[224:225], v[66:67] op_sel_hi:[1,0,1]
	s_nop 0
	v_pk_fma_f32 v[58:59], v[224:225], v[54:55], v[58:59] op_sel:[1,0,0]
	v_mov_b32_e32 v64, v227
	v_pk_fma_f32 v[58:59], v[226:227], v[62:63], v[58:59] op_sel_hi:[0,1,1]
	v_pk_fma_f32 v[58:59], v[64:65], v[52:53], v[58:59] op_sel_hi:[0,1,1]
	ds_read_b128 v[174:177], v238 offset:28848
	s_waitcnt lgkmcnt(8)
	v_pk_fma_f32 v[68:69], v[60:61], v[228:229], v[72:73] op_sel_hi:[1,0,1]
	s_nop 0
	v_pk_fma_f32 v[64:65], v[228:229], v[54:55], v[68:69] op_sel:[1,0,0]
	s_nop 0
	v_pk_fma_f32 v[64:65], v[230:231], v[62:63], v[64:65] op_sel_hi:[0,1,1]
	v_mov_b32_e32 v66, v231
	v_pk_fma_f32 v[64:65], v[66:67], v[52:53], v[64:65] op_sel_hi:[0,1,1]
	ds_read_b128 v[178:181], v238 offset:37056
	s_waitcnt lgkmcnt(8)
	v_pk_fma_f32 v[70:71], v[60:61], v[232:233], v[74:75] op_sel_hi:[1,0,1]
	s_nop 0
	v_pk_fma_f32 v[66:67], v[232:233], v[54:55], v[70:71] op_sel:[1,0,0]
	s_nop 0
	v_pk_fma_f32 v[66:67], v[234:235], v[62:63], v[66:67] op_sel_hi:[0,1,1]
	v_mov_b32_e32 v68, v235
	v_pk_fma_f32 v[66:67], v[68:69], v[52:53], v[66:67] op_sel_hi:[0,1,1]
	ds_read_b128 v[182:185], v238 offset:45264
	s_waitcnt lgkmcnt(8)
	v_pk_fma_f32 v[72:73], v[60:61], v[242:243], v[76:77] op_sel_hi:[1,0,1]
	s_nop 0
	v_pk_fma_f32 v[68:69], v[242:243], v[54:55], v[72:73] op_sel:[1,0,0]
	s_nop 0
	v_pk_fma_f32 v[68:69], v[244:245], v[62:63], v[68:69] op_sel_hi:[0,1,1]
	v_mov_b32_e32 v70, v245
	v_pk_fma_f32 v[68:69], v[70:71], v[52:53], v[68:69] op_sel_hi:[0,1,1]
	ds_read_b128 v[186:189], v238 offset:53472
	s_waitcnt lgkmcnt(8)
	v_pk_fma_f32 v[74:75], v[60:61], v[246:247], v[78:79] op_sel_hi:[1,0,1]
	s_nop 0
	v_pk_fma_f32 v[70:71], v[246:247], v[54:55], v[74:75] op_sel:[1,0,0]
	s_nop 0
	v_pk_fma_f32 v[70:71], v[248:249], v[62:63], v[70:71] op_sel_hi:[0,1,1]
	v_mov_b32_e32 v72, v249
	v_pk_fma_f32 v[70:71], v[72:73], v[52:53], v[70:71] op_sel_hi:[0,1,1]
	ds_read_b128 v[198:201], v238 offset:61680
	s_waitcnt lgkmcnt(8)
	v_pk_fma_f32 v[76:77], v[60:61], v[250:251], v[80:81] op_sel_hi:[1,0,1]
	s_nop 0
	v_pk_fma_f32 v[72:73], v[250:251], v[54:55], v[76:77] op_sel:[1,0,0]
	s_nop 0
	v_pk_fma_f32 v[72:73], v[252:253], v[62:63], v[72:73] op_sel_hi:[0,1,1]
	v_mov_b32_e32 v74, v253
	v_pk_fma_f32 v[72:73], v[74:75], v[52:53], v[72:73] op_sel_hi:[0,1,1]
	ds_read_b128 v[202:205], v25 offset:5120
	s_waitcnt lgkmcnt(8)
	v_pk_fma_f32 v[78:79], v[60:61], v[162:163], v[82:83] op_sel_hi:[1,0,1]
	s_nop 0
	v_pk_fma_f32 v[74:75], v[162:163], v[54:55], v[78:79] op_sel:[1,0,0]
	s_nop 0
	v_pk_fma_f32 v[74:75], v[164:165], v[62:63], v[74:75] op_sel_hi:[0,1,1]
	v_mov_b32_e32 v76, v165
	v_pk_fma_f32 v[74:75], v[76:77], v[52:53], v[74:75] op_sel_hi:[0,1,1]
	ds_read_b128 v[216:219], v25 offset:13328
	s_waitcnt lgkmcnt(8)
	v_pk_fma_f32 v[80:81], v[60:61], v[166:167], v[84:85] op_sel_hi:[1,0,1]
	s_nop 0
	v_pk_fma_f32 v[76:77], v[166:167], v[54:55], v[80:81] op_sel:[1,0,0]
	s_nop 0
	v_pk_fma_f32 v[76:77], v[168:169], v[62:63], v[76:77] op_sel_hi:[0,1,1]
	v_mov_b32_e32 v78, v169
	v_pk_fma_f32 v[76:77], v[78:79], v[52:53], v[76:77] op_sel_hi:[0,1,1]
	ds_read_b128 v[158:161], v25 offset:21536
	s_waitcnt lgkmcnt(8)
	v_pk_fma_f32 v[82:83], v[60:61], v[170:171], v[86:87] op_sel_hi:[1,0,1]
	s_nop 0
	v_pk_fma_f32 v[78:79], v[170:171], v[54:55], v[82:83] op_sel:[1,0,0]
	s_nop 0
	v_pk_fma_f32 v[78:79], v[172:173], v[62:63], v[78:79] op_sel_hi:[0,1,1]
	v_mov_b32_e32 v80, v173
	v_pk_fma_f32 v[78:79], v[80:81], v[52:53], v[78:79] op_sel_hi:[0,1,1]
	ds_read_b128 v[220:223], v25 offset:29744
	s_waitcnt lgkmcnt(8)
	v_pk_fma_f32 v[84:85], v[60:61], v[174:175], v[88:89] op_sel_hi:[1,0,1]
	s_nop 0
	v_pk_fma_f32 v[80:81], v[174:175], v[54:55], v[84:85] op_sel:[1,0,0]
	s_nop 0
	v_pk_fma_f32 v[80:81], v[176:177], v[62:63], v[80:81] op_sel_hi:[0,1,1]
	v_mov_b32_e32 v82, v177
	v_pk_fma_f32 v[80:81], v[82:83], v[52:53], v[80:81] op_sel_hi:[0,1,1]
	ds_read_b128 v[224:227], v25 offset:37952
	s_waitcnt lgkmcnt(8)
	v_pk_fma_f32 v[86:87], v[60:61], v[178:179], v[90:91] op_sel_hi:[1,0,1]
	s_nop 0
	v_pk_fma_f32 v[82:83], v[178:179], v[54:55], v[86:87] op_sel:[1,0,0]
	s_nop 0
	v_pk_fma_f32 v[82:83], v[180:181], v[62:63], v[82:83] op_sel_hi:[0,1,1]
	v_mov_b32_e32 v84, v181
	v_pk_fma_f32 v[82:83], v[84:85], v[52:53], v[82:83] op_sel_hi:[0,1,1]
	ds_read_b128 v[228:231], v25 offset:46160
	s_waitcnt lgkmcnt(8)
	v_pk_fma_f32 v[88:89], v[60:61], v[182:183], v[92:93] op_sel_hi:[1,0,1]
	s_nop 0
	v_pk_fma_f32 v[84:85], v[182:183], v[54:55], v[88:89] op_sel:[1,0,0]
	s_nop 0
	v_pk_fma_f32 v[84:85], v[184:185], v[62:63], v[84:85] op_sel_hi:[0,1,1]
	v_mov_b32_e32 v86, v185
	v_pk_fma_f32 v[84:85], v[86:87], v[52:53], v[84:85] op_sel_hi:[0,1,1]
	ds_read_b128 v[232:235], v25 offset:54368
	s_waitcnt lgkmcnt(8)
	v_pk_fma_f32 v[90:91], v[60:61], v[186:187], v[94:95] op_sel_hi:[1,0,1]
	s_nop 0
	v_pk_fma_f32 v[86:87], v[186:187], v[54:55], v[90:91] op_sel:[1,0,0]
	s_nop 0
	v_pk_fma_f32 v[86:87], v[188:189], v[62:63], v[86:87] op_sel_hi:[0,1,1]
	v_mov_b32_e32 v88, v189
	v_pk_fma_f32 v[86:87], v[88:89], v[52:53], v[86:87] op_sel_hi:[0,1,1]
	ds_read_b128 v[242:245], v25 offset:62576
	s_waitcnt lgkmcnt(8)
	v_pk_fma_f32 v[60:61], v[60:61], v[198:199], v[96:97] op_sel_hi:[1,0,1]
	s_nop 0
	v_pk_fma_f32 v[54:55], v[198:199], v[54:55], v[60:61] op_sel:[1,0,0]
	v_mov_b32_e32 v60, v201
	v_pk_fma_f32 v[54:55], v[200:201], v[62:63], v[54:55] op_sel_hi:[0,1,1]
	v_pk_fma_f32 v[88:89], v[60:61], v[52:53], v[54:55] op_sel_hi:[0,1,1]
	ds_read_b128 v[246:249], v238 offset:5248
	s_waitcnt lgkmcnt(8)
; #define LAS __attribute__((address_space(3)))
; __global__ void __launch_bounds__(NTHREADS, 2) hybrid_fwd(Args a) {
;     ...
; #pragma unroll
;                     for (int j = 0; j < 8; ++j) {
; #pragma unroll
;                         for (int e = 0; e < 16; ++e) { const f32x4 w = *(const LAS f32x4*)(rwT + e * 2052 + j * 256 + lane * 4);
;                             acc2[e] += y2[j][0] * (f32x2){w[0], w[0]}; acc2[e] += y2[j][1] * (f32x2){w[1], w[1]};
;                             acc2[e] += y2[j][2] * (f32x2){w[2], w[2]}; acc2[e] += y2[j][3] * (f32x2){w[3], w[3]}; }
;                         __builtin_amdgcn_sched_barrier(0);
;                     }
	v_pk_fma_f32 v[56:57], v[48:49], v[202:203], v[56:57] op_sel_hi:[1,0,1]
	s_nop 0
	v_pk_fma_f32 v[52:53], v[202:203], v[46:47], v[56:57] op_sel:[1,0,0]
	s_nop 0
	v_pk_fma_f32 v[52:53], v[204:205], v[50:51], v[52:53] op_sel_hi:[0,1,1]
	v_mov_b32_e32 v54, v205
	v_pk_fma_f32 v[52:53], v[54:55], v[44:45], v[52:53] op_sel_hi:[0,1,1]
	ds_read_b128 v[250:253], v238 offset:13456
	s_waitcnt lgkmcnt(8)
	v_pk_fma_f32 v[60:61], v[48:49], v[216:217], v[98:99] op_sel_hi:[1,0,1]
	s_nop 0
	v_pk_fma_f32 v[54:55], v[216:217], v[46:47], v[60:61] op_sel:[1,0,0]
	s_nop 0
	v_pk_fma_f32 v[54:55], v[218:219], v[50:51], v[54:55] op_sel_hi:[0,1,1]
	v_mov_b32_e32 v56, v219
	v_pk_fma_f32 v[90:91], v[56:57], v[44:45], v[54:55] op_sel_hi:[0,1,1]
	ds_read_b128 v[162:165], v238 offset:21664
	s_waitcnt lgkmcnt(8)
	v_pk_fma_f32 v[58:59], v[48:49], v[158:159], v[58:59] op_sel_hi:[1,0,1]
	s_nop 0
	v_pk_fma_f32 v[54:55], v[158:159], v[46:47], v[58:59] op_sel:[1,0,0]
	s_nop 0
	v_pk_fma_f32 v[54:55], v[160:161], v[50:51], v[54:55] op_sel_hi:[0,1,1]
	v_mov_b32_e32 v56, v161
	v_pk_fma_f32 v[54:55], v[56:57], v[44:45], v[54:55] op_sel_hi:[0,1,1]
	ds_read_b128 v[166:169], v238 offset:29872
	s_waitcnt lgkmcnt(8)
	v_pk_fma_f32 v[60:61], v[48:49], v[220:221], v[64:65] op_sel_hi:[1,0,1]
	s_nop 0
	v_pk_fma_f32 v[56:57], v[220:221], v[46:47], v[60:61] op_sel:[1,0,0]
	s_nop 0
	v_pk_fma_f32 v[56:57], v[222:223], v[50:51], v[56:57] op_sel_hi:[0,1,1]
	v_mov_b32_e32 v58, v223
	v_pk_fma_f32 v[56:57], v[58:59], v[44:45], v[56:57] op_sel_hi:[0,1,1]
	ds_read_b128 v[170:173], v238 offset:38080
	s_waitcnt lgkmcnt(8)
	v_pk_fma_f32 v[62:63], v[48:49], v[224:225], v[66:67] op_sel_hi:[1,0,1]
	s_nop 0
	v_pk_fma_f32 v[58:59], v[224:225], v[46:47], v[62:63] op_sel:[1,0,0]
	s_nop 0
	v_pk_fma_f32 v[58:59], v[226:227], v[50:51], v[58:59] op_sel_hi:[0,1,1]
	v_mov_b32_e32 v60, v227
	v_pk_fma_f32 v[58:59], v[60:61], v[44:45], v[58:59] op_sel_hi:[0,1,1]
	ds_read_b128 v[174:177], v238 offset:46288
	s_waitcnt lgkmcnt(8)
	v_pk_fma_f32 v[64:65], v[48:49], v[228:229], v[68:69] op_sel_hi:[1,0,1]
	s_nop 0
	v_pk_fma_f32 v[60:61], v[228:229], v[46:47], v[64:65] op_sel:[1,0,0]
	s_nop 0
	v_pk_fma_f32 v[60:61], v[230:231], v[50:51], v[60:61] op_sel_hi:[0,1,1]
	v_mov_b32_e32 v62, v231
	v_pk_fma_f32 v[60:61], v[62:63], v[44:45], v[60:61] op_sel_hi:[0,1,1]
	ds_read_b128 v[178:181], v238 offset:54496
	s_waitcnt lgkmcnt(8)
	v_pk_fma_f32 v[66:67], v[48:49], v[232:233], v[70:71] op_sel_hi:[1,0,1]
	s_nop 0
	v_pk_fma_f32 v[62:63], v[232:233], v[46:47], v[66:67] op_sel:[1,0,0]
	s_nop 0
	v_pk_fma_f32 v[62:63], v[234:235], v[50:51], v[62:63] op_sel_hi:[0,1,1]
	v_mov_b32_e32 v64, v235
	v_pk_fma_f32 v[62:63], v[64:65], v[44:45], v[62:63] op_sel_hi:[0,1,1]
	ds_read_b128 v[182:185], v238 offset:62704
	s_waitcnt lgkmcnt(8)
	v_pk_fma_f32 v[68:69], v[48:49], v[242:243], v[72:73] op_sel_hi:[1,0,1]
	s_nop 0
	v_pk_fma_f32 v[64:65], v[242:243], v[46:47], v[68:69] op_sel:[1,0,0]
	s_nop 0
	v_pk_fma_f32 v[64:65], v[244:245], v[50:51], v[64:65] op_sel_hi:[0,1,1]
	v_mov_b32_e32 v66, v245
	v_pk_fma_f32 v[64:65], v[66:67], v[44:45], v[64:65] op_sel_hi:[0,1,1]
	ds_read_b128 v[186:189], v25 offset:6144
	s_waitcnt lgkmcnt(8)
	v_pk_fma_f32 v[70:71], v[48:49], v[246:247], v[74:75] op_sel_hi:[1,0,1]
	s_nop 0
	v_pk_fma_f32 v[66:67], v[246:247], v[46:47], v[70:71] op_sel:[1,0,0]
	s_nop 0
	v_pk_fma_f32 v[66:67], v[248:249], v[50:51], v[66:67] op_sel_hi:[0,1,1]
	v_mov_b32_e32 v68, v249
	v_pk_fma_f32 v[66:67], v[68:69], v[44:45], v[66:67] op_sel_hi:[0,1,1]
	ds_read_b128 v[198:201], v25 offset:14352
	s_waitcnt lgkmcnt(8)
	v_pk_fma_f32 v[72:73], v[48:49], v[250:251], v[76:77] op_sel_hi:[1,0,1]
	s_nop 0
	v_pk_fma_f32 v[68:69], v[250:251], v[46:47], v[72:73] op_sel:[1,0,0]
	s_nop 0
	v_pk_fma_f32 v[68:69], v[252:253], v[50:51], v[68:69] op_sel_hi:[0,1,1]
	v_mov_b32_e32 v70, v253
	v_pk_fma_f32 v[68:69], v[70:71], v[44:45], v[68:69] op_sel_hi:[0,1,1]
	ds_read_b128 v[202:205], v25 offset:22560
	s_waitcnt lgkmcnt(8)
	v_pk_fma_f32 v[74:75], v[48:49], v[162:163], v[78:79] op_sel_hi:[1,0,1]
	s_nop 0
	v_pk_fma_f32 v[70:71], v[162:163], v[46:47], v[74:75] op_sel:[1,0,0]
	s_nop 0
	v_pk_fma_f32 v[70:71], v[164:165], v[50:51], v[70:71] op_sel_hi:[0,1,1]
	v_mov_b32_e32 v72, v165
	v_pk_fma_f32 v[70:71], v[72:73], v[44:45], v[70:71] op_sel_hi:[0,1,1]
	ds_read_b128 v[216:219], v25 offset:30768
	s_waitcnt lgkmcnt(8)
	v_pk_fma_f32 v[76:77], v[48:49], v[166:167], v[80:81] op_sel_hi:[1,0,1]
	s_nop 0
	v_pk_fma_f32 v[72:73], v[166:167], v[46:47], v[76:77] op_sel:[1,0,0]
	s_nop 0
	v_pk_fma_f32 v[72:73], v[168:169], v[50:51], v[72:73] op_sel_hi:[0,1,1]
	v_mov_b32_e32 v74, v169
	v_pk_fma_f32 v[72:73], v[74:75], v[44:45], v[72:73] op_sel_hi:[0,1,1]
	ds_read_b128 v[158:161], v25 offset:38976
	s_waitcnt lgkmcnt(8)
	v_pk_fma_f32 v[78:79], v[48:49], v[170:171], v[82:83] op_sel_hi:[1,0,1]
	s_nop 0
	v_pk_fma_f32 v[74:75], v[170:171], v[46:47], v[78:79] op_sel:[1,0,0]
	s_nop 0
	v_pk_fma_f32 v[74:75], v[172:173], v[50:51], v[74:75] op_sel_hi:[0,1,1]
	v_mov_b32_e32 v76, v173
	v_pk_fma_f32 v[74:75], v[76:77], v[44:45], v[74:75] op_sel_hi:[0,1,1]
	ds_read_b128 v[220:223], v25 offset:47184
	s_waitcnt lgkmcnt(8)
	v_pk_fma_f32 v[80:81], v[48:49], v[174:175], v[84:85] op_sel_hi:[1,0,1]
	s_nop 0
	v_pk_fma_f32 v[76:77], v[174:175], v[46:47], v[80:81] op_sel:[1,0,0]
	s_nop 0
	v_pk_fma_f32 v[76:77], v[176:177], v[50:51], v[76:77] op_sel_hi:[0,1,1]
	v_mov_b32_e32 v78, v177
	v_pk_fma_f32 v[76:77], v[78:79], v[44:45], v[76:77] op_sel_hi:[0,1,1]
	ds_read_b128 v[224:227], v25 offset:55392
	s_waitcnt lgkmcnt(8)
; #define LAS __attribute__((address_space(3)))
; __global__ void __launch_bounds__(NTHREADS, 2) hybrid_fwd(Args a) {
;     ...
; #pragma unroll
;                     for (int j = 0; j < 8; ++j) {
; #pragma unroll
;                         for (int e = 0; e < 16; ++e) { const f32x4 w = *(const LAS f32x4*)(rwT + e * 2052 + j * 256 + lane * 4);
;                             acc2[e] += y2[j][0] * (f32x2){w[0], w[0]}; acc2[e] += y2[j][1] * (f32x2){w[1], w[1]};
;                             acc2[e] += y2[j][2] * (f32x2){w[2], w[2]}; acc2[e] += y2[j][3] * (f32x2){w[3], w[3]}; }
;                         __builtin_amdgcn_sched_barrier(0);
;                     }
	v_pk_fma_f32 v[82:83], v[48:49], v[178:179], v[86:87] op_sel_hi:[1,0,1]
	s_nop 0
	v_pk_fma_f32 v[78:79], v[178:179], v[46:47], v[82:83] op_sel:[1,0,0]
	s_nop 0
	v_pk_fma_f32 v[78:79], v[180:181], v[50:51], v[78:79] op_sel_hi:[0,1,1]
	v_mov_b32_e32 v80, v181
	v_pk_fma_f32 v[78:79], v[80:81], v[44:45], v[78:79] op_sel_hi:[0,1,1]
	ds_read_b128 v[228:231], v25 offset:63600
	s_waitcnt lgkmcnt(8)
	v_pk_fma_f32 v[48:49], v[48:49], v[182:183], v[88:89] op_sel_hi:[1,0,1]
	s_nop 0
	v_pk_fma_f32 v[46:47], v[182:183], v[46:47], v[48:49] op_sel:[1,0,0]
	v_mov_b32_e32 v48, v185
	v_pk_fma_f32 v[46:47], v[184:185], v[50:51], v[46:47] op_sel_hi:[0,1,1]
	v_pk_fma_f32 v[80:81], v[48:49], v[44:45], v[46:47] op_sel_hi:[0,1,1]
	ds_read_b128 v[232:235], v238 offset:6272
	s_waitcnt lgkmcnt(8)
	v_pk_fma_f32 v[48:49], v[40:41], v[186:187], v[52:53] op_sel_hi:[1,0,1]
	s_nop 0
	v_pk_fma_f32 v[44:45], v[186:187], v[38:39], v[48:49] op_sel:[1,0,0]
	s_nop 0
	v_pk_fma_f32 v[44:45], v[188:189], v[42:43], v[44:45] op_sel_hi:[0,1,1]
	v_mov_b32_e32 v46, v189
	v_pk_fma_f32 v[44:45], v[46:47], v[36:37], v[44:45] op_sel_hi:[0,1,1]
	ds_read_b128 v[242:245], v238 offset:14480
	s_waitcnt lgkmcnt(8)
	v_pk_fma_f32 v[50:51], v[40:41], v[198:199], v[90:91] op_sel_hi:[1,0,1]
	s_nop 0
	v_pk_fma_f32 v[46:47], v[198:199], v[38:39], v[50:51] op_sel:[1,0,0]
	s_nop 0
	v_pk_fma_f32 v[46:47], v[200:201], v[42:43], v[46:47] op_sel_hi:[0,1,1]
	v_mov_b32_e32 v48, v201
	v_pk_fma_f32 v[82:83], v[48:49], v[36:37], v[46:47] op_sel_hi:[0,1,1]
	ds_read_b128 v[246:249], v238 offset:22688
	s_waitcnt lgkmcnt(8)
	v_pk_fma_f32 v[50:51], v[40:41], v[202:203], v[54:55] op_sel_hi:[1,0,1]
	s_nop 0
	v_pk_fma_f32 v[46:47], v[202:203], v[38:39], v[50:51] op_sel:[1,0,0]
	s_nop 0
	v_pk_fma_f32 v[46:47], v[204:205], v[42:43], v[46:47] op_sel_hi:[0,1,1]
	v_mov_b32_e32 v48, v205
	v_pk_fma_f32 v[46:47], v[48:49], v[36:37], v[46:47] op_sel_hi:[0,1,1]
	ds_read_b128 v[250:253], v238 offset:30896
	s_waitcnt lgkmcnt(8)
	v_pk_fma_f32 v[52:53], v[40:41], v[216:217], v[56:57] op_sel_hi:[1,0,1]
	s_nop 0
	v_pk_fma_f32 v[48:49], v[216:217], v[38:39], v[52:53] op_sel:[1,0,0]
	s_nop 0
	v_pk_fma_f32 v[48:49], v[218:219], v[42:43], v[48:49] op_sel_hi:[0,1,1]
	v_mov_b32_e32 v50, v219
	v_pk_fma_f32 v[48:49], v[50:51], v[36:37], v[48:49] op_sel_hi:[0,1,1]
	ds_read_b128 v[162:165], v238 offset:39104
	s_waitcnt lgkmcnt(8)
	v_pk_fma_f32 v[54:55], v[40:41], v[158:159], v[58:59] op_sel_hi:[1,0,1]
	s_nop 0
	v_pk_fma_f32 v[50:51], v[158:159], v[38:39], v[54:55] op_sel:[1,0,0]
	s_nop 0
	v_pk_fma_f32 v[50:51], v[160:161], v[42:43], v[50:51] op_sel_hi:[0,1,1]
	v_mov_b32_e32 v52, v161
	v_pk_fma_f32 v[50:51], v[52:53], v[36:37], v[50:51] op_sel_hi:[0,1,1]
	ds_read_b128 v[166:169], v238 offset:47312
	s_waitcnt lgkmcnt(8)
	v_pk_fma_f32 v[56:57], v[40:41], v[220:221], v[60:61] op_sel_hi:[1,0,1]
	s_nop 0
	v_pk_fma_f32 v[52:53], v[220:221], v[38:39], v[56:57] op_sel:[1,0,0]
	s_nop 0
	v_pk_fma_f32 v[52:53], v[222:223], v[42:43], v[52:53] op_sel_hi:[0,1,1]
	v_mov_b32_e32 v54, v223
	v_pk_fma_f32 v[52:53], v[54:55], v[36:37], v[52:53] op_sel_hi:[0,1,1]
	ds_read_b128 v[170:173], v238 offset:55520
	s_waitcnt lgkmcnt(8)
	v_pk_fma_f32 v[58:59], v[40:41], v[224:225], v[62:63] op_sel_hi:[1,0,1]
	s_nop 0
	v_pk_fma_f32 v[54:55], v[224:225], v[38:39], v[58:59] op_sel:[1,0,0]
	s_nop 0
	v_pk_fma_f32 v[54:55], v[226:227], v[42:43], v[54:55] op_sel_hi:[0,1,1]
	v_mov_b32_e32 v56, v227
	v_pk_fma_f32 v[54:55], v[56:57], v[36:37], v[54:55] op_sel_hi:[0,1,1]
	ds_read_b128 v[174:177], v238 offset:63728
	s_waitcnt lgkmcnt(8)
	v_pk_fma_f32 v[60:61], v[40:41], v[228:229], v[64:65] op_sel_hi:[1,0,1]
	s_nop 0
	v_pk_fma_f32 v[56:57], v[228:229], v[38:39], v[60:61] op_sel:[1,0,0]
	s_nop 0
	v_pk_fma_f32 v[56:57], v[230:231], v[42:43], v[56:57] op_sel_hi:[0,1,1]
	v_mov_b32_e32 v58, v231
	v_pk_fma_f32 v[56:57], v[58:59], v[36:37], v[56:57] op_sel_hi:[0,1,1]
	ds_read_b128 v[178:181], v25 offset:7168
	s_waitcnt lgkmcnt(8)
	v_pk_fma_f32 v[62:63], v[40:41], v[232:233], v[66:67] op_sel_hi:[1,0,1]
	s_nop 0
	v_pk_fma_f32 v[58:59], v[232:233], v[38:39], v[62:63] op_sel:[1,0,0]
	s_nop 0
	v_pk_fma_f32 v[58:59], v[234:235], v[42:43], v[58:59] op_sel_hi:[0,1,1]
	v_mov_b32_e32 v60, v235
	v_pk_fma_f32 v[58:59], v[60:61], v[36:37], v[58:59] op_sel_hi:[0,1,1]
	ds_read_b128 v[182:185], v25 offset:15376
	s_waitcnt lgkmcnt(8)
	v_pk_fma_f32 v[64:65], v[40:41], v[242:243], v[68:69] op_sel_hi:[1,0,1]
	s_nop 0
	v_pk_fma_f32 v[60:61], v[242:243], v[38:39], v[64:65] op_sel:[1,0,0]
	s_nop 0
	v_pk_fma_f32 v[60:61], v[244:245], v[42:43], v[60:61] op_sel_hi:[0,1,1]
	v_mov_b32_e32 v62, v245
	v_pk_fma_f32 v[60:61], v[62:63], v[36:37], v[60:61] op_sel_hi:[0,1,1]
	ds_read_b128 v[186:189], v25 offset:23584
	s_waitcnt lgkmcnt(8)
	v_pk_fma_f32 v[66:67], v[40:41], v[246:247], v[70:71] op_sel_hi:[1,0,1]
	s_nop 0
	v_pk_fma_f32 v[62:63], v[246:247], v[38:39], v[66:67] op_sel:[1,0,0]
	s_nop 0
	v_pk_fma_f32 v[62:63], v[248:249], v[42:43], v[62:63] op_sel_hi:[0,1,1]
	v_mov_b32_e32 v64, v249
	v_pk_fma_f32 v[62:63], v[64:65], v[36:37], v[62:63] op_sel_hi:[0,1,1]
	ds_read_b128 v[198:201], v25 offset:31792
	s_waitcnt lgkmcnt(8)
	v_pk_fma_f32 v[68:69], v[40:41], v[250:251], v[72:73] op_sel_hi:[1,0,1]
	s_nop 0
	v_pk_fma_f32 v[64:65], v[250:251], v[38:39], v[68:69] op_sel:[1,0,0]
	s_nop 0
	v_pk_fma_f32 v[64:65], v[252:253], v[42:43], v[64:65] op_sel_hi:[0,1,1]
	v_mov_b32_e32 v66, v253
	v_pk_fma_f32 v[64:65], v[66:67], v[36:37], v[64:65] op_sel_hi:[0,1,1]
	ds_read_b128 v[202:205], v25 offset:40000
	s_waitcnt lgkmcnt(8)
; #define LAS __attribute__((address_space(3)))
; __global__ void __launch_bounds__(NTHREADS, 2) hybrid_fwd(Args a) {
;     ...
; #pragma unroll
;                     for (int j = 0; j < 8; ++j) {
; #pragma unroll
;                         for (int e = 0; e < 16; ++e) { const f32x4 w = *(const LAS f32x4*)(rwT + e * 2052 + j * 256 + lane * 4);
;                             acc2[e] += y2[j][0] * (f32x2){w[0], w[0]}; acc2[e] += y2[j][1] * (f32x2){w[1], w[1]};
;                             acc2[e] += y2[j][2] * (f32x2){w[2], w[2]}; acc2[e] += y2[j][3] * (f32x2){w[3], w[3]}; }
;                         __builtin_amdgcn_sched_barrier(0);
;                     }
	v_pk_fma_f32 v[70:71], v[40:41], v[162:163], v[74:75] op_sel_hi:[1,0,1]
	s_nop 0
	v_pk_fma_f32 v[66:67], v[162:163], v[38:39], v[70:71] op_sel:[1,0,0]
	s_nop 0
	v_pk_fma_f32 v[66:67], v[164:165], v[42:43], v[66:67] op_sel_hi:[0,1,1]
	v_mov_b32_e32 v68, v165
	v_pk_fma_f32 v[66:67], v[68:69], v[36:37], v[66:67] op_sel_hi:[0,1,1]
	ds_read_b128 v[216:219], v25 offset:48208
	s_waitcnt lgkmcnt(8)
	v_pk_fma_f32 v[72:73], v[40:41], v[166:167], v[76:77] op_sel_hi:[1,0,1]
	s_nop 0
	v_pk_fma_f32 v[68:69], v[166:167], v[38:39], v[72:73] op_sel:[1,0,0]
	s_nop 0
	v_pk_fma_f32 v[68:69], v[168:169], v[42:43], v[68:69] op_sel_hi:[0,1,1]
	v_mov_b32_e32 v70, v169
	v_pk_fma_f32 v[68:69], v[70:71], v[36:37], v[68:69] op_sel_hi:[0,1,1]
	ds_read_b128 v[158:161], v25 offset:56416
	s_waitcnt lgkmcnt(8)
	v_pk_fma_f32 v[74:75], v[40:41], v[170:171], v[78:79] op_sel_hi:[1,0,1]
	s_nop 0
	v_pk_fma_f32 v[70:71], v[170:171], v[38:39], v[74:75] op_sel:[1,0,0]
	s_nop 0
	v_pk_fma_f32 v[70:71], v[172:173], v[42:43], v[70:71] op_sel_hi:[0,1,1]
	v_mov_b32_e32 v72, v173
	v_pk_fma_f32 v[70:71], v[72:73], v[36:37], v[70:71] op_sel_hi:[0,1,1]
	ds_read_b128 v[220:223], v25 offset:64624
	s_waitcnt lgkmcnt(8)
	v_pk_fma_f32 v[40:41], v[40:41], v[174:175], v[80:81] op_sel_hi:[1,0,1]
	s_nop 0
	v_pk_fma_f32 v[38:39], v[174:175], v[38:39], v[40:41] op_sel:[1,0,0]
	v_mov_b32_e32 v40, v177
	v_pk_fma_f32 v[38:39], v[176:177], v[42:43], v[38:39] op_sel_hi:[0,1,1]
	v_pk_fma_f32 v[72:73], v[40:41], v[36:37], v[38:39] op_sel_hi:[0,1,1]
	ds_read_b128 v[224:227], v238 offset:7296
	s_waitcnt lgkmcnt(8)
	v_pk_fma_f32 v[40:41], v[22:23], v[178:179], v[44:45] op_sel_hi:[1,0,1]
	s_nop 0
	v_pk_fma_f32 v[36:37], v[178:179], v[18:19], v[40:41] op_sel:[1,0,0]
	s_nop 0
	v_pk_fma_f32 v[36:37], v[180:181], v[20:21], v[36:37] op_sel_hi:[0,1,1]
	v_mov_b32_e32 v38, v181
	v_pk_fma_f32 v[36:37], v[38:39], v[16:17], v[36:37] op_sel_hi:[0,1,1]
	ds_read_b128 v[228:231], v238 offset:15504
	s_waitcnt lgkmcnt(8)
	v_pk_fma_f32 v[42:43], v[22:23], v[182:183], v[82:83] op_sel_hi:[1,0,1]
	s_nop 0
	v_pk_fma_f32 v[38:39], v[182:183], v[18:19], v[42:43] op_sel:[1,0,0]
	s_nop 0
	v_pk_fma_f32 v[38:39], v[184:185], v[20:21], v[38:39] op_sel_hi:[0,1,1]
	v_mov_b32_e32 v40, v185
	v_pk_fma_f32 v[38:39], v[40:41], v[16:17], v[38:39] op_sel_hi:[0,1,1]
	ds_read_b128 v[232:235], v238 offset:23712
	s_waitcnt lgkmcnt(8)
	v_pk_fma_f32 v[44:45], v[22:23], v[186:187], v[46:47] op_sel_hi:[1,0,1]
	s_nop 0
	v_pk_fma_f32 v[40:41], v[186:187], v[18:19], v[44:45] op_sel:[1,0,0]
	s_nop 0
	v_pk_fma_f32 v[40:41], v[188:189], v[20:21], v[40:41] op_sel_hi:[0,1,1]
	v_mov_b32_e32 v42, v189
	v_pk_fma_f32 v[40:41], v[42:43], v[16:17], v[40:41] op_sel_hi:[0,1,1]
	ds_read_b128 v[242:245], v238 offset:31920
	s_waitcnt lgkmcnt(8)
	v_pk_fma_f32 v[46:47], v[22:23], v[198:199], v[48:49] op_sel_hi:[1,0,1]
	s_nop 0
	v_pk_fma_f32 v[42:43], v[198:199], v[18:19], v[46:47] op_sel:[1,0,0]
	ds_read_b128 v[246:249], v238 offset:40128
	v_pk_fma_f32 v[42:43], v[200:201], v[20:21], v[42:43] op_sel_hi:[0,1,1]
	v_mov_b32_e32 v44, v201
	v_pk_fma_f32 v[44:45], v[44:45], v[16:17], v[42:43] op_sel_hi:[0,1,1]
	s_waitcnt lgkmcnt(8)
	v_pk_fma_f32 v[42:43], v[22:23], v[202:203], v[50:51] op_sel_hi:[1,0,1]
	s_nop 0
	v_pk_fma_f32 v[42:43], v[202:203], v[18:19], v[42:43] op_sel:[1,0,0]
	v_mov_b32_e32 v46, v205
	v_pk_fma_f32 v[42:43], v[204:205], v[20:21], v[42:43] op_sel_hi:[0,1,1]
	v_pk_fma_f32 v[42:43], v[46:47], v[16:17], v[42:43] op_sel_hi:[0,1,1]
	ds_read_b128 v[250:253], v238 offset:48336
	s_waitcnt lgkmcnt(8)
	v_pk_fma_f32 v[50:51], v[22:23], v[216:217], v[52:53] op_sel_hi:[1,0,1]
	s_nop 0
	v_pk_fma_f32 v[46:47], v[216:217], v[18:19], v[50:51] op_sel:[1,0,0]
	s_nop 0
	v_pk_fma_f32 v[46:47], v[218:219], v[20:21], v[46:47] op_sel_hi:[0,1,1]
	v_mov_b32_e32 v48, v219
	v_pk_fma_f32 v[46:47], v[48:49], v[16:17], v[46:47] op_sel_hi:[0,1,1]
	ds_read_b128 v[162:165], v238 offset:56544
	s_waitcnt lgkmcnt(8)
	v_pk_fma_f32 v[52:53], v[22:23], v[158:159], v[54:55] op_sel_hi:[1,0,1]
	s_nop 0
	v_pk_fma_f32 v[48:49], v[158:159], v[18:19], v[52:53] op_sel:[1,0,0]
	s_nop 0
	v_pk_fma_f32 v[48:49], v[160:161], v[20:21], v[48:49] op_sel_hi:[0,1,1]
	v_mov_b32_e32 v50, v161
	v_pk_fma_f32 v[48:49], v[50:51], v[16:17], v[48:49] op_sel_hi:[0,1,1]
	ds_read_b128 v[166:169], v238 offset:64752
	s_waitcnt lgkmcnt(8)
	v_pk_fma_f32 v[54:55], v[22:23], v[220:221], v[56:57] op_sel_hi:[1,0,1]
	s_nop 0
	v_pk_fma_f32 v[50:51], v[220:221], v[18:19], v[54:55] op_sel:[1,0,0]
	s_nop 0
	v_pk_fma_f32 v[50:51], v[222:223], v[20:21], v[50:51] op_sel_hi:[0,1,1]
	v_mov_b32_e32 v52, v223
	v_pk_fma_f32 v[50:51], v[52:53], v[16:17], v[50:51] op_sel_hi:[0,1,1]
	s_waitcnt lgkmcnt(7)
	v_pk_fma_f32 v[56:57], v[22:23], v[224:225], v[58:59] op_sel_hi:[1,0,1]
	s_nop 0
	v_pk_fma_f32 v[52:53], v[224:225], v[18:19], v[56:57] op_sel:[1,0,0]
	s_nop 0
	v_pk_fma_f32 v[52:53], v[226:227], v[20:21], v[52:53] op_sel_hi:[0,1,1]
	v_mov_b32_e32 v54, v227
	v_pk_fma_f32 v[52:53], v[54:55], v[16:17], v[52:53] op_sel_hi:[0,1,1]
	s_waitcnt lgkmcnt(6)
	v_pk_fma_f32 v[58:59], v[22:23], v[228:229], v[60:61] op_sel_hi:[1,0,1]
	s_nop 0
	v_pk_fma_f32 v[54:55], v[228:229], v[18:19], v[58:59] op_sel:[1,0,0]
	s_nop 0
	v_pk_fma_f32 v[54:55], v[230:231], v[20:21], v[54:55] op_sel_hi:[0,1,1]
	v_mov_b32_e32 v56, v231
	v_pk_fma_f32 v[54:55], v[56:57], v[16:17], v[54:55] op_sel_hi:[0,1,1]
	s_waitcnt lgkmcnt(5)
	v_pk_fma_f32 v[60:61], v[22:23], v[232:233], v[62:63] op_sel_hi:[1,0,1]
	s_nop 0
	v_pk_fma_f32 v[56:57], v[232:233], v[18:19], v[60:61] op_sel:[1,0,0]
	s_nop 0
	v_pk_fma_f32 v[56:57], v[234:235], v[20:21], v[56:57] op_sel_hi:[0,1,1]
	v_mov_b32_e32 v58, v235
	v_pk_fma_f32 v[56:57], v[58:59], v[16:17], v[56:57] op_sel_hi:[0,1,1]
	s_waitcnt lgkmcnt(4)
; #define WS_STEP(ctrl) v += __int_as_float(__builtin_amdgcn_update_dpp(0, __float_as_int(v), (ctrl), 0xf, 0xf, true))
; __device__ __forceinline__ float wave_sum(float v) {
;     ...
;     WS_STEP(0xB1); WS_STEP(0x4E); WS_STEP(0x124); WS_STEP(0x128);
;     ...
;     const auto r16 = __builtin_amdgcn_permlane16_swap(__float_as_uint(v), __float_as_uint(v), false, false);
;     v = __uint_as_float(r16[0]) + __uint_as_float(r16[1]);
;     const auto rr = __builtin_amdgcn_permlane32_swap(__float_as_uint(v), __float_as_uint(v), false, false);
;     return __uint_as_float(rr[0]) + __uint_as_float(rr[1]);
; }
	v_pk_fma_f32 v[62:63], v[22:23], v[242:243], v[64:65] op_sel_hi:[1,0,1]
	s_nop 0
	v_pk_fma_f32 v[58:59], v[242:243], v[18:19], v[62:63] op_sel:[1,0,0]
	s_nop 0
	v_pk_fma_f32 v[58:59], v[244:245], v[20:21], v[58:59] op_sel_hi:[0,1,1]
	v_mov_b32_e32 v60, v245
	v_pk_fma_f32 v[58:59], v[60:61], v[16:17], v[58:59] op_sel_hi:[0,1,1]
	s_waitcnt lgkmcnt(3)
	v_pk_fma_f32 v[64:65], v[22:23], v[246:247], v[66:67] op_sel_hi:[1,0,1]
	s_nop 0
	v_pk_fma_f32 v[60:61], v[246:247], v[18:19], v[64:65] op_sel:[1,0,0]
	s_nop 0
	v_pk_fma_f32 v[60:61], v[248:249], v[20:21], v[60:61] op_sel_hi:[0,1,1]
	v_mov_b32_e32 v62, v249
	v_pk_fma_f32 v[60:61], v[62:63], v[16:17], v[60:61] op_sel_hi:[0,1,1]
	s_waitcnt lgkmcnt(2)
	v_pk_fma_f32 v[66:67], v[22:23], v[250:251], v[68:69] op_sel_hi:[1,0,1]
	s_nop 0
	v_pk_fma_f32 v[62:63], v[250:251], v[18:19], v[66:67] op_sel:[1,0,0]
	s_nop 0
	v_pk_fma_f32 v[62:63], v[252:253], v[20:21], v[62:63] op_sel_hi:[0,1,1]
	v_mov_b32_e32 v64, v253
	v_pk_fma_f32 v[62:63], v[64:65], v[16:17], v[62:63] op_sel_hi:[0,1,1]
	s_waitcnt lgkmcnt(1)
	v_pk_fma_f32 v[68:69], v[22:23], v[162:163], v[70:71] op_sel_hi:[1,0,1]
	s_nop 0
	v_pk_fma_f32 v[64:65], v[162:163], v[18:19], v[68:69] op_sel:[1,0,0]
	s_nop 0
	v_pk_fma_f32 v[64:65], v[164:165], v[20:21], v[64:65] op_sel_hi:[0,1,1]
	v_mov_b32_e32 v66, v165
	v_pk_fma_f32 v[64:65], v[66:67], v[16:17], v[64:65] op_sel_hi:[0,1,1]
	s_waitcnt lgkmcnt(0)
	v_pk_fma_f32 v[22:23], v[22:23], v[166:167], v[72:73] op_sel_hi:[1,0,1]
	s_nop 0
	v_pk_fma_f32 v[18:19], v[166:167], v[18:19], v[22:23] op_sel:[1,0,0]
	s_nop 0
	v_pk_fma_f32 v[18:19], v[168:169], v[20:21], v[18:19] op_sel_hi:[0,1,1]
	v_mov_b32_e32 v20, v169
	v_pk_fma_f32 v[16:17], v[20:21], v[16:17], v[18:19] op_sel_hi:[0,1,1]
	s_nop 1
	v_permlane32_swap_b32_e32 v16, v17
	v_permlane32_swap_b32_e32 v36, v37
	v_permlane32_swap_b32_e32 v38, v39
	v_permlane32_swap_b32_e32 v40, v41
	v_permlane32_swap_b32_e32 v42, v43
	v_permlane32_swap_b32_e32 v44, v45
	v_permlane32_swap_b32_e32 v46, v47
	v_permlane32_swap_b32_e32 v48, v49
	v_permlane32_swap_b32_e32 v50, v51
	v_permlane32_swap_b32_e32 v52, v53
	v_permlane32_swap_b32_e32 v54, v55
	v_permlane32_swap_b32_e32 v56, v57
	v_permlane32_swap_b32_e32 v58, v59
	v_permlane32_swap_b32_e32 v60, v61
	v_permlane32_swap_b32_e32 v62, v63
	v_permlane32_swap_b32_e32 v64, v65
	v_add_f32_e32 v16, v16, v17
	v_add_f32_e32 v36, v36, v37
	v_add_f32_e32 v38, v38, v39
	v_add_f32_e32 v40, v40, v41
	v_add_f32_e32 v42, v42, v43
	v_add_f32_e32 v44, v44, v45
	v_add_f32_e32 v46, v46, v47
	v_add_f32_e32 v48, v48, v49
	v_add_f32_e32 v50, v50, v51
	v_add_f32_e32 v52, v52, v53
	v_add_f32_e32 v54, v54, v55
	v_add_f32_e32 v56, v56, v57
	v_add_f32_e32 v58, v58, v59
	v_add_f32_e32 v60, v60, v61
	v_add_f32_e32 v62, v62, v63
	v_add_f32_e32 v64, v64, v65
	s_nop 1
	v_add_f32_dpp v18, v36, v36 quad_perm:[1,0,3,2] row_mask:0xf bank_mask:0xf bound_ctrl:1
	s_nop 0
	v_add_f32_dpp v16, v16, v16 quad_perm:[1,0,3,2] row_mask:0xf bank_mask:0xf bound_ctrl:1
	v_add_f32_dpp v36, v62, v62 quad_perm:[1,0,3,2] row_mask:0xf bank_mask:0xf bound_ctrl:1
	v_add_f32_dpp v18, v18, v18 quad_perm:[2,3,0,1] row_mask:0xf bank_mask:0xf bound_ctrl:1
	v_add_f32_dpp v16, v16, v16 quad_perm:[2,3,0,1] row_mask:0xf bank_mask:0xf bound_ctrl:1
	v_add_f32_dpp v36, v36, v36 quad_perm:[2,3,0,1] row_mask:0xf bank_mask:0xf bound_ctrl:1
	v_add_f32_dpp v18, v18, v18 row_ror:4 row_mask:0xf bank_mask:0xf bound_ctrl:1
	v_add_f32_dpp v16, v16, v16 row_ror:4 row_mask:0xf bank_mask:0xf bound_ctrl:1
	v_add_f32_dpp v36, v36, v36 row_ror:4 row_mask:0xf bank_mask:0xf bound_ctrl:1
	v_add_f32_dpp v18, v18, v18 row_ror:8 row_mask:0xf bank_mask:0xf bound_ctrl:1
	v_mov_b32_e32 v19, v18
	s_nop 1
	v_permlane16_swap_b32_e32 v18, v19
	v_add_f32_e32 v18, v18, v19
	v_mov_b32_e32 v19, v18
	s_nop 1
	s_nop 0
	v_mov_b32_e32 v18, v18
	s_nop 0
	v_add_f32_dpp v19, v38, v38 quad_perm:[1,0,3,2] row_mask:0xf bank_mask:0xf bound_ctrl:1
	v_mul_f32_e32 v18, 0xbfb8aa3b, v18
	v_exp_f32_e32 v18, v18
	v_add_f32_dpp v19, v19, v19 quad_perm:[2,3,0,1] row_mask:0xf bank_mask:0xf bound_ctrl:1
	v_add_f32_dpp v16, v16, v16 row_ror:8 row_mask:0xf bank_mask:0xf bound_ctrl:1
	v_add_f32_dpp v36, v36, v36 row_ror:8 row_mask:0xf bank_mask:0xf bound_ctrl:1
	v_add_f32_dpp v19, v19, v19 row_ror:4 row_mask:0xf bank_mask:0xf bound_ctrl:1
	v_add_f32_e32 v18, 1.0, v18
	v_rcp_f32_e32 v18, v18
	v_add_f32_dpp v19, v19, v19 row_ror:8 row_mask:0xf bank_mask:0xf bound_ctrl:1
	v_mov_b32_e32 v20, v19
	s_nop 1
	v_permlane16_swap_b32_e32 v19, v20
	v_add_f32_e32 v19, v19, v20
	v_mov_b32_e32 v20, v19
	s_nop 1
	s_nop 0
	v_mov_b32_e32 v19, v19
	s_nop 0
	v_add_f32_dpp v20, v40, v40 quad_perm:[1,0,3,2] row_mask:0xf bank_mask:0xf bound_ctrl:1
	v_mul_f32_e32 v19, 0xbfb8aa3b, v19
	v_exp_f32_e32 v19, v19
	v_add_f32_dpp v20, v20, v20 quad_perm:[2,3,0,1] row_mask:0xf bank_mask:0xf bound_ctrl:1
	v_add_f32_dpp v40, v64, v64 quad_perm:[1,0,3,2] row_mask:0xf bank_mask:0xf bound_ctrl:1
	v_mov_b32_e32 v38, v36
	v_add_f32_dpp v20, v20, v20 row_ror:4 row_mask:0xf bank_mask:0xf bound_ctrl:1
	v_add_f32_e32 v19, 1.0, v19
	v_rcp_f32_e32 v19, v19
	v_add_f32_dpp v20, v20, v20 row_ror:8 row_mask:0xf bank_mask:0xf bound_ctrl:1
	v_mov_b32_e32 v21, v20
	s_nop 1
	v_permlane16_swap_b32_e32 v20, v21
	v_add_f32_e32 v20, v20, v21
	v_mov_b32_e32 v21, v20
	s_nop 1
	s_nop 0
	v_mov_b32_e32 v20, v20
	s_nop 0
	v_add_f32_dpp v21, v44, v44 quad_perm:[1,0,3,2] row_mask:0xf bank_mask:0xf bound_ctrl:1
	v_mul_f32_e32 v20, 0xbfb8aa3b, v20
	v_exp_f32_e32 v20, v20
	v_add_f32_dpp v21, v21, v21 quad_perm:[2,3,0,1] row_mask:0xf bank_mask:0xf bound_ctrl:1
	v_mov_b32_e32 v44, v16
	s_nop 1
	v_permlane16_swap_b32_e32 v16, v44
; #define WS_STEP(ctrl) v += __int_as_float(__builtin_amdgcn_update_dpp(0, __float_as_int(v), (ctrl), 0xf, 0xf, true))
; __device__ __forceinline__ float wave_sum(float v) {
;     ...
;     WS_STEP(0xB1); WS_STEP(0x4E); WS_STEP(0x124); WS_STEP(0x128);
;     ...
;     const auto r16 = __builtin_amdgcn_permlane16_swap(__float_as_uint(v), __float_as_uint(v), false, false);
;     v = __uint_as_float(r16[0]) + __uint_as_float(r16[1]);
;     const auto rr = __builtin_amdgcn_permlane32_swap(__float_as_uint(v), __float_as_uint(v), false, false);
;     return __uint_as_float(rr[0]) + __uint_as_float(rr[1]);
; }
	v_add_f32_dpp v21, v21, v21 row_ror:4 row_mask:0xf bank_mask:0xf bound_ctrl:1
	v_add_f32_e32 v20, 1.0, v20
	v_rcp_f32_e32 v70, v20
	v_add_f32_dpp v21, v21, v21 row_ror:8 row_mask:0xf bank_mask:0xf bound_ctrl:1
	v_mov_b32_e32 v22, v21
	s_nop 1
	v_permlane16_swap_b32_e32 v21, v22
	v_add_f32_e32 v21, v21, v22
	v_mov_b32_e32 v22, v21
	s_nop 1
	s_nop 0
	v_mov_b32_e32 v21, v21
	s_nop 0
	v_add_f32_dpp v22, v42, v42 quad_perm:[1,0,3,2] row_mask:0xf bank_mask:0xf bound_ctrl:1
	v_mul_f32_e32 v21, 0xbfb8aa3b, v21
	v_exp_f32_e32 v21, v21
	v_add_f32_dpp v22, v22, v22 quad_perm:[2,3,0,1] row_mask:0xf bank_mask:0xf bound_ctrl:1
	v_add_f32_e32 v79, v14, v70
	v_add_f32_e32 v44, v16, v44
	v_add_f32_dpp v22, v22, v22 row_ror:4 row_mask:0xf bank_mask:0xf bound_ctrl:1
	v_add_f32_e32 v20, 1.0, v21
	v_rcp_f32_e32 v72, v20
	v_add_f32_dpp v22, v22, v22 row_ror:8 row_mask:0xf bank_mask:0xf bound_ctrl:1
	v_mov_b32_e32 v23, v22
	s_nop 1
	v_permlane16_swap_b32_e32 v22, v23
	v_add_f32_e32 v69, v22, v23
	s_nop 0
	v_add_f32_dpp v22, v46, v46 quad_perm:[1,0,3,2] row_mask:0xf bank_mask:0xf bound_ctrl:1
	v_pk_add_f32 v[20:21], v[12:13], v[18:19]
	v_add_f32_e32 v80, v15, v72
	v_add_f32_dpp v22, v22, v22 quad_perm:[2,3,0,1] row_mask:0xf bank_mask:0xf bound_ctrl:1
	v_cmp_gt_f32_e32 vcc, v21, v20
	v_add_f32_dpp v40, v40, v40 quad_perm:[2,3,0,1] row_mask:0xf bank_mask:0xf bound_ctrl:1
	v_add_f32_dpp v22, v22, v22 row_ror:4 row_mask:0xf bank_mask:0xf bound_ctrl:1
	v_cndmask_b32_e32 v16, v20, v21, vcc
	v_cmp_gt_f32_e64 s[6:7], v79, v16
	v_add_f32_dpp v22, v22, v22 row_ror:8 row_mask:0xf bank_mask:0xf bound_ctrl:1
	v_mov_b32_e32 v23, v22
	s_nop 1
	v_permlane16_swap_b32_e32 v22, v23
	v_add_f32_e32 v73, v22, v23
	s_nop 0
	v_add_f32_dpp v22, v48, v48 quad_perm:[1,0,3,2] row_mask:0xf bank_mask:0xf bound_ctrl:1
	v_cndmask_b32_e64 v48, 0, 1, vcc
	v_cndmask_b32_e64 v16, v16, v79, s[6:7]
	v_add_f32_dpp v22, v22, v22 quad_perm:[2,3,0,1] row_mask:0xf bank_mask:0xf bound_ctrl:1
	v_cndmask_b32_e64 v48, v48, 2, s[6:7]
	v_cmp_ngt_f32_e64 s[8:9], v80, v16
	v_add_f32_dpp v22, v22, v22 row_ror:4 row_mask:0xf bank_mask:0xf bound_ctrl:1
	v_add_f32_dpp v40, v40, v40 row_ror:4 row_mask:0xf bank_mask:0xf bound_ctrl:1
	v_permlane16_swap_b32_e32 v36, v38
	v_add_f32_dpp v22, v22, v22 row_ror:8 row_mask:0xf bank_mask:0xf bound_ctrl:1
	v_mov_b32_e32 v23, v22
	s_nop 1
	v_permlane16_swap_b32_e32 v22, v23
	v_add_f32_e32 v75, v22, v23
	s_nop 0
	v_add_f32_dpp v22, v50, v50 quad_perm:[1,0,3,2] row_mask:0xf bank_mask:0xf bound_ctrl:1
	v_add_f32_dpp v40, v40, v40 row_ror:8 row_mask:0xf bank_mask:0xf bound_ctrl:1
	v_mov_b32_e32 v42, v40
	v_add_f32_dpp v22, v22, v22 quad_perm:[2,3,0,1] row_mask:0xf bank_mask:0xf bound_ctrl:1
	s_nop 0
	v_permlane16_swap_b32_e32 v40, v42
	v_add_f32_dpp v22, v22, v22 row_ror:4 row_mask:0xf bank_mask:0xf bound_ctrl:1
	v_add_f32_e32 v36, v36, v38
	v_add_f32_e32 v40, v40, v42
	v_add_f32_dpp v22, v22, v22 row_ror:8 row_mask:0xf bank_mask:0xf bound_ctrl:1
	v_mov_b32_e32 v23, v22
	s_nop 1
	v_permlane16_swap_b32_e32 v22, v23
	v_add_f32_e32 v77, v22, v23
	s_nop 0
	v_add_f32_dpp v22, v52, v52 quad_perm:[1,0,3,2] row_mask:0xf bank_mask:0xf bound_ctrl:1
	v_cndmask_b32_e64 v62, v80, v16, s[8:9]
	v_mov_b32_e32 v71, v69
	v_add_f32_dpp v22, v22, v22 quad_perm:[2,3,0,1] row_mask:0xf bank_mask:0xf bound_ctrl:1
	v_mov_b32_e32 v74, v73
	v_mov_b32_e32 v76, v75
	v_add_f32_dpp v22, v22, v22 row_ror:4 row_mask:0xf bank_mask:0xf bound_ctrl:1
	v_mov_b32_e32 v78, v77
	v_mov_b32_e32 v38, v36
	v_add_f32_dpp v22, v22, v22 row_ror:8 row_mask:0xf bank_mask:0xf bound_ctrl:1
	v_mov_b32_e32 v23, v22
	s_nop 1
	v_permlane16_swap_b32_e32 v22, v23
	v_add_f32_e32 v50, v22, v23
	s_nop 0
	v_add_f32_dpp v22, v54, v54 quad_perm:[1,0,3,2] row_mask:0xf bank_mask:0xf bound_ctrl:1
	v_mov_b32_e32 v52, v50
	v_mov_b32_e32 v42, v40
	v_add_f32_dpp v22, v22, v22 quad_perm:[2,3,0,1] row_mask:0xf bank_mask:0xf bound_ctrl:1
	v_mov_b32_e32 v46, v44
	s_nop 0
	v_add_f32_dpp v22, v22, v22 row_ror:4 row_mask:0xf bank_mask:0xf bound_ctrl:1
	s_nop 0
	s_nop 0
	v_add_f32_dpp v22, v22, v22 row_ror:8 row_mask:0xf bank_mask:0xf bound_ctrl:1
	v_mov_b32_e32 v23, v22
	s_nop 1
	v_permlane16_swap_b32_e32 v22, v23
	v_add_f32_e32 v54, v22, v23
	s_nop 0
	v_add_f32_dpp v22, v56, v56 quad_perm:[1,0,3,2] row_mask:0xf bank_mask:0xf bound_ctrl:1
	v_mov_b32_e32 v66, v54
	s_nop 0
	v_add_f32_dpp v22, v22, v22 quad_perm:[2,3,0,1] row_mask:0xf bank_mask:0xf bound_ctrl:1
	s_nop 0
	s_nop 0
	v_add_f32_dpp v22, v22, v22 row_ror:4 row_mask:0xf bank_mask:0xf bound_ctrl:1
	s_nop 0
	s_nop 0
	v_add_f32_dpp v22, v22, v22 row_ror:8 row_mask:0xf bank_mask:0xf bound_ctrl:1
	v_mov_b32_e32 v23, v22
	s_nop 1
	v_permlane16_swap_b32_e32 v22, v23
	v_add_f32_e32 v56, v22, v23
	s_nop 0
	v_add_f32_dpp v22, v58, v58 quad_perm:[1,0,3,2] row_mask:0xf bank_mask:0xf bound_ctrl:1
	v_mov_b32_e32 v67, v56
	s_nop 0
	v_add_f32_dpp v22, v22, v22 quad_perm:[2,3,0,1] row_mask:0xf bank_mask:0xf bound_ctrl:1
	s_nop 0
	s_nop 0
	v_add_f32_dpp v22, v22, v22 row_ror:4 row_mask:0xf bank_mask:0xf bound_ctrl:1
	s_nop 0
	s_nop 0
	v_add_f32_dpp v22, v22, v22 row_ror:8 row_mask:0xf bank_mask:0xf bound_ctrl:1
	v_mov_b32_e32 v23, v22
	s_nop 1
	v_permlane16_swap_b32_e32 v22, v23
	v_add_f32_e32 v58, v22, v23
	s_nop 0
	v_add_f32_dpp v22, v60, v60 quad_perm:[1,0,3,2] row_mask:0xf bank_mask:0xf bound_ctrl:1
	v_cndmask_b32_e64 v60, 3, v48, s[8:9]
	v_mov_b32_e32 v48, 0xff800000
	v_cmp_eq_u32_e64 s[10:11], 0, v60
	v_cmp_nlg_f32_e64 s[12:13], v20, v48
	s_or_b64 s[10:11], s[10:11], s[12:13]
	v_cndmask_b32_e64 v20, v20, v48, s[10:11]
	v_cmp_ne_u32_e64 s[12:13], 1, v60
	v_cmp_gt_f32_e64 s[14:15], v21, v20
	s_and_b64 s[12:13], s[12:13], s[14:15]
	v_cndmask_b32_e64 v20, v20, v21, s[12:13]
	v_add_f32_dpp v22, v22, v22 quad_perm:[2,3,0,1] row_mask:0xf bank_mask:0xf bound_ctrl:1
	v_cmp_ne_u32_e64 s[14:15], 2, v60
	v_cmp_gt_f32_e64 s[16:17], v79, v20
	v_add_f32_dpp v22, v22, v22 row_ror:4 row_mask:0xf bank_mask:0xf bound_ctrl:1
	s_and_b64 s[14:15], s[14:15], s[16:17]
	v_cndmask_b32_e64 v20, v20, v79, s[14:15]
	v_add_f32_dpp v22, v22, v22 row_ror:8 row_mask:0xf bank_mask:0xf bound_ctrl:1
	v_mov_b32_e32 v23, v22
	v_cmp_gt_f32_e64 s[16:17], v80, v20
	s_nop 0
	v_permlane16_swap_b32_e32 v22, v23
	s_and_b64 s[16:17], s[8:9], s[16:17]
	v_add_f32_e32 v22, v22, v23
	v_cndmask_b32_e64 v20, v20, v80, s[16:17]
	v_mov_b32_e32 v68, v58
	v_mov_b32_e32 v23, v22
	v_add_f32_e32 v62, v62, v20
	s_nop 0
	s_nop 0
	s_nop 0
	s_nop 0
	v_mov_b32_e32 v16, 1
	v_cmp_lg_f32_e64 s[18:19], v62, v48
	v_mov_b32_e32 v21, 0
	v_mov_b32_e32 v20, 0
	s_and_saveexec_b64 s[38:39], s[18:19]
	s_cbranch_execz .LBB0_911
	v_cndmask_b32_e64 v20, v18, 0, s[10:11]
	v_cndmask_b32_e64 v16, 0, 1, s[12:13]
	v_cndmask_b32_e64 v20, v20, v19, s[12:13]
	v_cndmask_b32_e32 v18, v18, v19, vcc
	v_cndmask_b32_e64 v16, v16, 2, s[14:15]
	v_cndmask_b32_e64 v20, v20, v70, s[14:15]
	v_cndmask_b32_e64 v18, v18, v70, s[6:7]
	v_cndmask_b32_e64 v16, v16, 3, s[16:17]
	v_cndmask_b32_e64 v35, v20, v72, s[16:17]
	v_cndmask_b32_e64 v21, v72, v18, s[8:9]
	v_mov_b32_e32 v20, v60
	v_mov_b32_e32 v48, v62
.LBB0_911:
	s_or_b64 exec, exec, s[38:39]
	v_mov_b32_e32 v18, v69
	v_mov_b32_e32 v19, v73
	v_mul_f32_e32 v18, 0xbfb8aa3b, v18
	v_mul_f32_e32 v19, 0xbfb8aa3b, v19
	v_exp_f32_e32 v18, v18
	v_exp_f32_e32 v19, v19
	v_mov_b32_e32 v60, v75
	v_mul_f32_e32 v60, 0xbfb8aa3b, v60
	v_exp_f32_e32 v60, v60
	v_mov_b32_e32 v62, v77
	v_mul_f32_e32 v62, 0xbfb8aa3b, v62
	v_add_f32_e32 v18, 1.0, v18
	v_add_f32_e32 v19, 1.0, v19
	v_exp_f32_e32 v62, v62
	v_rcp_f32_e32 v18, v18
	v_rcp_f32_e32 v19, v19
	v_add_f32_e32 v60, 1.0, v60
	v_rcp_f32_e32 v60, v60
	v_add_f32_e32 v62, 1.0, v62
	v_rcp_f32_e32 v62, v62
	v_add_f32_e32 v69, v8, v18
	v_add_f32_e32 v70, v9, v19
	v_cmp_gt_f32_e32 vcc, v70, v69
	v_add_f32_e32 v71, v10, v60
	v_add_f32_e32 v72, v11, v62
	v_cndmask_b32_e32 v64, v69, v70, vcc
	v_cmp_gt_f32_e64 s[6:7], v71, v64
	v_cndmask_b32_e64 v73, 0, 1, vcc
	v_cmp_nlg_f32_e64 s[12:13], s89, v69
	v_cndmask_b32_e64 v64, v64, v71, s[6:7]
	v_cndmask_b32_e64 v73, v73, 2, s[6:7]
	v_cmp_ngt_f32_e64 s[8:9], v72, v64
	s_nop 1
	v_cndmask_b32_e64 v74, v72, v64, s[8:9]
	v_cndmask_b32_e64 v64, 3, v73, s[8:9]
	v_cmp_eq_u32_e64 s[10:11], 0, v64
	s_or_b64 s[10:11], s[10:11], s[12:13]
	v_cmp_ne_u32_e64 s[12:13], 1, v64
	v_cndmask_b32_e64 v69, v69, v210, s[10:11]
	v_cmp_gt_f32_e64 s[14:15], v70, v69
	s_and_b64 s[12:13], s[12:13], s[14:15]
	v_cndmask_b32_e64 v69, v69, v70, s[12:13]
	v_cmp_ne_u32_e64 s[14:15], 2, v64
	v_cmp_gt_f32_e64 s[16:17], v71, v69
	s_and_b64 s[14:15], s[14:15], s[16:17]
	v_cndmask_b32_e64 v69, v69, v71, s[14:15]
	v_cmp_gt_f32_e64 s[16:17], v72, v69
	s_and_b64 s[16:17], s[8:9], s[16:17]
	s_nop 0
	v_cndmask_b32_e64 v69, v69, v72, s[16:17]
	v_add_f32_e32 v69, v74, v69
	v_cmp_gt_f32_e64 s[18:19], v69, v48
	s_and_saveexec_b64 s[38:39], s[18:19]
	s_cbranch_execz .LBB0_913
	v_cndmask_b32_e64 v16, 0, 1, s[12:13]
	v_cndmask_b32_e64 v21, v18, 0, s[10:11]
	v_or_b32_e32 v16, 4, v16
	v_cndmask_b32_e64 v21, v21, v19, s[12:13]
	v_cndmask_b32_e32 v18, v18, v19, vcc
	v_cndmask_b32_e64 v16, v16, 6, s[14:15]
	v_cndmask_b32_e64 v21, v21, v60, s[14:15]
	v_cndmask_b32_e64 v18, v18, v60, s[6:7]
	v_cndmask_b32_e64 v16, v16, 7, s[16:17]
	v_or_b32_e32 v20, 4, v64
	v_cndmask_b32_e64 v35, v21, v62, s[16:17]
	v_cndmask_b32_e64 v21, v62, v18, s[8:9]
	v_mov_b32_e32 v48, v69
.LBB0_913:
	s_or_b64 exec, exec, s[38:39]
	v_mov_b32_e32 v18, v50
	v_mov_b32_e32 v19, v54
	v_mul_f32_e32 v18, 0xbfb8aa3b, v18
	v_mul_f32_e32 v19, 0xbfb8aa3b, v19
	v_exp_f32_e32 v18, v18
	v_exp_f32_e32 v19, v19
	v_mov_b32_e32 v50, v56
	v_mul_f32_e32 v50, 0xbfb8aa3b, v50
	v_exp_f32_e32 v50, v50
	v_mov_b32_e32 v52, v58
	v_mul_f32_e32 v52, 0xbfb8aa3b, v52
	v_add_f32_e32 v18, 1.0, v18
	v_add_f32_e32 v19, 1.0, v19
	v_exp_f32_e32 v52, v52
	v_rcp_f32_e32 v18, v18
	v_rcp_f32_e32 v19, v19
	v_add_f32_e32 v50, 1.0, v50
	v_rcp_f32_e32 v50, v50
	v_add_f32_e32 v52, 1.0, v52
	v_rcp_f32_e32 v52, v52
	v_add_f32_e32 v56, v4, v18
	v_add_f32_e32 v58, v5, v19
	v_cmp_gt_f32_e32 vcc, v58, v56
	v_add_f32_e32 v60, v6, v50
	v_add_f32_e32 v62, v7, v52
	v_cndmask_b32_e32 v54, v56, v58, vcc
	v_cmp_gt_f32_e64 s[6:7], v60, v54
	v_cndmask_b32_e64 v64, 0, 1, vcc
	v_cmp_nlg_f32_e64 s[12:13], s89, v56
	v_cndmask_b32_e64 v54, v54, v60, s[6:7]
	v_cndmask_b32_e64 v64, v64, 2, s[6:7]
	v_cmp_ngt_f32_e64 s[8:9], v62, v54
	s_nop 1
	v_cndmask_b32_e64 v66, v62, v54, s[8:9]
	v_cndmask_b32_e64 v54, 3, v64, s[8:9]
	v_cmp_eq_u32_e64 s[10:11], 0, v54
	s_or_b64 s[10:11], s[10:11], s[12:13]
	v_cmp_ne_u32_e64 s[12:13], 1, v54
	v_cndmask_b32_e64 v56, v56, v210, s[10:11]
	v_cmp_gt_f32_e64 s[14:15], v58, v56
	s_and_b64 s[12:13], s[12:13], s[14:15]
	v_cndmask_b32_e64 v56, v56, v58, s[12:13]
	v_cmp_ne_u32_e64 s[14:15], 2, v54
	v_cmp_gt_f32_e64 s[16:17], v60, v56
	s_and_b64 s[14:15], s[14:15], s[16:17]
	v_cndmask_b32_e64 v56, v56, v60, s[14:15]
	v_cmp_gt_f32_e64 s[16:17], v62, v56
	s_and_b64 s[16:17], s[8:9], s[16:17]
	s_nop 0
	v_cndmask_b32_e64 v56, v56, v62, s[16:17]
	v_add_f32_e32 v56, v66, v56
	v_cmp_gt_f32_e64 s[18:19], v56, v48
	s_and_saveexec_b64 s[38:39], s[18:19]
	s_cbranch_execz .LBB0_915
	v_cndmask_b32_e64 v16, 0, 1, s[12:13]
	v_cndmask_b32_e64 v21, v18, 0, s[10:11]
	v_or_b32_e32 v16, 8, v16
	v_cndmask_b32_e64 v21, v21, v19, s[12:13]
	v_cndmask_b32_e32 v18, v18, v19, vcc
	v_cndmask_b32_e64 v16, v16, 10, s[14:15]
	v_cndmask_b32_e64 v21, v21, v50, s[14:15]
	v_cndmask_b32_e64 v18, v18, v50, s[6:7]
	v_cndmask_b32_e64 v16, v16, 11, s[16:17]
	v_or_b32_e32 v20, 8, v54
	v_cndmask_b32_e64 v35, v21, v52, s[16:17]
	v_cndmask_b32_e64 v21, v52, v18, s[8:9]
	v_mov_b32_e32 v48, v56
.LBB0_915:
	s_or_b64 exec, exec, s[38:39]
	v_mov_b32_e32 v18, v22
	v_mov_b32_e32 v19, v36
	v_mul_f32_e32 v18, 0xbfb8aa3b, v18
	v_mul_f32_e32 v19, 0xbfb8aa3b, v19
	v_exp_f32_e32 v18, v18
	v_exp_f32_e32 v19, v19
	v_mov_b32_e32 v22, v40
	v_mul_f32_e32 v22, 0xbfb8aa3b, v22
	v_exp_f32_e32 v22, v22
	v_mov_b32_e32 v23, v44
	v_mul_f32_e32 v23, 0xbfb8aa3b, v23
	v_add_f32_e32 v18, 1.0, v18
	v_add_f32_e32 v19, 1.0, v19
	v_exp_f32_e32 v23, v23
	v_rcp_f32_e32 v18, v18
	v_rcp_f32_e32 v19, v19
	v_add_f32_e32 v22, 1.0, v22
	v_rcp_f32_e32 v22, v22
	v_add_f32_e32 v23, 1.0, v23
	v_rcp_f32_e32 v23, v23
	v_add_f32_e32 v38, v0, v18
	v_add_f32_e32 v40, v1, v19
	v_cmp_gt_f32_e32 vcc, v40, v38
	v_add_f32_e32 v42, v2, v22
	v_add_f32_e32 v44, v3, v23
	v_cndmask_b32_e32 v36, v38, v40, vcc
	v_cmp_gt_f32_e64 s[6:7], v42, v36
	v_cndmask_b32_e64 v46, 0, 1, vcc
	v_cmp_nlg_f32_e64 s[12:13], s89, v38
	v_cndmask_b32_e64 v36, v36, v42, s[6:7]
	v_cndmask_b32_e64 v46, v46, 2, s[6:7]
	v_cmp_ngt_f32_e64 s[8:9], v44, v36
	s_nop 1
	v_cndmask_b32_e64 v50, v44, v36, s[8:9]
	v_cndmask_b32_e64 v36, 3, v46, s[8:9]
	v_cmp_eq_u32_e64 s[10:11], 0, v36
	s_or_b64 s[10:11], s[10:11], s[12:13]
	v_cmp_ne_u32_e64 s[12:13], 1, v36
	v_cndmask_b32_e64 v38, v38, v210, s[10:11]
	v_cmp_gt_f32_e64 s[14:15], v40, v38
	s_and_b64 s[12:13], s[12:13], s[14:15]
	v_cndmask_b32_e64 v38, v38, v40, s[12:13]
	v_cmp_ne_u32_e64 s[14:15], 2, v36
	v_cmp_gt_f32_e64 s[16:17], v42, v38
	s_and_b64 s[14:15], s[14:15], s[16:17]
	v_cndmask_b32_e64 v38, v38, v42, s[14:15]
	v_cmp_gt_f32_e64 s[16:17], v44, v38
	s_and_b64 s[16:17], s[8:9], s[16:17]
	s_nop 0
	v_cndmask_b32_e64 v38, v38, v44, s[16:17]
	v_add_f32_e32 v38, v50, v38
	v_cmp_gt_f32_e64 s[18:19], v38, v48
	s_and_saveexec_b64 s[38:39], s[18:19]
	s_cbranch_execz .LBB0_917
	v_cndmask_b32_e64 v16, 0, 1, s[12:13]
	v_cndmask_b32_e64 v21, v18, 0, s[10:11]
	v_or_b32_e32 v16, 12, v16
	v_cndmask_b32_e64 v21, v21, v19, s[12:13]
	v_cndmask_b32_e32 v18, v18, v19, vcc
	v_cndmask_b32_e64 v16, v16, 14, s[14:15]
	v_cndmask_b32_e64 v21, v21, v22, s[14:15]
	v_cndmask_b32_e64 v18, v18, v22, s[6:7]
	v_cndmask_b32_e64 v16, v16, 15, s[16:17]
	v_or_b32_e32 v20, 12, v36
	v_cndmask_b32_e64 v35, v21, v23, s[16:17]
	v_cndmask_b32_e64 v21, v23, v18, s[8:9]
.LBB0_917:
	s_or_b64 exec, exec, s[38:39]
	s_mov_b64 s[6:7], exec
	s_mov_b32 exec_lo, 1
	s_mov_b32 exec_hi, 1
	s_cbranch_execz .LBB0_919
	v_add_f32_e32 v18, v35, v21
	v_div_scale_f32 v19, s[8:9], v18, v18, 1.0
	v_rcp_f32_e32 v22, v19
	v_div_scale_f32 v23, vcc, 1.0, v18, 1.0
	s_add_i32 s8, s49, s50
	v_fma_f32 v36, -v19, v22, 1.0
	v_fmac_f32_e32 v22, v36, v22
	v_mul_f32_e32 v36, v23, v22
	v_fma_f32 v38, -v19, v36, v23
	v_fmac_f32_e32 v36, v38, v22
	v_fma_f32 v19, -v19, v36, v23
	v_div_fmas_f32 v19, v19, v22, v36
	v_div_fixup_f32 v18, v19, v18, 1.0
	v_lshl_add_u32 v19, v20, 2, s23
	ds_add_rtn_u32 v19, v19, v206
	v_lshl_add_u32 v22, v16, 2, s23
	ds_add_rtn_u32 v22, v22, v206
	v_mbcnt_lo_u32_b32 v23, -1, 0
	v_mul_u32_u24_e32 v23, 6, v23
	v_add_u32_e32 v23, s8, v23
	s_waitcnt lgkmcnt(0)
	ds_write2_b32 v23, v20, v19 offset0:96 offset1:97
	v_mul_f32_e32 v19, v21, v18
	ds_write2_b32 v23, v19, v16 offset0:98 offset1:99
	v_mul_f32_e32 v16, v35, v18
	ds_write2_b32 v23, v22, v16 offset0:100 offset1:101
